# baseline (speedup 1.0000x reference)
.LBB1_9:
	s_or_b64 exec, exec, s[26:27]
	v_lshlrev_b32_e32 v8, 6, v0
	v_lshlrev_b32_e32 v10, 2, v0
	s_add_i32 s26, 0, 0x20000
	v_and_b32_e32 v84, 48, v0
	v_and_b32_e32 v9, 0x3c0, v8
	v_and_b32_e32 v10, 32, v10
	s_add_u32 s42, s12, s24
	v_bitop3_b32 v85, v9, v10, v84 bitop3:0x36
	s_addc_u32 s43, s13, s25
	v_add_u32_e32 v83, 0, v85
	v_and_b32_e32 v9, 0x4000, v8
	s_add_u32 s44, s14, s0
	v_bfe_u32 v1, v0, 6, 1
	v_lshrrev_b32_e32 v87, 7, v0
	s_waitcnt vmcnt(6)
	v_and_b32_e32 v8, 0x2000, v8
	v_add_u32_e32 v9, v83, v9
	v_add_u32_e32 v82, s23, v85
	v_add_u32_e32 v130, v4, v5
	v_lshlrev_b32_e32 v4, 5, v6
	v_lshlrev_b32_e32 v3, 12, v3
	s_mov_b32 s23, 0x70000
	s_addc_u32 s45, s15, s1
	s_add_i32 s48, 0, 0x18000
	s_add_i32 s49, 0, 0x1c000
	v_lshlrev_b32_e32 v7, 13, v1
	v_add_u32_e32 v10, s26, v85
	v_add_u32_e32 v11, 0x18000, v9
	v_add_u32_e32 v92, v9, v8
	v_and_or_b32 v70, v4, s23, v3
	v_mov_b32_e32 v71, v67
	v_lshl_or_b32 v72, v87, 16, v3
	v_mov_b32_e32 v73, v67
	v_add_u32_e32 v98, s26, v2
	v_add_u32_e32 v147, s48, v2
	v_add_u32_e32 v148, s49, v2
	v_mov_b32_e32 v131, v67
	s_mov_b32 s23, -3
	v_add_u32_e32 v97, v83, v7
	s_mov_b64 s[0:1], 0x1000100
	s_mov_b64 s[24:25], 0x100
	s_mov_b64 s[26:27], 0x80100
	v_add_u32_e32 v96, v82, v7
	s_mov_b64 s[28:29], 0x1000180
	s_mov_b64 s[30:31], 0x180
	s_mov_b64 s[34:35], 0x80180
	v_add_u32_e32 v99, v10, v7
	v_add_u32_e32 v100, v11, v8
	s_mov_b64 s[36:37], 0x1000200
	s_mov_b64 s[38:39], 0x200
	s_mov_b64 s[40:41], 0x80200
	v_mov_b32_e32 v2, v67
	v_mov_b32_e32 v3, v67
	v_mov_b32_e32 v4, v67
	v_mov_b32_e32 v5, v67
	v_mov_b32_e32 v6, v67
	v_mov_b32_e32 v7, v67
	v_mov_b32_e32 v8, v67
	v_mov_b32_e32 v9, v67
	v_mov_b32_e32 v10, v67
	v_mov_b32_e32 v11, v67
	v_mov_b32_e32 v12, v67
	v_mov_b32_e32 v13, v67
	v_mov_b32_e32 v14, v67
	v_mov_b32_e32 v15, v67
	v_mov_b32_e32 v16, v67
	v_mov_b32_e32 v17, v67
	v_mov_b32_e32 v18, v67
	v_mov_b32_e32 v19, v67
	v_mov_b32_e32 v20, v67
	v_mov_b32_e32 v21, v67
	v_mov_b32_e32 v22, v67
	v_mov_b32_e32 v23, v67
	v_mov_b32_e32 v24, v67
	v_mov_b32_e32 v25, v67
	v_mov_b32_e32 v26, v67
	v_mov_b32_e32 v27, v67
	v_mov_b32_e32 v28, v67
	v_mov_b32_e32 v29, v67
	v_mov_b32_e32 v30, v67
	v_mov_b32_e32 v31, v67
	v_mov_b32_e32 v32, v67
	v_mov_b32_e32 v33, v67
	v_mov_b32_e32 v34, v67
	v_mov_b32_e32 v35, v67
	v_mov_b32_e32 v36, v67
	v_mov_b32_e32 v37, v67
	v_mov_b32_e32 v38, v67
	v_mov_b32_e32 v39, v67
	v_mov_b32_e32 v40, v67
	v_mov_b32_e32 v41, v67
	v_mov_b32_e32 v42, v67
	v_mov_b32_e32 v43, v67
	v_mov_b32_e32 v44, v67
	v_mov_b32_e32 v45, v67
	v_mov_b32_e32 v46, v67
	v_mov_b32_e32 v47, v67
	v_mov_b32_e32 v48, v67
	v_mov_b32_e32 v49, v67
	v_mov_b32_e32 v50, v67
	v_mov_b32_e32 v51, v67
	v_mov_b32_e32 v52, v67
	v_mov_b32_e32 v53, v67
	v_mov_b32_e32 v54, v67
	v_mov_b32_e32 v55, v67
	v_mov_b32_e32 v56, v67
	v_mov_b32_e32 v57, v67
	v_mov_b32_e32 v58, v67
	v_mov_b32_e32 v59, v67
	v_mov_b32_e32 v60, v67
	v_mov_b32_e32 v61, v67
	v_mov_b32_e32 v62, v67
	v_mov_b32_e32 v63, v67
	v_mov_b32_e32 v64, v67
	v_mov_b32_e32 v65, v67
	v_add_u32_e32 v101, 0x19000, v92
	v_add_u32_e32 v102, 0x19400, v92
	v_add_u32_e32 v103, 0x19800, v92
	v_add_u32_e32 v104, 0x19c00, v92
	v_add_u32_e32 v105, 0x2000, v98
	v_add_u32_e32 v106, 0x2000, v147
	v_add_u32_e32 v107, 0x2000, v148
	v_add_u32_e32 v108, 0x2000, v145
	v_add_u32_e32 v109, 0x2000, v146
	v_lshl_add_u64 v[74:75], s[42:43], 0, v[70:71]
	v_lshl_add_u64 v[76:77], s[42:43], 0, v[72:73]
	v_lshl_add_u64 v[78:79], s[44:45], 0, v[70:71]
	v_lshl_add_u64 v[80:81], s[44:45], 0, v[72:73]
	s_barrier
	s_barrier
	s_nop 1
	v_readfirstlane_b32 s74, v98
	v_readfirstlane_b32 s75, v105
	v_readfirstlane_b32 s76, v147
	v_readfirstlane_b32 s77, v106
	v_readfirstlane_b32 s78, v148
	v_readfirstlane_b32 s79, v107
	v_readfirstlane_b32 s80, v88
	v_readfirstlane_b32 s81, v89
	v_readfirstlane_b32 s82, v144
	v_readfirstlane_b32 s83, v90
	v_readfirstlane_b32 s84, v91
	v_readfirstlane_b32 s85, v93
	v_readfirstlane_b32 s86, v145
	v_readfirstlane_b32 s87, v108
	v_readfirstlane_b32 s88, v94
	v_readfirstlane_b32 s89, v95
	v_readfirstlane_b32 s90, v146
	v_readfirstlane_b32 s91, v109
	v_lshl_add_u64 v[182:183], v[80:81], 0, v[130:131]
	v_lshl_add_u64 v[110:111], v[182:183], 0, s[0:1]
	s_mov_b32 m0, s74
	v_lshl_add_u64 v[184:185], v[78:79], 0, v[130:131]
	global_load_lds_dwordx4 v[110:111], off
	v_lshl_add_u64 v[110:111], v[184:185], 0, s[0:1]
	s_mov_b32 m0, s75
	v_lshl_add_u64 v[186:187], v[76:77], 0, v[130:131]
	global_load_lds_dwordx4 v[110:111], off
	v_lshl_add_u64 v[110:111], v[186:187], 0, s[24:25]
	s_mov_b32 m0, s76
	v_lshl_add_u64 v[188:189], v[74:75], 0, v[130:131]
	global_load_lds_dwordx4 v[110:111], off
	s_mov_b32 m0, s77
	v_lshl_add_u64 v[110:111], v[188:189], 0, s[24:25]
	global_load_lds_dwordx4 v[110:111], off
	s_mov_b32 m0, s78
	v_lshl_add_u64 v[110:111], v[186:187], 0, s[26:27]
	global_load_lds_dwordx4 v[110:111], off
	s_mov_b32 m0, s79
	v_lshl_add_u64 v[110:111], v[188:189], 0, s[26:27]
	global_load_lds_dwordx4 v[110:111], off
	ds_read_b128 v[110:113], v97 offset:32768
	ds_read_b128 v[114:117], v97 offset:33792
	ds_read_b128 v[118:121], v97 offset:34816
	ds_read_b128 v[122:125], v97 offset:35840
	ds_read_b128 v[126:129], v97 offset:36864
	ds_read_b128 v[132:135], v97 offset:37888
	ds_read_b128 v[136:139], v97 offset:38912
	ds_read_b128 v[140:143], v97 offset:39936
	ds_read_b128 v[150:153], v92
	ds_read_b128 v[154:157], v92 offset:1024
	ds_read_b128 v[158:161], v92 offset:2048
	ds_read_b128 v[162:165], v92 offset:3072
	ds_read_b128 v[166:169], v92 offset:4096
	ds_read_b128 v[170:173], v92 offset:5120
	ds_read_b128 v[174:177], v92 offset:6144
	ds_read_b128 v[178:181], v92 offset:7168
	s_waitcnt vmcnt(6)
	s_waitcnt lgkmcnt(0)
	s_barrier
	s_setprio 1
	s_waitcnt lgkmcnt(0)
	v_mfma_f32_16x16x32_f16 v[62:65], v[110:113], v[150:153], v[62:65]
	s_lshl_b32 s60, s66, 16
	s_add_u32 s62, s58, s60
	s_addc_u32 s63, s59, 0
	s_lshl_b32 s61, s66, 15
	s_add_u32 s64, s52, s61
	s_addc_u32 s65, s53, 0
	v_lshlrev_b32_e32 v254, 5, v0
	v_lshlrev_b32_e32 v255, 4, v0
	global_load_dwordx4 v[230:233], v254, s[62:63] nt
	v_mfma_f32_16x16x32_f16 v[58:61], v[118:121], v[150:153], v[58:61]
	global_load_dwordx4 v[234:237], v254, s[62:63] offset:16 nt
	v_mfma_f32_16x16x32_f16 v[54:57], v[126:129], v[150:153], v[54:57]
	s_add_u32 s62, s62, 0x4000
	s_addc_u32 s63, s63, 0
	global_load_dwordx4 v[238:241], v254, s[62:63] nt
	v_mfma_f32_16x16x32_f16 v[50:53], v[136:139], v[150:153], v[50:53]
	global_load_dwordx4 v[242:245], v254, s[62:63] offset:16 nt
	v_mfma_f32_16x16x32_f16 v[46:49], v[110:113], v[158:161], v[46:49]
	s_add_u32 s62, s62, 0x4000
	s_addc_u32 s63, s63, 0
	global_load_dwordx4 v[246:249], v254, s[62:63] nt
	v_mfma_f32_16x16x32_f16 v[42:45], v[118:121], v[158:161], v[42:45]
	global_load_dwordx4 v[250:253], v254, s[62:63] offset:16 nt
	v_mfma_f32_16x16x32_f16 v[38:41], v[126:129], v[158:161], v[38:41]
	s_add_u32 s62, s62, 0x4000
	s_addc_u32 s63, s63, 0
	global_load_dwordx4 v[190:193], v254, s[62:63] nt
	v_mfma_f32_16x16x32_f16 v[34:37], v[136:139], v[158:161], v[34:37]
	global_load_dwordx4 v[194:197], v254, s[62:63] offset:16 nt
	v_mfma_f32_16x16x32_f16 v[30:33], v[110:113], v[166:169], v[30:33]
	v_mfma_f32_16x16x32_f16 v[26:29], v[118:121], v[166:169], v[26:29]
	v_mfma_f32_16x16x32_f16 v[22:25], v[126:129], v[166:169], v[22:25]
	v_mfma_f32_16x16x32_f16 v[18:21], v[136:139], v[166:169], v[18:21]
	v_mfma_f32_16x16x32_f16 v[14:17], v[110:113], v[174:177], v[14:17]
	v_mfma_f32_16x16x32_f16 v[10:13], v[118:121], v[174:177], v[10:13]
	v_mfma_f32_16x16x32_f16 v[6:9], v[126:129], v[174:177], v[6:9]
	v_mfma_f32_16x16x32_f16 v[2:5], v[136:139], v[174:177], v[2:5]
	v_mfma_f32_16x16x32_f16 v[62:65], v[114:117], v[154:157], v[62:65]
	v_mfma_f32_16x16x32_f16 v[58:61], v[122:125], v[154:157], v[58:61]
	v_mfma_f32_16x16x32_f16 v[54:57], v[132:135], v[154:157], v[54:57]
	v_mfma_f32_16x16x32_f16 v[50:53], v[140:143], v[154:157], v[50:53]
	v_mfma_f32_16x16x32_f16 v[46:49], v[114:117], v[162:165], v[46:49]
	v_mfma_f32_16x16x32_f16 v[42:45], v[122:125], v[162:165], v[42:45]
	v_mfma_f32_16x16x32_f16 v[38:41], v[132:135], v[162:165], v[38:41]
	v_mfma_f32_16x16x32_f16 v[34:37], v[140:143], v[162:165], v[34:37]
	v_mfma_f32_16x16x32_f16 v[30:33], v[114:117], v[170:173], v[30:33]
	v_mfma_f32_16x16x32_f16 v[26:29], v[122:125], v[170:173], v[26:29]
	v_mfma_f32_16x16x32_f16 v[22:25], v[132:135], v[170:173], v[22:25]
	v_mfma_f32_16x16x32_f16 v[18:21], v[140:143], v[170:173], v[18:21]
	v_mfma_f32_16x16x32_f16 v[14:17], v[114:117], v[178:181], v[14:17]
	v_mfma_f32_16x16x32_f16 v[10:13], v[122:125], v[178:181], v[10:13]
	v_mfma_f32_16x16x32_f16 v[6:9], v[132:135], v[178:181], v[6:9]
	v_mfma_f32_16x16x32_f16 v[2:5], v[140:143], v[178:181], v[2:5]
	s_setprio 0
	s_barrier
	v_lshl_add_u64 v[150:151], v[182:183], 0, s[28:29]
	s_mov_b32 m0, s80
	ds_read_b128 v[110:113], v92 offset:49152
	ds_read_b128 v[114:117], v92 offset:50176
	ds_read_b128 v[118:121], v92 offset:51200
	ds_read_b128 v[122:125], v92 offset:52224
	ds_read_b128 v[126:129], v92 offset:53248
	ds_read_b128 v[132:135], v92 offset:54272
	ds_read_b128 v[136:139], v92 offset:55296
	ds_read_b128 v[140:143], v92 offset:56320
	global_load_lds_dwordx4 v[150:151], off
	s_mov_b32 m0, s81
	v_lshl_add_u64 v[150:151], v[184:185], 0, s[28:29]
	global_load_lds_dwordx4 v[150:151], off
	s_mov_b32 m0, s82
	v_lshl_add_u64 v[150:151], v[186:187], 0, s[30:31]
	global_load_lds_dwordx4 v[150:151], off
	s_mov_b32 m0, s83
	v_lshl_add_u64 v[150:151], v[188:189], 0, s[30:31]
	global_load_lds_dwordx4 v[150:151], off
	s_mov_b32 m0, s84
	v_lshl_add_u64 v[150:151], v[186:187], 0, s[34:35]
	global_load_lds_dwordx4 v[150:151], off
	s_mov_b32 m0, s85
	v_lshl_add_u64 v[150:151], v[188:189], 0, s[34:35]
	global_load_lds_dwordx4 v[150:151], off
	ds_read_b128 v[150:153], v96
	ds_read_b128 v[154:157], v96 offset:1024
	ds_read_b128 v[158:161], v96 offset:2048
	ds_read_b128 v[162:165], v96 offset:3072
	ds_read_b128 v[166:169], v96 offset:4096
	ds_read_b128 v[170:173], v96 offset:5120
	ds_read_b128 v[174:177], v96 offset:6144
	ds_read_b128 v[178:181], v96 offset:7168
	s_waitcnt vmcnt(14)
	s_waitcnt lgkmcnt(0)
	s_barrier
	s_setprio 1
	s_waitcnt lgkmcnt(0)
	v_mfma_f32_16x16x32_f16 v[62:65], v[150:153], v[110:113], v[62:65]
	v_mfma_f32_16x16x32_f16 v[58:61], v[158:161], v[110:113], v[58:61]
	v_mfma_f32_16x16x32_f16 v[54:57], v[166:169], v[110:113], v[54:57]
	v_mfma_f32_16x16x32_f16 v[50:53], v[174:177], v[110:113], v[50:53]
	v_mfma_f32_16x16x32_f16 v[46:49], v[150:153], v[118:121], v[46:49]
	v_mfma_f32_16x16x32_f16 v[42:45], v[158:161], v[118:121], v[42:45]
	v_mfma_f32_16x16x32_f16 v[38:41], v[166:169], v[118:121], v[38:41]
	v_mfma_f32_16x16x32_f16 v[34:37], v[174:177], v[118:121], v[34:37]
	v_mfma_f32_16x16x32_f16 v[30:33], v[150:153], v[126:129], v[30:33]
	v_mfma_f32_16x16x32_f16 v[26:29], v[158:161], v[126:129], v[26:29]
	v_mfma_f32_16x16x32_f16 v[22:25], v[166:169], v[126:129], v[22:25]
	v_mfma_f32_16x16x32_f16 v[18:21], v[174:177], v[126:129], v[18:21]
	v_mfma_f32_16x16x32_f16 v[14:17], v[150:153], v[136:139], v[14:17]
	v_mfma_f32_16x16x32_f16 v[10:13], v[158:161], v[136:139], v[10:13]
	v_mfma_f32_16x16x32_f16 v[6:9], v[166:169], v[136:139], v[6:9]
	v_mfma_f32_16x16x32_f16 v[2:5], v[174:177], v[136:139], v[2:5]
	v_mfma_f32_16x16x32_f16 v[62:65], v[154:157], v[114:117], v[62:65]
	v_mfma_f32_16x16x32_f16 v[58:61], v[162:165], v[114:117], v[58:61]
	v_mfma_f32_16x16x32_f16 v[54:57], v[170:173], v[114:117], v[54:57]
	v_mfma_f32_16x16x32_f16 v[50:53], v[178:181], v[114:117], v[50:53]
	v_mfma_f32_16x16x32_f16 v[46:49], v[154:157], v[122:125], v[46:49]
	v_mfma_f32_16x16x32_f16 v[42:45], v[162:165], v[122:125], v[42:45]
	v_mfma_f32_16x16x32_f16 v[38:41], v[170:173], v[122:125], v[38:41]
	v_mfma_f32_16x16x32_f16 v[34:37], v[178:181], v[122:125], v[34:37]
	v_mfma_f32_16x16x32_f16 v[30:33], v[154:157], v[132:135], v[30:33]
	v_mfma_f32_16x16x32_f16 v[26:29], v[162:165], v[132:135], v[26:29]
	v_mfma_f32_16x16x32_f16 v[22:25], v[170:173], v[132:135], v[22:25]
	v_mfma_f32_16x16x32_f16 v[18:21], v[178:181], v[132:135], v[18:21]
	v_mfma_f32_16x16x32_f16 v[14:17], v[154:157], v[140:143], v[14:17]
	v_mfma_f32_16x16x32_f16 v[10:13], v[162:165], v[140:143], v[10:13]
	v_mfma_f32_16x16x32_f16 v[6:9], v[170:173], v[140:143], v[6:9]
	v_mfma_f32_16x16x32_f16 v[2:5], v[178:181], v[140:143], v[2:5]
	s_setprio 0
	s_barrier
	v_lshl_add_u64 v[150:151], v[182:183], 0, s[36:37]
	s_mov_b32 m0, s86
	ds_read_b128 v[110:113], v100
	ds_read_b128 v[114:117], v100 offset:1024
	ds_read_b128 v[118:121], v100 offset:2048
	ds_read_b128 v[122:125], v100 offset:3072
	ds_read_b128 v[126:129], v101
	ds_read_b128 v[132:135], v102
	ds_read_b128 v[136:139], v103
	ds_read_b128 v[140:143], v104
	global_load_lds_dwordx4 v[150:151], off
	s_mov_b32 m0, s87
	v_lshl_add_u64 v[150:151], v[184:185], 0, s[36:37]
	global_load_lds_dwordx4 v[150:151], off
	s_mov_b32 m0, s88
	v_lshl_add_u64 v[150:151], v[186:187], 0, s[38:39]
	global_load_lds_dwordx4 v[150:151], off
	s_mov_b32 m0, s89
	v_lshl_add_u64 v[150:151], v[188:189], 0, s[38:39]
	global_load_lds_dwordx4 v[150:151], off
	s_mov_b32 m0, s90
	v_lshl_add_u64 v[150:151], v[186:187], 0, s[40:41]
	global_load_lds_dwordx4 v[150:151], off
	s_mov_b32 m0, s91
	v_lshl_add_u64 v[150:151], v[188:189], 0, s[40:41]
	global_load_lds_dwordx4 v[150:151], off
	ds_read_b128 v[150:153], v99
	ds_read_b128 v[154:157], v99 offset:1024
	ds_read_b128 v[158:161], v99 offset:2048
	ds_read_b128 v[162:165], v99 offset:3072
	ds_read_b128 v[166:169], v99 offset:4096
	ds_read_b128 v[170:173], v99 offset:5120
	ds_read_b128 v[174:177], v99 offset:6144
	ds_read_b128 v[178:181], v99 offset:7168
	s_waitcnt vmcnt(6)
	s_waitcnt lgkmcnt(0)
	s_barrier
	s_setprio 1
	s_waitcnt lgkmcnt(0)
	v_mfma_f32_16x16x32_f16 v[62:65], v[150:153], v[110:113], v[62:65]
	v_cvt_pk_f16_f32 v230, v230, v231
	v_mfma_f32_16x16x32_f16 v[58:61], v[158:161], v[110:113], v[58:61]
	v_cvt_pk_f16_f32 v231, v232, v233
	v_mfma_f32_16x16x32_f16 v[54:57], v[166:169], v[110:113], v[54:57]
	v_cvt_pk_f16_f32 v232, v234, v235
	v_mfma_f32_16x16x32_f16 v[50:53], v[174:177], v[110:113], v[50:53]
	v_cvt_pk_f16_f32 v233, v236, v237
	v_mfma_f32_16x16x32_f16 v[46:49], v[150:153], v[118:121], v[46:49]
	global_store_dwordx4 v255, v[230:233], s[64:65]
	v_mfma_f32_16x16x32_f16 v[42:45], v[158:161], v[118:121], v[42:45]
	s_add_u32 s64, s64, 0x2000
	s_addc_u32 s65, s65, 0
	v_mfma_f32_16x16x32_f16 v[38:41], v[166:169], v[118:121], v[38:41]
	v_cvt_pk_f16_f32 v238, v238, v239
	v_mfma_f32_16x16x32_f16 v[34:37], v[174:177], v[118:121], v[34:37]
	v_cvt_pk_f16_f32 v239, v240, v241
	v_mfma_f32_16x16x32_f16 v[30:33], v[150:153], v[126:129], v[30:33]
	v_cvt_pk_f16_f32 v240, v242, v243
	v_mfma_f32_16x16x32_f16 v[26:29], v[158:161], v[126:129], v[26:29]
	v_cvt_pk_f16_f32 v241, v244, v245
	v_mfma_f32_16x16x32_f16 v[22:25], v[166:169], v[126:129], v[22:25]
	global_store_dwordx4 v255, v[238:241], s[64:65]
	v_mfma_f32_16x16x32_f16 v[18:21], v[174:177], v[126:129], v[18:21]
	s_add_u32 s64, s64, 0x2000
	s_addc_u32 s65, s65, 0
	v_mfma_f32_16x16x32_f16 v[14:17], v[150:153], v[136:139], v[14:17]
	v_cvt_pk_f16_f32 v246, v246, v247
	v_mfma_f32_16x16x32_f16 v[10:13], v[158:161], v[136:139], v[10:13]
	v_cvt_pk_f16_f32 v247, v248, v249
	v_mfma_f32_16x16x32_f16 v[6:9], v[166:169], v[136:139], v[6:9]
	v_cvt_pk_f16_f32 v248, v250, v251
	v_mfma_f32_16x16x32_f16 v[2:5], v[174:177], v[136:139], v[2:5]
	v_cvt_pk_f16_f32 v249, v252, v253
	v_mfma_f32_16x16x32_f16 v[62:65], v[154:157], v[114:117], v[62:65]
	global_store_dwordx4 v255, v[246:249], s[64:65]
	v_mfma_f32_16x16x32_f16 v[58:61], v[162:165], v[114:117], v[58:61]
	s_add_u32 s64, s64, 0x2000
	s_addc_u32 s65, s65, 0
	v_mfma_f32_16x16x32_f16 v[54:57], v[170:173], v[114:117], v[54:57]
	v_cvt_pk_f16_f32 v190, v190, v191
	v_mfma_f32_16x16x32_f16 v[50:53], v[178:181], v[114:117], v[50:53]
	v_cvt_pk_f16_f32 v191, v192, v193
	v_mfma_f32_16x16x32_f16 v[46:49], v[154:157], v[122:125], v[46:49]
	v_cvt_pk_f16_f32 v192, v194, v195
	v_mfma_f32_16x16x32_f16 v[42:45], v[162:165], v[122:125], v[42:45]
	v_cvt_pk_f16_f32 v193, v196, v197
	v_mfma_f32_16x16x32_f16 v[38:41], v[170:173], v[122:125], v[38:41]
	global_store_dwordx4 v255, v[190:193], s[64:65]
	v_mfma_f32_16x16x32_f16 v[34:37], v[178:181], v[122:125], v[34:37]
	v_mfma_f32_16x16x32_f16 v[30:33], v[154:157], v[132:135], v[30:33]
	v_mfma_f32_16x16x32_f16 v[26:29], v[162:165], v[132:135], v[26:29]
	v_mfma_f32_16x16x32_f16 v[22:25], v[170:173], v[132:135], v[22:25]
	v_mfma_f32_16x16x32_f16 v[18:21], v[178:181], v[132:135], v[18:21]
	v_mfma_f32_16x16x32_f16 v[14:17], v[154:157], v[140:143], v[14:17]
	v_mfma_f32_16x16x32_f16 v[10:13], v[162:165], v[140:143], v[10:13]
	v_mfma_f32_16x16x32_f16 v[6:9], v[170:173], v[140:143], v[6:9]
	v_mfma_f32_16x16x32_f16 v[2:5], v[178:181], v[140:143], v[2:5]
	s_setprio 0
	s_barrier
	s_add_i32 s23, s23, 3
	v_lshl_add_u64 v[74:75], v[74:75], 0, s[30:31]
	v_lshl_add_u64 v[76:77], v[76:77], 0, s[30:31]
	v_lshl_add_u64 v[78:79], v[78:79], 0, s[30:31]
	v_lshl_add_u64 v[80:81], v[80:81], 0, s[30:31]
.LBB1_10:
	v_lshl_add_u64 v[182:183], v[80:81], 0, v[130:131]
	v_lshl_add_u64 v[110:111], v[182:183], 0, s[0:1]
	s_mov_b32 m0, s74
	v_lshl_add_u64 v[184:185], v[78:79], 0, v[130:131]
	global_load_lds_dwordx4 v[110:111], off
	v_lshl_add_u64 v[110:111], v[184:185], 0, s[0:1]
	s_mov_b32 m0, s75
	v_lshl_add_u64 v[186:187], v[76:77], 0, v[130:131]
	global_load_lds_dwordx4 v[110:111], off
	v_lshl_add_u64 v[110:111], v[186:187], 0, s[24:25]
	s_mov_b32 m0, s76
	v_lshl_add_u64 v[188:189], v[74:75], 0, v[130:131]
	global_load_lds_dwordx4 v[110:111], off
	s_mov_b32 m0, s77
	v_lshl_add_u64 v[110:111], v[188:189], 0, s[24:25]
	global_load_lds_dwordx4 v[110:111], off
	s_mov_b32 m0, s78
	v_lshl_add_u64 v[110:111], v[186:187], 0, s[26:27]
	global_load_lds_dwordx4 v[110:111], off
	s_mov_b32 m0, s79
	v_lshl_add_u64 v[110:111], v[188:189], 0, s[26:27]
	global_load_lds_dwordx4 v[110:111], off
	ds_read_b128 v[110:113], v97 offset:32768
	ds_read_b128 v[114:117], v97 offset:33792
	ds_read_b128 v[118:121], v97 offset:34816
	ds_read_b128 v[122:125], v97 offset:35840
	ds_read_b128 v[126:129], v97 offset:36864
	ds_read_b128 v[132:135], v97 offset:37888
	ds_read_b128 v[136:139], v97 offset:38912
	ds_read_b128 v[140:143], v97 offset:39936
	ds_read_b128 v[150:153], v92
	ds_read_b128 v[154:157], v92 offset:1024
	ds_read_b128 v[158:161], v92 offset:2048
	ds_read_b128 v[162:165], v92 offset:3072
	ds_read_b128 v[166:169], v92 offset:4096
	ds_read_b128 v[170:173], v92 offset:5120
	ds_read_b128 v[174:177], v92 offset:6144
	ds_read_b128 v[178:181], v92 offset:7168
	s_waitcnt vmcnt(6)
	s_waitcnt lgkmcnt(0)
	s_barrier
	s_setprio 1
	s_waitcnt lgkmcnt(0)
	v_mfma_f32_16x16x32_f16 v[62:65], v[110:113], v[150:153], v[62:65]
	v_mfma_f32_16x16x32_f16 v[58:61], v[118:121], v[150:153], v[58:61]
	v_mfma_f32_16x16x32_f16 v[54:57], v[126:129], v[150:153], v[54:57]
	v_mfma_f32_16x16x32_f16 v[50:53], v[136:139], v[150:153], v[50:53]
	v_mfma_f32_16x16x32_f16 v[46:49], v[110:113], v[158:161], v[46:49]
	v_mfma_f32_16x16x32_f16 v[42:45], v[118:121], v[158:161], v[42:45]
	v_mfma_f32_16x16x32_f16 v[38:41], v[126:129], v[158:161], v[38:41]
	v_mfma_f32_16x16x32_f16 v[34:37], v[136:139], v[158:161], v[34:37]
	v_mfma_f32_16x16x32_f16 v[30:33], v[110:113], v[166:169], v[30:33]
	v_mfma_f32_16x16x32_f16 v[26:29], v[118:121], v[166:169], v[26:29]
	v_mfma_f32_16x16x32_f16 v[22:25], v[126:129], v[166:169], v[22:25]
	v_mfma_f32_16x16x32_f16 v[18:21], v[136:139], v[166:169], v[18:21]
	v_mfma_f32_16x16x32_f16 v[14:17], v[110:113], v[174:177], v[14:17]
	v_mfma_f32_16x16x32_f16 v[10:13], v[118:121], v[174:177], v[10:13]
	v_mfma_f32_16x16x32_f16 v[6:9], v[126:129], v[174:177], v[6:9]
	v_mfma_f32_16x16x32_f16 v[2:5], v[136:139], v[174:177], v[2:5]
	v_mfma_f32_16x16x32_f16 v[62:65], v[114:117], v[154:157], v[62:65]
	v_mfma_f32_16x16x32_f16 v[58:61], v[122:125], v[154:157], v[58:61]
	v_mfma_f32_16x16x32_f16 v[54:57], v[132:135], v[154:157], v[54:57]
	v_mfma_f32_16x16x32_f16 v[50:53], v[140:143], v[154:157], v[50:53]
	v_mfma_f32_16x16x32_f16 v[46:49], v[114:117], v[162:165], v[46:49]
	v_mfma_f32_16x16x32_f16 v[42:45], v[122:125], v[162:165], v[42:45]
	v_mfma_f32_16x16x32_f16 v[38:41], v[132:135], v[162:165], v[38:41]
	v_mfma_f32_16x16x32_f16 v[34:37], v[140:143], v[162:165], v[34:37]
	v_mfma_f32_16x16x32_f16 v[30:33], v[114:117], v[170:173], v[30:33]
	v_mfma_f32_16x16x32_f16 v[26:29], v[122:125], v[170:173], v[26:29]
	v_mfma_f32_16x16x32_f16 v[22:25], v[132:135], v[170:173], v[22:25]
	v_mfma_f32_16x16x32_f16 v[18:21], v[140:143], v[170:173], v[18:21]
	v_mfma_f32_16x16x32_f16 v[14:17], v[114:117], v[178:181], v[14:17]
	v_mfma_f32_16x16x32_f16 v[10:13], v[122:125], v[178:181], v[10:13]
	v_mfma_f32_16x16x32_f16 v[6:9], v[132:135], v[178:181], v[6:9]
	v_mfma_f32_16x16x32_f16 v[2:5], v[140:143], v[178:181], v[2:5]
	s_setprio 0
	s_barrier
	v_lshl_add_u64 v[150:151], v[182:183], 0, s[28:29]
	s_mov_b32 m0, s80
	ds_read_b128 v[110:113], v92 offset:49152
	ds_read_b128 v[114:117], v92 offset:50176
	ds_read_b128 v[118:121], v92 offset:51200
	ds_read_b128 v[122:125], v92 offset:52224
	ds_read_b128 v[126:129], v92 offset:53248
	ds_read_b128 v[132:135], v92 offset:54272
	ds_read_b128 v[136:139], v92 offset:55296
	ds_read_b128 v[140:143], v92 offset:56320
	global_load_lds_dwordx4 v[150:151], off
	s_mov_b32 m0, s81
	v_lshl_add_u64 v[150:151], v[184:185], 0, s[28:29]
	global_load_lds_dwordx4 v[150:151], off
	s_mov_b32 m0, s82
	v_lshl_add_u64 v[150:151], v[186:187], 0, s[30:31]
	global_load_lds_dwordx4 v[150:151], off
	s_mov_b32 m0, s83
	v_lshl_add_u64 v[150:151], v[188:189], 0, s[30:31]
	global_load_lds_dwordx4 v[150:151], off
	s_mov_b32 m0, s84
	v_lshl_add_u64 v[150:151], v[186:187], 0, s[34:35]
	global_load_lds_dwordx4 v[150:151], off
	s_mov_b32 m0, s85
	v_lshl_add_u64 v[150:151], v[188:189], 0, s[34:35]
	global_load_lds_dwordx4 v[150:151], off
	ds_read_b128 v[150:153], v96
	ds_read_b128 v[154:157], v96 offset:1024
	ds_read_b128 v[158:161], v96 offset:2048
	ds_read_b128 v[162:165], v96 offset:3072
	ds_read_b128 v[166:169], v96 offset:4096
	ds_read_b128 v[170:173], v96 offset:5120
	ds_read_b128 v[174:177], v96 offset:6144
	ds_read_b128 v[178:181], v96 offset:7168
	s_waitcnt vmcnt(6)
	s_waitcnt lgkmcnt(0)
	s_barrier
	s_setprio 1
	s_waitcnt lgkmcnt(0)
	v_mfma_f32_16x16x32_f16 v[62:65], v[150:153], v[110:113], v[62:65]
	v_mfma_f32_16x16x32_f16 v[58:61], v[158:161], v[110:113], v[58:61]
	v_mfma_f32_16x16x32_f16 v[54:57], v[166:169], v[110:113], v[54:57]
	v_mfma_f32_16x16x32_f16 v[50:53], v[174:177], v[110:113], v[50:53]
	v_mfma_f32_16x16x32_f16 v[46:49], v[150:153], v[118:121], v[46:49]
	v_mfma_f32_16x16x32_f16 v[42:45], v[158:161], v[118:121], v[42:45]
	v_mfma_f32_16x16x32_f16 v[38:41], v[166:169], v[118:121], v[38:41]
	v_mfma_f32_16x16x32_f16 v[34:37], v[174:177], v[118:121], v[34:37]
	v_mfma_f32_16x16x32_f16 v[30:33], v[150:153], v[126:129], v[30:33]
	v_mfma_f32_16x16x32_f16 v[26:29], v[158:161], v[126:129], v[26:29]
	v_mfma_f32_16x16x32_f16 v[22:25], v[166:169], v[126:129], v[22:25]
	v_mfma_f32_16x16x32_f16 v[18:21], v[174:177], v[126:129], v[18:21]
	v_mfma_f32_16x16x32_f16 v[14:17], v[150:153], v[136:139], v[14:17]
	v_mfma_f32_16x16x32_f16 v[10:13], v[158:161], v[136:139], v[10:13]
	v_mfma_f32_16x16x32_f16 v[6:9], v[166:169], v[136:139], v[6:9]
	v_mfma_f32_16x16x32_f16 v[2:5], v[174:177], v[136:139], v[2:5]
	v_mfma_f32_16x16x32_f16 v[62:65], v[154:157], v[114:117], v[62:65]
	v_mfma_f32_16x16x32_f16 v[58:61], v[162:165], v[114:117], v[58:61]
	v_mfma_f32_16x16x32_f16 v[54:57], v[170:173], v[114:117], v[54:57]
	v_mfma_f32_16x16x32_f16 v[50:53], v[178:181], v[114:117], v[50:53]
	v_mfma_f32_16x16x32_f16 v[46:49], v[154:157], v[122:125], v[46:49]
	v_mfma_f32_16x16x32_f16 v[42:45], v[162:165], v[122:125], v[42:45]
	v_mfma_f32_16x16x32_f16 v[38:41], v[170:173], v[122:125], v[38:41]
	v_mfma_f32_16x16x32_f16 v[34:37], v[178:181], v[122:125], v[34:37]
	v_mfma_f32_16x16x32_f16 v[30:33], v[154:157], v[132:135], v[30:33]
	v_mfma_f32_16x16x32_f16 v[26:29], v[162:165], v[132:135], v[26:29]
	v_mfma_f32_16x16x32_f16 v[22:25], v[170:173], v[132:135], v[22:25]
	v_mfma_f32_16x16x32_f16 v[18:21], v[178:181], v[132:135], v[18:21]
	v_mfma_f32_16x16x32_f16 v[14:17], v[154:157], v[140:143], v[14:17]
	v_mfma_f32_16x16x32_f16 v[10:13], v[162:165], v[140:143], v[10:13]
	v_mfma_f32_16x16x32_f16 v[6:9], v[170:173], v[140:143], v[6:9]
	v_mfma_f32_16x16x32_f16 v[2:5], v[178:181], v[140:143], v[2:5]
	s_setprio 0
	s_barrier
	v_lshl_add_u64 v[150:151], v[182:183], 0, s[36:37]
	s_mov_b32 m0, s86
	ds_read_b128 v[110:113], v100
	ds_read_b128 v[114:117], v100 offset:1024
	ds_read_b128 v[118:121], v100 offset:2048
	ds_read_b128 v[122:125], v100 offset:3072
	ds_read_b128 v[126:129], v101
	ds_read_b128 v[132:135], v102
	ds_read_b128 v[136:139], v103
	ds_read_b128 v[140:143], v104
	global_load_lds_dwordx4 v[150:151], off
	s_mov_b32 m0, s87
	v_lshl_add_u64 v[150:151], v[184:185], 0, s[36:37]
	global_load_lds_dwordx4 v[150:151], off
	s_mov_b32 m0, s88
	v_lshl_add_u64 v[150:151], v[186:187], 0, s[38:39]
	global_load_lds_dwordx4 v[150:151], off
	s_mov_b32 m0, s89
	v_lshl_add_u64 v[150:151], v[188:189], 0, s[38:39]
	global_load_lds_dwordx4 v[150:151], off
	s_mov_b32 m0, s90
	v_lshl_add_u64 v[150:151], v[186:187], 0, s[40:41]
	global_load_lds_dwordx4 v[150:151], off
	s_mov_b32 m0, s91
	v_lshl_add_u64 v[150:151], v[188:189], 0, s[40:41]
	global_load_lds_dwordx4 v[150:151], off
	ds_read_b128 v[150:153], v99
	ds_read_b128 v[154:157], v99 offset:1024
	ds_read_b128 v[158:161], v99 offset:2048
	ds_read_b128 v[162:165], v99 offset:3072
	ds_read_b128 v[166:169], v99 offset:4096
	ds_read_b128 v[170:173], v99 offset:5120
	ds_read_b128 v[174:177], v99 offset:6144
	ds_read_b128 v[178:181], v99 offset:7168
	s_waitcnt vmcnt(6)
	s_waitcnt lgkmcnt(0)
	s_barrier
	s_setprio 1
	s_waitcnt lgkmcnt(0)
	v_mfma_f32_16x16x32_f16 v[62:65], v[150:153], v[110:113], v[62:65]
	v_mfma_f32_16x16x32_f16 v[58:61], v[158:161], v[110:113], v[58:61]
	v_mfma_f32_16x16x32_f16 v[54:57], v[166:169], v[110:113], v[54:57]
	v_mfma_f32_16x16x32_f16 v[50:53], v[174:177], v[110:113], v[50:53]
	v_mfma_f32_16x16x32_f16 v[46:49], v[150:153], v[118:121], v[46:49]
	v_mfma_f32_16x16x32_f16 v[42:45], v[158:161], v[118:121], v[42:45]
	v_mfma_f32_16x16x32_f16 v[38:41], v[166:169], v[118:121], v[38:41]
	v_mfma_f32_16x16x32_f16 v[34:37], v[174:177], v[118:121], v[34:37]
	v_mfma_f32_16x16x32_f16 v[30:33], v[150:153], v[126:129], v[30:33]
	v_mfma_f32_16x16x32_f16 v[26:29], v[158:161], v[126:129], v[26:29]
	v_mfma_f32_16x16x32_f16 v[22:25], v[166:169], v[126:129], v[22:25]
	v_mfma_f32_16x16x32_f16 v[18:21], v[174:177], v[126:129], v[18:21]
	v_mfma_f32_16x16x32_f16 v[14:17], v[150:153], v[136:139], v[14:17]
	v_mfma_f32_16x16x32_f16 v[10:13], v[158:161], v[136:139], v[10:13]
	v_mfma_f32_16x16x32_f16 v[6:9], v[166:169], v[136:139], v[6:9]
	v_mfma_f32_16x16x32_f16 v[2:5], v[174:177], v[136:139], v[2:5]
	v_mfma_f32_16x16x32_f16 v[62:65], v[154:157], v[114:117], v[62:65]
	v_mfma_f32_16x16x32_f16 v[58:61], v[162:165], v[114:117], v[58:61]
	v_mfma_f32_16x16x32_f16 v[54:57], v[170:173], v[114:117], v[54:57]
	v_mfma_f32_16x16x32_f16 v[50:53], v[178:181], v[114:117], v[50:53]
	v_mfma_f32_16x16x32_f16 v[46:49], v[154:157], v[122:125], v[46:49]
	v_mfma_f32_16x16x32_f16 v[42:45], v[162:165], v[122:125], v[42:45]
	v_mfma_f32_16x16x32_f16 v[38:41], v[170:173], v[122:125], v[38:41]
	v_mfma_f32_16x16x32_f16 v[34:37], v[178:181], v[122:125], v[34:37]
	v_mfma_f32_16x16x32_f16 v[30:33], v[154:157], v[132:135], v[30:33]
	v_mfma_f32_16x16x32_f16 v[26:29], v[162:165], v[132:135], v[26:29]
	v_mfma_f32_16x16x32_f16 v[22:25], v[170:173], v[132:135], v[22:25]
	v_mfma_f32_16x16x32_f16 v[18:21], v[178:181], v[132:135], v[18:21]
	v_mfma_f32_16x16x32_f16 v[14:17], v[154:157], v[140:143], v[14:17]
	v_mfma_f32_16x16x32_f16 v[10:13], v[162:165], v[140:143], v[10:13]
	v_mfma_f32_16x16x32_f16 v[6:9], v[170:173], v[140:143], v[6:9]
	v_mfma_f32_16x16x32_f16 v[2:5], v[178:181], v[140:143], v[2:5]
	s_setprio 0
	s_barrier
	s_add_i32 s23, s23, 3
	v_lshl_add_u64 v[74:75], v[74:75], 0, s[30:31]
	v_lshl_add_u64 v[76:77], v[76:77], 0, s[30:31]
	v_lshl_add_u64 v[78:79], v[78:79], 0, s[30:31]
	s_cmp_lt_u32 s23, 27
	v_lshl_add_u64 v[80:81], v[80:81], 0, s[30:31]
	s_cbranch_scc1 .LBB1_10
	ds_read_b128 v[74:77], v97 offset:32768
	ds_read_b128 v[78:81], v97 offset:33792
	ds_read_b128 v[88:91], v97 offset:34816
	ds_read_b128 v[98:101], v97 offset:35840
	ds_read_b128 v[102:105], v97 offset:36864
	ds_read_b128 v[106:109], v97 offset:37888
	ds_read_b128 v[110:113], v97 offset:38912
	ds_read_b128 v[114:117], v97 offset:39936
	ds_read_b128 v[118:121], v92
	ds_read_b128 v[122:125], v92 offset:1024
	ds_read_b128 v[126:129], v92 offset:2048
	ds_read_b128 v[132:135], v92 offset:3072
	ds_read_b128 v[136:139], v92 offset:4096
	ds_read_b128 v[140:143], v92 offset:5120
	ds_read_b128 v[150:153], v92 offset:6144
	ds_read_b128 v[154:157], v92 offset:7168
	s_waitcnt vmcnt(0)
	s_waitcnt lgkmcnt(0)
	s_barrier
	s_setprio 1
	s_waitcnt lgkmcnt(0)
	v_mfma_f32_16x16x32_f16 v[62:65], v[74:77], v[118:121], v[62:65]
	v_mfma_f32_16x16x32_f16 v[58:61], v[88:91], v[118:121], v[58:61]
	v_mfma_f32_16x16x32_f16 v[54:57], v[102:105], v[118:121], v[54:57]
	v_mfma_f32_16x16x32_f16 v[50:53], v[110:113], v[118:121], v[50:53]
	v_mfma_f32_16x16x32_f16 v[46:49], v[74:77], v[126:129], v[46:49]
	v_mfma_f32_16x16x32_f16 v[42:45], v[88:91], v[126:129], v[42:45]
	v_mfma_f32_16x16x32_f16 v[38:41], v[102:105], v[126:129], v[38:41]
	v_mfma_f32_16x16x32_f16 v[34:37], v[110:113], v[126:129], v[34:37]
	v_mfma_f32_16x16x32_f16 v[30:33], v[74:77], v[136:139], v[30:33]
	v_mfma_f32_16x16x32_f16 v[26:29], v[88:91], v[136:139], v[26:29]
	v_mfma_f32_16x16x32_f16 v[22:25], v[102:105], v[136:139], v[22:25]
	v_mfma_f32_16x16x32_f16 v[18:21], v[110:113], v[136:139], v[18:21]
	v_mfma_f32_16x16x32_f16 v[14:17], v[74:77], v[150:153], v[14:17]
	v_mfma_f32_16x16x32_f16 v[10:13], v[88:91], v[150:153], v[10:13]
	v_mfma_f32_16x16x32_f16 v[6:9], v[102:105], v[150:153], v[6:9]
	v_mfma_f32_16x16x32_f16 v[2:5], v[110:113], v[150:153], v[2:5]
	v_mfma_f32_16x16x32_f16 v[62:65], v[78:81], v[122:125], v[62:65]
	v_mfma_f32_16x16x32_f16 v[58:61], v[98:101], v[122:125], v[58:61]
	v_mfma_f32_16x16x32_f16 v[54:57], v[106:109], v[122:125], v[54:57]
	v_mfma_f32_16x16x32_f16 v[50:53], v[114:117], v[122:125], v[50:53]
	v_mfma_f32_16x16x32_f16 v[46:49], v[78:81], v[132:135], v[46:49]
	v_mfma_f32_16x16x32_f16 v[42:45], v[98:101], v[132:135], v[42:45]
	v_mfma_f32_16x16x32_f16 v[38:41], v[106:109], v[132:135], v[38:41]
	v_mfma_f32_16x16x32_f16 v[34:37], v[114:117], v[132:135], v[34:37]
	v_mfma_f32_16x16x32_f16 v[30:33], v[78:81], v[140:143], v[30:33]
	v_mfma_f32_16x16x32_f16 v[26:29], v[98:101], v[140:143], v[26:29]
	v_mfma_f32_16x16x32_f16 v[22:25], v[106:109], v[140:143], v[22:25]
	v_mfma_f32_16x16x32_f16 v[18:21], v[114:117], v[140:143], v[18:21]
	v_mfma_f32_16x16x32_f16 v[14:17], v[78:81], v[154:157], v[14:17]
	v_mfma_f32_16x16x32_f16 v[10:13], v[98:101], v[154:157], v[10:13]
	v_mfma_f32_16x16x32_f16 v[6:9], v[106:109], v[154:157], v[6:9]
	v_mfma_f32_16x16x32_f16 v[2:5], v[114:117], v[154:157], v[2:5]
	s_setprio 0
	s_barrier
	ds_read_b128 v[74:77], v96
	ds_read_b128 v[78:81], v96 offset:1024
	ds_read_b128 v[88:91], v96 offset:2048
	ds_read_b128 v[98:101], v96 offset:3072
	ds_read_b128 v[102:105], v96 offset:4096
	ds_read_b128 v[106:109], v96 offset:5120
	ds_read_b128 v[110:113], v96 offset:6144
	ds_read_b128 v[94:97], v96 offset:7168
	ds_read_b128 v[114:117], v92 offset:49152
	ds_read_b128 v[118:121], v92 offset:50176
	ds_read_b128 v[122:125], v92 offset:51200
	ds_read_b128 v[126:129], v92 offset:52224
	ds_read_b128 v[132:135], v92 offset:53248
	ds_read_b128 v[136:139], v92 offset:54272
	ds_read_b128 v[140:143], v92 offset:55296
	ds_read_b128 v[150:153], v92 offset:56320
	s_waitcnt lgkmcnt(0)
	s_barrier
	s_setprio 1
	s_waitcnt lgkmcnt(0)
	v_mfma_f32_16x16x32_f16 v[62:65], v[74:77], v[114:117], v[62:65]
	v_mfma_f32_16x16x32_f16 v[58:61], v[88:91], v[114:117], v[58:61]
	v_mfma_f32_16x16x32_f16 v[54:57], v[102:105], v[114:117], v[54:57]
	v_mfma_f32_16x16x32_f16 v[50:53], v[110:113], v[114:117], v[50:53]
	v_mfma_f32_16x16x32_f16 v[46:49], v[74:77], v[122:125], v[46:49]
	v_mfma_f32_16x16x32_f16 v[42:45], v[88:91], v[122:125], v[42:45]
	v_mfma_f32_16x16x32_f16 v[38:41], v[102:105], v[122:125], v[38:41]
	v_mfma_f32_16x16x32_f16 v[34:37], v[110:113], v[122:125], v[34:37]
	v_mfma_f32_16x16x32_f16 v[30:33], v[74:77], v[132:135], v[30:33]
	v_mfma_f32_16x16x32_f16 v[26:29], v[88:91], v[132:135], v[26:29]
	v_mfma_f32_16x16x32_f16 v[22:25], v[102:105], v[132:135], v[22:25]
	v_mfma_f32_16x16x32_f16 v[18:21], v[110:113], v[132:135], v[18:21]
	v_mfma_f32_16x16x32_f16 v[14:17], v[74:77], v[140:143], v[14:17]
	v_mfma_f32_16x16x32_f16 v[10:13], v[88:91], v[140:143], v[10:13]
	v_mfma_f32_16x16x32_f16 v[6:9], v[102:105], v[140:143], v[6:9]
	v_mfma_f32_16x16x32_f16 v[2:5], v[110:113], v[140:143], v[2:5]
	v_mfma_f32_16x16x32_f16 v[62:65], v[78:81], v[118:121], v[62:65]
	v_mfma_f32_16x16x32_f16 v[58:61], v[98:101], v[118:121], v[58:61]
	v_mfma_f32_16x16x32_f16 v[54:57], v[106:109], v[118:121], v[54:57]
	v_mfma_f32_16x16x32_f16 v[50:53], v[94:97], v[118:121], v[50:53]
	v_mfma_f32_16x16x32_f16 v[46:49], v[78:81], v[126:129], v[46:49]
	v_mfma_f32_16x16x32_f16 v[42:45], v[98:101], v[126:129], v[42:45]
	v_mfma_f32_16x16x32_f16 v[38:41], v[106:109], v[126:129], v[38:41]
	v_mfma_f32_16x16x32_f16 v[34:37], v[94:97], v[126:129], v[34:37]
	v_mfma_f32_16x16x32_f16 v[30:33], v[78:81], v[136:139], v[30:33]
	v_mfma_f32_16x16x32_f16 v[26:29], v[98:101], v[136:139], v[26:29]
	v_mfma_f32_16x16x32_f16 v[22:25], v[106:109], v[136:139], v[22:25]
	v_mfma_f32_16x16x32_f16 v[18:21], v[94:97], v[136:139], v[18:21]
	v_mfma_f32_16x16x32_f16 v[14:17], v[78:81], v[150:153], v[14:17]
	v_mfma_f32_16x16x32_f16 v[10:13], v[98:101], v[150:153], v[10:13]
	v_mfma_f32_16x16x32_f16 v[6:9], v[106:109], v[150:153], v[6:9]
	v_mfma_f32_16x16x32_f16 v[2:5], v[94:97], v[150:153], v[2:5]
	s_setprio 0
	s_movk_i32 s0, 0x100
	v_cmp_gt_u32_e64 s[0:1], s0, v0
	s_barrier
	s_and_saveexec_b64 s[24:25], s[0:1]
	s_cbranch_execz .LBB1_13
	s_barrier

.LBB1_20:
	ds_read_b128 v[168:171], v165
	ds_read_b128 v[172:175], v165 offset:1024
	ds_read_b128 v[176:179], v165 offset:2048
	ds_read_b128 v[180:183], v165 offset:3072
	v_lshl_add_u64 v[200:201], v[140:141], 0, v[130:131]
	v_lshl_add_u64 v[184:185], v[200:201], 0, s[26:27]
	s_mov_b32 m0, s74
	v_lshl_add_u64 v[206:207], v[142:143], 0, v[130:131]
	global_load_lds_dwordx4 v[184:185], off
	s_mov_b32 m0, s75
	v_lshl_add_u64 v[184:185], v[206:207], 0, s[26:27]
	global_load_lds_dwordx4 v[184:185], off
	ds_read_b128 v[184:187], v152
	ds_read_b128 v[188:191], v152 offset:1024
	ds_read_b128 v[192:195], v151
	ds_read_b128 v[196:199], v151 offset:1024
	ds_read_b128 v[216:219], v150
	ds_read_b128 v[220:223], v150 offset:1024
	ds_read_b128 v[224:227], v149
	ds_read_b128 v[228:231], v149 offset:1024
	s_waitcnt lgkmcnt(8)
	s_barrier
	s_waitcnt lgkmcnt(0)
	s_setprio 1
	s_waitcnt lgkmcnt(0)
	v_mfma_f32_16x16x32_f16 v[126:129], v[168:171], v[184:187], v[126:129]
	v_mfma_f32_16x16x32_f16 v[122:125], v[176:179], v[184:187], v[122:125]
	v_mfma_f32_16x16x32_f16 v[118:121], v[168:171], v[192:195], v[118:121]
	v_mfma_f32_16x16x32_f16 v[114:117], v[176:179], v[192:195], v[114:117]
	v_mfma_f32_16x16x32_f16 v[110:113], v[168:171], v[216:219], v[110:113]
	v_mfma_f32_16x16x32_f16 v[106:109], v[176:179], v[216:219], v[106:109]
	v_mfma_f32_16x16x32_f16 v[102:105], v[168:171], v[224:227], v[102:105]
	v_mfma_f32_16x16x32_f16 v[98:101], v[176:179], v[224:227], v[98:101]
	v_mfma_f32_16x16x32_f16 v[126:129], v[172:175], v[188:191], v[126:129]
	v_mfma_f32_16x16x32_f16 v[122:125], v[180:183], v[188:191], v[122:125]
	v_mfma_f32_16x16x32_f16 v[118:121], v[172:175], v[196:199], v[118:121]
	v_mfma_f32_16x16x32_f16 v[114:117], v[180:183], v[196:199], v[114:117]
	v_mfma_f32_16x16x32_f16 v[110:113], v[172:175], v[220:223], v[110:113]
	v_mfma_f32_16x16x32_f16 v[106:109], v[180:183], v[220:223], v[106:109]
	v_mfma_f32_16x16x32_f16 v[102:105], v[172:175], v[228:231], v[102:105]
	v_mfma_f32_16x16x32_f16 v[98:101], v[180:183], v[228:231], v[98:101]
	s_setprio 0
	s_barrier
	v_lshl_add_u64 v[248:249], v[136:137], 0, v[130:131]
	v_lshl_add_u64 v[250:251], v[248:249], 0, s[28:29]
	s_mov_b32 m0, s76
	ds_read_b128 v[232:235], v161
	ds_read_b128 v[236:239], v161 offset:1024
	ds_read_b128 v[240:243], v161 offset:2048
	ds_read_b128 v[244:247], v161 offset:3072
	global_load_lds_dwordx4 v[250:251], off
	v_lshl_add_u64 v[250:251], v[138:139], 0, v[130:131]
	s_mov_b32 m0, s77
	v_lshl_add_u64 v[252:253], v[250:251], 0, s[28:29]
	global_load_lds_dwordx4 v[252:253], off
	s_barrier
	s_waitcnt lgkmcnt(0)
	s_setprio 1
	s_waitcnt lgkmcnt(0)
	v_mfma_f32_16x16x32_f16 v[94:97], v[232:235], v[184:187], v[94:97]
	v_mfma_f32_16x16x32_f16 v[90:93], v[240:243], v[184:187], v[90:93]
	v_mfma_f32_16x16x32_f16 v[86:89], v[232:235], v[192:195], v[86:89]
	v_mfma_f32_16x16x32_f16 v[82:85], v[240:243], v[192:195], v[82:85]
	v_mfma_f32_16x16x32_f16 v[70:73], v[232:235], v[216:219], v[70:73]
	v_mfma_f32_16x16x32_f16 v[66:69], v[240:243], v[216:219], v[66:69]
	v_mfma_f32_16x16x32_f16 v[62:65], v[232:235], v[224:227], v[62:65]
	v_mfma_f32_16x16x32_f16 v[58:61], v[240:243], v[224:227], v[58:61]
	v_mfma_f32_16x16x32_f16 v[94:97], v[236:239], v[188:191], v[94:97]
	v_mfma_f32_16x16x32_f16 v[90:93], v[244:247], v[188:191], v[90:93]
	v_mfma_f32_16x16x32_f16 v[86:89], v[236:239], v[196:199], v[86:89]
	v_mfma_f32_16x16x32_f16 v[82:85], v[244:247], v[196:199], v[82:85]
	v_mfma_f32_16x16x32_f16 v[70:73], v[236:239], v[220:223], v[70:73]
	v_mfma_f32_16x16x32_f16 v[66:69], v[244:247], v[220:223], v[66:69]
	v_mfma_f32_16x16x32_f16 v[62:65], v[236:239], v[228:231], v[62:65]
	v_mfma_f32_16x16x32_f16 v[58:61], v[244:247], v[228:231], v[58:61]
	s_setprio 0
	v_lshl_add_u64 v[252:253], v[200:201], 0, s[28:29]
	s_mov_b32 m0, s78
	s_barrier
	ds_read_b128 v[184:187], v152 offset:16384
	ds_read_b128 v[188:191], v152 offset:17408
	ds_read_b128 v[192:195], v151 offset:16384
	ds_read_b128 v[196:199], v151 offset:17408
	ds_read_b128 v[216:219], v150 offset:16384
	ds_read_b128 v[220:223], v150 offset:17408
	ds_read_b128 v[224:227], v149 offset:16384
	ds_read_b128 v[228:231], v149 offset:17408
	global_load_lds_dwordx4 v[252:253], off
	s_mov_b32 m0, s79
	v_lshl_add_u64 v[252:253], v[206:207], 0, s[28:29]
	global_load_lds_dwordx4 v[252:253], off
	s_barrier
	s_waitcnt lgkmcnt(0)
	s_setprio 1
	s_waitcnt lgkmcnt(0)
	v_mfma_f32_16x16x32_f16 v[54:57], v[168:171], v[184:187], v[54:57]
	v_mfma_f32_16x16x32_f16 v[50:53], v[176:179], v[184:187], v[50:53]
	v_mfma_f32_16x16x32_f16 v[46:49], v[168:171], v[192:195], v[46:49]
	v_mfma_f32_16x16x32_f16 v[42:45], v[176:179], v[192:195], v[42:45]
	v_mfma_f32_16x16x32_f16 v[38:41], v[168:171], v[216:219], v[38:41]
	v_mfma_f32_16x16x32_f16 v[34:37], v[176:179], v[216:219], v[34:37]
	v_mfma_f32_16x16x32_f16 v[30:33], v[168:171], v[224:227], v[30:33]
	v_mfma_f32_16x16x32_f16 v[26:29], v[176:179], v[224:227], v[26:29]
	v_mfma_f32_16x16x32_f16 v[54:57], v[172:175], v[188:191], v[54:57]
	v_mfma_f32_16x16x32_f16 v[50:53], v[180:183], v[188:191], v[50:53]
	v_mfma_f32_16x16x32_f16 v[46:49], v[172:175], v[196:199], v[46:49]
	v_mfma_f32_16x16x32_f16 v[42:45], v[180:183], v[196:199], v[42:45]
	v_mfma_f32_16x16x32_f16 v[38:41], v[172:175], v[220:223], v[38:41]
	v_mfma_f32_16x16x32_f16 v[34:37], v[180:183], v[220:223], v[34:37]
	v_mfma_f32_16x16x32_f16 v[30:33], v[172:175], v[228:231], v[30:33]
	v_mfma_f32_16x16x32_f16 v[26:29], v[180:183], v[228:231], v[26:29]
	s_setprio 0
	s_barrier
	s_mov_b32 m0, s80
	v_lshl_add_u64 v[168:169], v[248:249], 0, s[30:31]
	global_load_lds_dwordx4 v[168:169], off
	s_mov_b32 m0, s81
	v_lshl_add_u64 v[168:169], v[250:251], 0, s[30:31]
	global_load_lds_dwordx4 v[168:169], off
	s_waitcnt vmcnt(6)
	s_barrier
	s_setprio 1
	v_mfma_f32_16x16x32_f16 v[22:25], v[232:235], v[184:187], v[22:25]
	v_mfma_f32_16x16x32_f16 v[18:21], v[240:243], v[184:187], v[18:21]
	v_mfma_f32_16x16x32_f16 v[14:17], v[232:235], v[192:195], v[14:17]
	v_mfma_f32_16x16x32_f16 v[10:13], v[240:243], v[192:195], v[10:13]
	v_mfma_f32_16x16x32_f16 v[6:9], v[232:235], v[216:219], v[6:9]
	v_mfma_f32_16x16x32_f16 v[2:5], v[240:243], v[216:219], v[2:5]
	v_mfma_f32_16x16x32_f16 v[74:77], v[232:235], v[224:227], v[74:77]
	v_mfma_f32_16x16x32_f16 v[78:81], v[240:243], v[224:227], v[78:81]
	v_mfma_f32_16x16x32_f16 v[22:25], v[236:239], v[188:191], v[22:25]
	v_mfma_f32_16x16x32_f16 v[18:21], v[244:247], v[188:191], v[18:21]
	v_mfma_f32_16x16x32_f16 v[14:17], v[236:239], v[196:199], v[14:17]
	v_mfma_f32_16x16x32_f16 v[10:13], v[244:247], v[196:199], v[10:13]
	v_mfma_f32_16x16x32_f16 v[6:9], v[236:239], v[220:223], v[6:9]
	v_mfma_f32_16x16x32_f16 v[2:5], v[244:247], v[220:223], v[2:5]
	v_mfma_f32_16x16x32_f16 v[74:77], v[236:239], v[228:231], v[74:77]
	v_mfma_f32_16x16x32_f16 v[78:81], v[244:247], v[228:231], v[78:81]
	s_setprio 0
	s_barrier
	ds_read_b128 v[168:171], v155
	ds_read_b128 v[172:175], v155 offset:1024
	ds_read_b128 v[176:179], v155 offset:2048
	ds_read_b128 v[180:183], v155 offset:3072
	v_lshl_add_u64 v[232:233], v[200:201], 0, s[30:31]
	s_mov_b32 m0, s82
	ds_read_b128 v[184:187], v152 offset:32768
	ds_read_b128 v[188:191], v152 offset:33792
	ds_read_b128 v[192:195], v151 offset:32768
	ds_read_b128 v[196:199], v151 offset:33792
	ds_read_b128 v[216:219], v150 offset:32768
	ds_read_b128 v[220:223], v150 offset:33792
	ds_read_b128 v[224:227], v149 offset:32768
	ds_read_b128 v[228:231], v149 offset:33792
	global_load_lds_dwordx4 v[232:233], off
	s_mov_b32 m0, s83
	v_lshl_add_u64 v[232:233], v[206:207], 0, s[30:31]
	global_load_lds_dwordx4 v[232:233], off
	s_waitcnt lgkmcnt(8)
	s_barrier
	s_waitcnt lgkmcnt(0)
	s_setprio 1
	s_waitcnt lgkmcnt(0)
	v_mfma_f32_16x16x32_f16 v[126:129], v[168:171], v[184:187], v[126:129]
	v_mfma_f32_16x16x32_f16 v[122:125], v[176:179], v[184:187], v[122:125]
	v_mfma_f32_16x16x32_f16 v[118:121], v[168:171], v[192:195], v[118:121]
	v_mfma_f32_16x16x32_f16 v[114:117], v[176:179], v[192:195], v[114:117]
	v_mfma_f32_16x16x32_f16 v[110:113], v[168:171], v[216:219], v[110:113]
	v_mfma_f32_16x16x32_f16 v[106:109], v[176:179], v[216:219], v[106:109]
	v_mfma_f32_16x16x32_f16 v[102:105], v[168:171], v[224:227], v[102:105]
	v_mfma_f32_16x16x32_f16 v[98:101], v[176:179], v[224:227], v[98:101]
	v_mfma_f32_16x16x32_f16 v[126:129], v[172:175], v[188:191], v[126:129]
	v_mfma_f32_16x16x32_f16 v[122:125], v[180:183], v[188:191], v[122:125]
	v_mfma_f32_16x16x32_f16 v[118:121], v[172:175], v[196:199], v[118:121]
	v_mfma_f32_16x16x32_f16 v[114:117], v[180:183], v[196:199], v[114:117]
	v_mfma_f32_16x16x32_f16 v[110:113], v[172:175], v[220:223], v[110:113]
	v_mfma_f32_16x16x32_f16 v[106:109], v[180:183], v[220:223], v[106:109]
	v_mfma_f32_16x16x32_f16 v[102:105], v[172:175], v[228:231], v[102:105]
	v_mfma_f32_16x16x32_f16 v[98:101], v[180:183], v[228:231], v[98:101]
	s_setprio 0
	s_barrier
	v_lshl_add_u64 v[252:253], v[248:249], 0, s[34:35]
	s_mov_b32 m0, s84
	ds_read_b128 v[232:235], v153
	ds_read_b128 v[236:239], v153 offset:1024
	ds_read_b128 v[240:243], v153 offset:2048
	ds_read_b128 v[244:247], v153 offset:3072
	global_load_lds_dwordx4 v[252:253], off
	s_mov_b32 m0, s85
	v_lshl_add_u64 v[252:253], v[250:251], 0, s[34:35]
	global_load_lds_dwordx4 v[252:253], off
	s_barrier
	s_waitcnt lgkmcnt(0)
	s_setprio 1
	s_waitcnt lgkmcnt(0)
	v_mfma_f32_16x16x32_f16 v[94:97], v[232:235], v[184:187], v[94:97]
	v_mfma_f32_16x16x32_f16 v[90:93], v[240:243], v[184:187], v[90:93]
	v_mfma_f32_16x16x32_f16 v[86:89], v[232:235], v[192:195], v[86:89]
	v_mfma_f32_16x16x32_f16 v[82:85], v[240:243], v[192:195], v[82:85]
	v_mfma_f32_16x16x32_f16 v[70:73], v[232:235], v[216:219], v[70:73]
	v_mfma_f32_16x16x32_f16 v[66:69], v[240:243], v[216:219], v[66:69]
	v_mfma_f32_16x16x32_f16 v[62:65], v[232:235], v[224:227], v[62:65]
	v_mfma_f32_16x16x32_f16 v[58:61], v[240:243], v[224:227], v[58:61]
	v_mfma_f32_16x16x32_f16 v[94:97], v[236:239], v[188:191], v[94:97]
	v_mfma_f32_16x16x32_f16 v[90:93], v[244:247], v[188:191], v[90:93]
	v_mfma_f32_16x16x32_f16 v[86:89], v[236:239], v[196:199], v[86:89]
	v_mfma_f32_16x16x32_f16 v[82:85], v[244:247], v[196:199], v[82:85]
	v_mfma_f32_16x16x32_f16 v[70:73], v[236:239], v[220:223], v[70:73]
	v_mfma_f32_16x16x32_f16 v[66:69], v[244:247], v[220:223], v[66:69]
	v_mfma_f32_16x16x32_f16 v[62:65], v[236:239], v[228:231], v[62:65]
	v_mfma_f32_16x16x32_f16 v[58:61], v[244:247], v[228:231], v[58:61]
	s_setprio 0
	v_lshl_add_u64 v[200:201], v[200:201], 0, s[34:35]
	s_mov_b32 m0, s86
	s_barrier
	ds_read_b128 v[184:187], v152 offset:49152
	ds_read_b128 v[188:191], v152 offset:50176
	ds_read_b128 v[192:195], v151 offset:49152
	ds_read_b128 v[196:199], v151 offset:50176
	ds_read_b128 v[216:219], v150 offset:49152
	ds_read_b128 v[220:223], v150 offset:50176
	ds_read_b128 v[224:227], v149 offset:49152
	ds_read_b128 v[228:231], v149 offset:50176
	global_load_lds_dwordx4 v[200:201], off
	s_mov_b32 m0, s87
	v_lshl_add_u64 v[200:201], v[206:207], 0, s[34:35]
	global_load_lds_dwordx4 v[200:201], off
	s_barrier
	s_waitcnt lgkmcnt(0)
	s_setprio 1
	s_waitcnt lgkmcnt(0)
	v_mfma_f32_16x16x32_f16 v[54:57], v[168:171], v[184:187], v[54:57]
	v_mfma_f32_16x16x32_f16 v[50:53], v[176:179], v[184:187], v[50:53]
	v_mfma_f32_16x16x32_f16 v[46:49], v[168:171], v[192:195], v[46:49]
	v_mfma_f32_16x16x32_f16 v[42:45], v[176:179], v[192:195], v[42:45]
	v_mfma_f32_16x16x32_f16 v[38:41], v[168:171], v[216:219], v[38:41]
	v_mfma_f32_16x16x32_f16 v[34:37], v[176:179], v[216:219], v[34:37]
	v_mfma_f32_16x16x32_f16 v[30:33], v[168:171], v[224:227], v[30:33]
	v_mfma_f32_16x16x32_f16 v[26:29], v[176:179], v[224:227], v[26:29]
	v_mfma_f32_16x16x32_f16 v[54:57], v[172:175], v[188:191], v[54:57]
	v_mfma_f32_16x16x32_f16 v[50:53], v[180:183], v[188:191], v[50:53]
	v_mfma_f32_16x16x32_f16 v[46:49], v[172:175], v[196:199], v[46:49]
	v_mfma_f32_16x16x32_f16 v[42:45], v[180:183], v[196:199], v[42:45]
	v_mfma_f32_16x16x32_f16 v[38:41], v[172:175], v[220:223], v[38:41]
	v_mfma_f32_16x16x32_f16 v[34:37], v[180:183], v[220:223], v[34:37]
	v_mfma_f32_16x16x32_f16 v[30:33], v[172:175], v[228:231], v[30:33]
	v_mfma_f32_16x16x32_f16 v[26:29], v[180:183], v[228:231], v[26:29]
	s_setprio 0
	s_barrier
	s_mov_b32 m0, s88
	v_lshl_add_u64 v[168:169], v[248:249], 0, s[36:37]
	global_load_lds_dwordx4 v[168:169], off
	s_mov_b32 m0, s89
	v_lshl_add_u64 v[168:169], v[250:251], 0, s[36:37]
	global_load_lds_dwordx4 v[168:169], off
	s_waitcnt vmcnt(6)
	s_barrier
	s_setprio 1
	v_mfma_f32_16x16x32_f16 v[22:25], v[232:235], v[184:187], v[22:25]
	v_mfma_f32_16x16x32_f16 v[18:21], v[240:243], v[184:187], v[18:21]
	v_mfma_f32_16x16x32_f16 v[14:17], v[232:235], v[192:195], v[14:17]
	v_mfma_f32_16x16x32_f16 v[10:13], v[240:243], v[192:195], v[10:13]
	v_mfma_f32_16x16x32_f16 v[6:9], v[232:235], v[216:219], v[6:9]
	v_mfma_f32_16x16x32_f16 v[2:5], v[240:243], v[216:219], v[2:5]
	v_mfma_f32_16x16x32_f16 v[74:77], v[232:235], v[224:227], v[74:77]
	v_mfma_f32_16x16x32_f16 v[78:81], v[240:243], v[224:227], v[78:81]
	v_mfma_f32_16x16x32_f16 v[22:25], v[236:239], v[188:191], v[22:25]
	v_mfma_f32_16x16x32_f16 v[18:21], v[244:247], v[188:191], v[18:21]
	v_mfma_f32_16x16x32_f16 v[14:17], v[236:239], v[196:199], v[14:17]
	v_mfma_f32_16x16x32_f16 v[10:13], v[244:247], v[196:199], v[10:13]
	v_mfma_f32_16x16x32_f16 v[6:9], v[236:239], v[220:223], v[6:9]
	v_mfma_f32_16x16x32_f16 v[2:5], v[244:247], v[220:223], v[2:5]
	v_mfma_f32_16x16x32_f16 v[74:77], v[236:239], v[228:231], v[74:77]
	v_mfma_f32_16x16x32_f16 v[78:81], v[244:247], v[228:231], v[78:81]
	s_setprio 0
	s_add_i32 s21, s21, 2
	v_lshl_add_u64 v[136:137], v[136:137], 0, s[28:29]
	v_lshl_add_u64 v[138:139], v[138:139], 0, s[28:29]
	v_lshl_add_u64 v[140:141], v[140:141], 0, s[28:29]
	s_cmp_lt_u32 s21, 28
	v_lshl_add_u64 v[142:143], v[142:143], 0, s[28:29]
	s_barrier
	s_cbranch_scc1 .LBB1_20
	s_mov_b64 s[26:27], 0xf80
	v_lshl_add_u64 v[130:131], v[132:133], 0, s[26:27]
	v_add_u32_e32 v132, 0xc000, v144
	ds_read_b128 v[136:139], v165
	ds_read_b128 v[140:143], v165 offset:1024
	ds_read_b128 v[156:159], v165 offset:2048
	ds_read_b128 v[162:165], v165 offset:3072
	v_readfirstlane_b32 s21, v132
	v_add_u32_e32 v132, 0xe000, v144
	s_mov_b32 m0, s21
	v_readfirstlane_b32 s21, v132
	global_load_lds_dwordx4 v[130:131], off
	s_mov_b32 m0, s21
	v_lshl_add_u64 v[130:131], v[134:135], 0, s[26:27]
	global_load_lds_dwordx4 v[130:131], off
	ds_read_b128 v[130:133], v152
	ds_read_b128 v[144:147], v152 offset:1024
	ds_read_b128 v[166:169], v151
	ds_read_b128 v[170:173], v151 offset:1024
	ds_read_b128 v[174:177], v150
	ds_read_b128 v[178:181], v150 offset:1024
	ds_read_b128 v[182:185], v149
	ds_read_b128 v[186:189], v149 offset:1024
	s_barrier
	s_waitcnt lgkmcnt(0)
	s_setprio 1
	s_waitcnt lgkmcnt(0)
	v_mfma_f32_16x16x32_f16 v[126:129], v[136:139], v[130:133], v[126:129]
	v_mfma_f32_16x16x32_f16 v[118:121], v[136:139], v[166:169], v[118:121]
	v_mfma_f32_16x16x32_f16 v[110:113], v[136:139], v[174:177], v[110:113]
	v_mfma_f32_16x16x32_f16 v[106:109], v[156:159], v[174:177], v[106:109]
	v_mfma_f32_16x16x32_f16 v[126:129], v[140:143], v[144:147], v[126:129]
	v_mfma_f32_16x16x32_f16 v[122:125], v[156:159], v[130:133], v[122:125]
	v_mfma_f32_16x16x32_f16 v[118:121], v[140:143], v[170:173], v[118:121]
	v_mfma_f32_16x16x32_f16 v[114:117], v[156:159], v[166:169], v[114:117]
	v_mfma_f32_16x16x32_f16 v[110:113], v[140:143], v[178:181], v[110:113]
	v_mfma_f32_16x16x32_f16 v[106:109], v[162:165], v[178:181], v[106:109]
	v_mfma_f32_16x16x32_f16 v[102:105], v[136:139], v[182:185], v[102:105]
	v_mfma_f32_16x16x32_f16 v[98:101], v[156:159], v[182:185], v[98:101]
	v_mfma_f32_16x16x32_f16 v[190:193], v[162:165], v[144:147], v[122:125]
	v_mfma_f32_16x16x32_f16 v[194:197], v[162:165], v[170:173], v[114:117]
	v_mfma_f32_16x16x32_f16 v[198:201], v[140:143], v[186:189], v[102:105]
	v_mfma_f32_16x16x32_f16 v[216:219], v[162:165], v[186:189], v[98:101]
	s_setprio 0
	s_barrier
	s_nop 1
	ds_read_b128 v[98:101], v161
	ds_read_b128 v[102:105], v161 offset:1024
	ds_read_b128 v[114:117], v161 offset:2048
	ds_read_b128 v[122:125], v161 offset:3072
	s_barrier
	s_waitcnt lgkmcnt(0)
	s_setprio 1
	s_waitcnt lgkmcnt(0)
	v_mfma_f32_16x16x32_f16 v[94:97], v[98:101], v[130:133], v[94:97]
	v_mfma_f32_16x16x32_f16 v[90:93], v[114:117], v[130:133], v[90:93]
	v_mfma_f32_16x16x32_f16 v[66:69], v[114:117], v[174:177], v[66:69]
	v_mfma_f32_16x16x32_f16 v[62:65], v[98:101], v[182:185], v[62:65]
	v_mfma_f32_16x16x32_f16 v[94:97], v[102:105], v[144:147], v[94:97]
	v_mfma_f32_16x16x32_f16 v[90:93], v[122:125], v[144:147], v[90:93]
	v_mfma_f32_16x16x32_f16 v[86:89], v[98:101], v[166:169], v[86:89]
	v_mfma_f32_16x16x32_f16 v[82:85], v[114:117], v[166:169], v[82:85]
	v_mfma_f32_16x16x32_f16 v[70:73], v[98:101], v[174:177], v[70:73]
	v_mfma_f32_16x16x32_f16 v[66:69], v[122:125], v[178:181], v[66:69]
	v_mfma_f32_16x16x32_f16 v[62:65], v[102:105], v[186:189], v[62:65]
	v_mfma_f32_16x16x32_f16 v[58:61], v[114:117], v[182:185], v[58:61]
	v_mfma_f32_16x16x32_f16 v[130:133], v[102:105], v[170:173], v[86:89]
	v_mfma_f32_16x16x32_f16 v[144:147], v[122:125], v[170:173], v[82:85]
	v_mfma_f32_16x16x32_f16 v[166:169], v[102:105], v[178:181], v[70:73]
	v_mfma_f32_16x16x32_f16 v[170:173], v[122:125], v[186:189], v[58:61]
	s_setprio 0
	s_barrier
	s_nop 1
	ds_read_b128 v[58:61], v152 offset:16384
	ds_read_b128 v[70:73], v152 offset:17408
	ds_read_b128 v[82:85], v151 offset:16384
	ds_read_b128 v[86:89], v151 offset:17408
	ds_read_b128 v[174:177], v150 offset:16384
	ds_read_b128 v[178:181], v150 offset:17408
	ds_read_b128 v[182:185], v149 offset:16384
	ds_read_b128 v[186:189], v149 offset:17408
	s_waitcnt vmcnt(4)
	s_barrier
	s_waitcnt lgkmcnt(0)
	s_setprio 1
	s_waitcnt lgkmcnt(0)
	v_mfma_f32_16x16x32_f16 v[54:57], v[136:139], v[58:61], v[54:57]
	v_mfma_f32_16x16x32_f16 v[50:53], v[156:159], v[58:61], v[50:53]
	v_mfma_f32_16x16x32_f16 v[46:49], v[136:139], v[82:85], v[46:49]
	v_mfma_f32_16x16x32_f16 v[42:45], v[156:159], v[82:85], v[42:45]
	v_mfma_f32_16x16x32_f16 v[38:41], v[136:139], v[174:177], v[38:41]
	v_mfma_f32_16x16x32_f16 v[26:29], v[156:159], v[182:185], v[26:29]
	v_mfma_f32_16x16x32_f16 v[54:57], v[140:143], v[70:73], v[54:57]
	v_mfma_f32_16x16x32_f16 v[50:53], v[162:165], v[70:73], v[50:53]
	v_mfma_f32_16x16x32_f16 v[46:49], v[140:143], v[86:89], v[46:49]
	v_mfma_f32_16x16x32_f16 v[42:45], v[162:165], v[86:89], v[42:45]
	v_mfma_f32_16x16x32_f16 v[38:41], v[140:143], v[178:181], v[38:41]
	v_mfma_f32_16x16x32_f16 v[34:37], v[156:159], v[174:177], v[34:37]
	v_mfma_f32_16x16x32_f16 v[30:33], v[136:139], v[182:185], v[30:33]
	v_mfma_f32_16x16x32_f16 v[26:29], v[162:165], v[186:189], v[26:29]
	v_mfma_f32_16x16x32_f16 v[220:223], v[162:165], v[178:181], v[34:37]
	v_mfma_f32_16x16x32_f16 v[134:137], v[140:143], v[186:189], v[30:33]
	s_setprio 0
	s_setprio 1
	v_mfma_f32_16x16x32_f16 v[2:5], v[114:117], v[174:177], v[2:5]
	v_mfma_f32_16x16x32_f16 v[22:25], v[98:101], v[58:61], v[22:25]
	v_mfma_f32_16x16x32_f16 v[10:13], v[114:117], v[82:85], v[10:13]
	v_mfma_f32_16x16x32_f16 v[6:9], v[98:101], v[174:177], v[6:9]
	v_mfma_f32_16x16x32_f16 v[160:163], v[122:125], v[178:181], v[2:5]
	v_mfma_f32_16x16x32_f16 v[2:5], v[98:101], v[182:185], v[74:77]
	v_mfma_f32_16x16x32_f16 v[22:25], v[102:105], v[70:73], v[22:25]
	v_mfma_f32_16x16x32_f16 v[18:21], v[114:117], v[58:61], v[18:21]
	v_mfma_f32_16x16x32_f16 v[14:17], v[98:101], v[82:85], v[14:17]
	v_mfma_f32_16x16x32_f16 v[10:13], v[122:125], v[86:89], v[10:13]
	v_mfma_f32_16x16x32_f16 v[6:9], v[102:105], v[178:181], v[6:9]
	v_mfma_f32_16x16x32_f16 v[174:177], v[102:105], v[186:189], v[2:5]
	v_mfma_f32_16x16x32_f16 v[2:5], v[114:117], v[182:185], v[78:81]
	v_mfma_f32_16x16x32_f16 v[138:141], v[122:125], v[70:73], v[18:21]
	v_mfma_f32_16x16x32_f16 v[156:159], v[102:105], v[86:89], v[14:17]
	v_mfma_f32_16x16x32_f16 v[178:181], v[122:125], v[186:189], v[2:5]
	s_setprio 0
	s_barrier
	s_nop 2
	ds_read_b128 v[2:5], v155
	ds_read_b128 v[14:17], v155 offset:1024
	ds_read_b128 v[182:185], v155 offset:2048
	ds_read_b128 v[186:189], v155 offset:3072
	ds_read_b128 v[18:21], v152 offset:32768
	ds_read_b128 v[30:33], v152 offset:33792
	ds_read_b128 v[34:37], v151 offset:32768
	ds_read_b128 v[74:77], v151 offset:33792
	ds_read_b128 v[78:81], v150 offset:32768
	ds_read_b128 v[224:227], v150 offset:33792
	ds_read_b128 v[228:231], v149 offset:32768
	ds_read_b128 v[232:235], v149 offset:33792
	s_waitcnt vmcnt(2)
	s_barrier
	s_waitcnt lgkmcnt(0)
	s_setprio 1
	s_waitcnt lgkmcnt(0)
	v_mfma_f32_16x16x32_f16 v[58:61], v[2:5], v[18:21], v[126:129]
	v_mfma_f32_16x16x32_f16 v[122:125], v[14:17], v[30:33], v[58:61]
	v_mfma_f32_16x16x32_f16 v[58:61], v[182:185], v[18:21], v[190:193]
	v_mfma_f32_16x16x32_f16 v[114:117], v[186:189], v[30:33], v[58:61]
	v_mfma_f32_16x16x32_f16 v[58:61], v[2:5], v[34:37], v[118:121]
	v_mfma_f32_16x16x32_f16 v[102:105], v[14:17], v[74:77], v[58:61]
	v_mfma_f32_16x16x32_f16 v[58:61], v[182:185], v[34:37], v[194:197]
	v_mfma_f32_16x16x32_f16 v[98:101], v[186:189], v[74:77], v[58:61]
	v_mfma_f32_16x16x32_f16 v[58:61], v[2:5], v[78:81], v[110:113]
	v_mfma_f32_16x16x32_f16 v[86:89], v[14:17], v[224:227], v[58:61]
	v_mfma_f32_16x16x32_f16 v[58:61], v[182:185], v[78:81], v[106:109]
	v_mfma_f32_16x16x32_f16 v[82:85], v[186:189], v[224:227], v[58:61]
	v_mfma_f32_16x16x32_f16 v[58:61], v[2:5], v[228:231], v[198:201]
	v_mfma_f32_16x16x32_f16 v[70:73], v[14:17], v[232:235], v[58:61]
	v_mfma_f32_16x16x32_f16 v[58:61], v[182:185], v[228:231], v[216:219]
	v_mfma_f32_16x16x32_f16 v[58:61], v[186:189], v[232:235], v[58:61]
	s_setprio 0
	s_barrier
	ds_read_b128 v[190:193], v153
	ds_read_b128 v[194:197], v153 offset:1024
	ds_read_b128 v[198:201], v153 offset:2048
	ds_read_b128 v[216:219], v153 offset:3072
	s_waitcnt vmcnt(0)
	s_barrier
	s_waitcnt lgkmcnt(0)
	s_setprio 1
	s_waitcnt lgkmcnt(0)
	v_mfma_f32_16x16x32_f16 v[94:97], v[190:193], v[18:21], v[94:97]
	v_mfma_f32_16x16x32_f16 v[18:21], v[198:201], v[18:21], v[90:93]
	v_mfma_f32_16x16x32_f16 v[118:121], v[216:219], v[30:33], v[18:21]
	v_mfma_f32_16x16x32_f16 v[18:21], v[190:193], v[34:37], v[130:133]
	v_mfma_f32_16x16x32_f16 v[110:113], v[194:197], v[74:77], v[18:21]
	v_mfma_f32_16x16x32_f16 v[18:21], v[198:201], v[34:37], v[144:147]
	v_mfma_f32_16x16x32_f16 v[106:109], v[216:219], v[74:77], v[18:21]
	v_mfma_f32_16x16x32_f16 v[18:21], v[190:193], v[78:81], v[166:169]
	v_mfma_f32_16x16x32_f16 v[126:129], v[194:197], v[30:33], v[94:97]
	v_mfma_f32_16x16x32_f16 v[94:97], v[194:197], v[224:227], v[18:21]
	v_mfma_f32_16x16x32_f16 v[18:21], v[198:201], v[78:81], v[66:69]
	v_mfma_f32_16x16x32_f16 v[90:93], v[216:219], v[224:227], v[18:21]
	v_mfma_f32_16x16x32_f16 v[18:21], v[190:193], v[228:231], v[62:65]
	v_mfma_f32_16x16x32_f16 v[78:81], v[194:197], v[232:235], v[18:21]
	v_mfma_f32_16x16x32_f16 v[18:21], v[198:201], v[228:231], v[170:173]
	v_mfma_f32_16x16x32_f16 v[74:77], v[216:219], v[232:235], v[18:21]
	s_setprio 0
	s_barrier
	ds_read_b128 v[130:133], v152 offset:49152
	ds_read_b128 v[142:145], v152 offset:50176
	ds_read_b128 v[152:155], v151 offset:49152
	ds_read_b128 v[164:167], v151 offset:50176
	ds_read_b128 v[168:171], v150 offset:49152
	ds_read_b128 v[224:227], v150 offset:50176
	ds_read_b128 v[228:231], v149 offset:49152
	ds_read_b128 v[146:149], v149 offset:50176
	s_barrier
	s_waitcnt lgkmcnt(0)
	s_setprio 1
	s_waitcnt lgkmcnt(0)
	v_mfma_f32_16x16x32_f16 v[18:21], v[2:5], v[130:133], v[54:57]
	v_mfma_f32_16x16x32_f16 v[66:69], v[14:17], v[142:145], v[18:21]
	v_mfma_f32_16x16x32_f16 v[18:21], v[182:185], v[130:133], v[50:53]
	v_mfma_f32_16x16x32_f16 v[50:53], v[186:189], v[142:145], v[18:21]
	v_mfma_f32_16x16x32_f16 v[18:21], v[2:5], v[152:155], v[46:49]
	v_mfma_f32_16x16x32_f16 v[46:49], v[14:17], v[164:167], v[18:21]
	v_mfma_f32_16x16x32_f16 v[18:21], v[182:185], v[152:155], v[42:45]
	v_mfma_f32_16x16x32_f16 v[34:37], v[186:189], v[164:167], v[18:21]
	v_mfma_f32_16x16x32_f16 v[18:21], v[2:5], v[168:171], v[38:41]
	v_mfma_f32_16x16x32_f16 v[2:5], v[2:5], v[228:231], v[134:137]
	v_mfma_f32_16x16x32_f16 v[30:33], v[14:17], v[224:227], v[18:21]
	v_mfma_f32_16x16x32_f16 v[18:21], v[182:185], v[168:171], v[220:223]
	v_mfma_f32_16x16x32_f16 v[14:17], v[14:17], v[146:149], v[2:5]
	v_mfma_f32_16x16x32_f16 v[2:5], v[182:185], v[228:231], v[26:29]
	v_mfma_f32_16x16x32_f16 v[18:21], v[186:189], v[224:227], v[18:21]
	v_mfma_f32_16x16x32_f16 v[2:5], v[186:189], v[146:149], v[2:5]
	s_setprio 0
	s_setprio 1
	v_mfma_f32_16x16x32_f16 v[22:25], v[190:193], v[130:133], v[22:25]
	v_mfma_f32_16x16x32_f16 v[62:65], v[194:197], v[142:145], v[22:25]
	v_mfma_f32_16x16x32_f16 v[22:25], v[198:201], v[130:133], v[138:141]
	v_mfma_f32_16x16x32_f16 v[6:9], v[190:193], v[168:171], v[6:9]
	v_mfma_f32_16x16x32_f16 v[54:57], v[216:219], v[142:145], v[22:25]
	v_mfma_f32_16x16x32_f16 v[22:25], v[190:193], v[152:155], v[156:159]
	v_mfma_f32_16x16x32_f16 v[26:29], v[194:197], v[224:227], v[6:9]
	v_mfma_f32_16x16x32_f16 v[6:9], v[198:201], v[168:171], v[160:163]
	v_mfma_f32_16x16x32_f16 v[42:45], v[194:197], v[164:167], v[22:25]
	v_mfma_f32_16x16x32_f16 v[10:13], v[198:201], v[152:155], v[10:13]
	v_mfma_f32_16x16x32_f16 v[22:25], v[216:219], v[224:227], v[6:9]
	v_mfma_f32_16x16x32_f16 v[6:9], v[190:193], v[228:231], v[174:177]
	v_mfma_f32_16x16x32_f16 v[38:41], v[216:219], v[164:167], v[10:13]
	v_mfma_f32_16x16x32_f16 v[10:13], v[194:197], v[146:149], v[6:9]
	v_mfma_f32_16x16x32_f16 v[6:9], v[198:201], v[228:231], v[178:181]
	v_mfma_f32_16x16x32_f16 v[6:9], v[216:219], v[146:149], v[6:9]
	s_setprio 0
	s_barrier
	s_and_saveexec_b64 s[26:27], s[0:1]
	s_cbranch_execz .LBB1_23
	s_barrier

.LBB1_67:
	ds_read_b128 v[158:161], v156
	ds_read_b128 v[162:165], v156 offset:1024
	ds_read_b128 v[166:169], v156 offset:2048
	ds_read_b128 v[170:173], v156 offset:3072
	v_add_u32_e32 v157, 0xc000, v218
	v_lshl_add_u64 v[212:213], v[138:139], 0, v[202:203]
	v_readfirstlane_b32 s23, v157
	v_add_u32_e32 v157, 0xe000, v218
	v_lshl_add_u64 v[174:175], v[212:213], 0, s[0:1]
	s_mov_b32 m0, s23
	v_lshl_add_u64 v[250:251], v[140:141], 0, v[202:203]
	v_readfirstlane_b32 s23, v157
	global_load_lds_dwordx4 v[174:175], off
	s_mov_b32 m0, s23
	v_lshl_add_u64 v[174:175], v[250:251], 0, s[0:1]
	global_load_lds_dwordx4 v[174:175], off
	ds_read_b128 v[174:177], v145
	ds_read_b128 v[178:181], v145 offset:1024
	ds_read_b128 v[182:185], v144
	ds_read_b128 v[186:189], v144 offset:1024
	ds_read_b128 v[190:193], v143
	ds_read_b128 v[194:197], v143 offset:1024
	ds_read_b128 v[198:201], v142
	ds_read_b128 v[230:233], v142 offset:1024
	s_waitcnt lgkmcnt(8)
	s_barrier
	s_waitcnt lgkmcnt(0)
	s_setprio 1
	s_waitcnt lgkmcnt(0)
	v_mfma_f32_16x16x32_f16 v[126:129], v[158:161], v[174:177], v[126:129]
	v_mfma_f32_16x16x32_f16 v[122:125], v[166:169], v[174:177], v[122:125]
	v_mfma_f32_16x16x32_f16 v[118:121], v[158:161], v[182:185], v[118:121]
	v_mfma_f32_16x16x32_f16 v[114:117], v[166:169], v[182:185], v[114:117]
	v_mfma_f32_16x16x32_f16 v[110:113], v[158:161], v[190:193], v[110:113]
	v_mfma_f32_16x16x32_f16 v[106:109], v[166:169], v[190:193], v[106:109]
	v_mfma_f32_16x16x32_f16 v[102:105], v[158:161], v[198:201], v[102:105]
	v_mfma_f32_16x16x32_f16 v[98:101], v[166:169], v[198:201], v[98:101]
	v_mfma_f32_16x16x32_f16 v[126:129], v[162:165], v[178:181], v[126:129]
	v_mfma_f32_16x16x32_f16 v[122:125], v[170:173], v[178:181], v[122:125]
	v_mfma_f32_16x16x32_f16 v[118:121], v[162:165], v[186:189], v[118:121]
	v_mfma_f32_16x16x32_f16 v[114:117], v[170:173], v[186:189], v[114:117]
	v_mfma_f32_16x16x32_f16 v[110:113], v[162:165], v[194:197], v[110:113]
	v_mfma_f32_16x16x32_f16 v[106:109], v[170:173], v[194:197], v[106:109]
	v_mfma_f32_16x16x32_f16 v[102:105], v[162:165], v[230:233], v[102:105]
	v_mfma_f32_16x16x32_f16 v[98:101], v[170:173], v[230:233], v[98:101]
	s_setprio 0
	s_barrier
	v_lshl_add_u64 v[252:253], v[134:135], 0, v[202:203]
	v_lshl_add_u64 v[254:255], v[252:253], 0, s[26:27]
	s_mov_b32 m0, s74
	v_add_u32_e32 v157, 0x2000, v216
	ds_read_b128 v[234:237], v155
	ds_read_b128 v[238:241], v155 offset:1024
	ds_read_b128 v[242:245], v155 offset:2048
	ds_read_b128 v[246:249], v155 offset:3072
	global_load_lds_dwordx4 v[254:255], off
	v_lshl_add_u64 v[254:255], v[136:137], 0, v[202:203]
	v_readfirstlane_b32 s23, v157
	s_mov_b32 m0, s23
	v_lshl_add_u64 v[228:229], v[254:255], 0, s[26:27]
	global_load_lds_dwordx4 v[228:229], off
	s_barrier
	s_waitcnt lgkmcnt(0)
	s_setprio 1
	s_waitcnt lgkmcnt(0)
	v_mfma_f32_16x16x32_f16 v[94:97], v[234:237], v[174:177], v[94:97]
	v_mfma_f32_16x16x32_f16 v[90:93], v[242:245], v[174:177], v[90:93]
	v_mfma_f32_16x16x32_f16 v[86:89], v[234:237], v[182:185], v[86:89]
	v_mfma_f32_16x16x32_f16 v[82:85], v[242:245], v[182:185], v[82:85]
	v_mfma_f32_16x16x32_f16 v[74:77], v[234:237], v[190:193], v[74:77]
	v_mfma_f32_16x16x32_f16 v[66:69], v[242:245], v[190:193], v[66:69]
	v_mfma_f32_16x16x32_f16 v[62:65], v[234:237], v[198:201], v[62:65]
	v_mfma_f32_16x16x32_f16 v[58:61], v[242:245], v[198:201], v[58:61]
	v_mfma_f32_16x16x32_f16 v[94:97], v[238:241], v[178:181], v[94:97]
	v_mfma_f32_16x16x32_f16 v[90:93], v[246:249], v[178:181], v[90:93]
	v_mfma_f32_16x16x32_f16 v[86:89], v[238:241], v[186:189], v[86:89]
	v_mfma_f32_16x16x32_f16 v[82:85], v[246:249], v[186:189], v[82:85]
	v_mfma_f32_16x16x32_f16 v[74:77], v[238:241], v[194:197], v[74:77]
	v_mfma_f32_16x16x32_f16 v[66:69], v[246:249], v[194:197], v[66:69]
	v_mfma_f32_16x16x32_f16 v[62:65], v[238:241], v[230:233], v[62:65]
	v_mfma_f32_16x16x32_f16 v[58:61], v[246:249], v[230:233], v[58:61]
	s_setprio 0
	v_lshl_add_u64 v[228:229], v[212:213], 0, s[26:27]
	s_mov_b32 m0, s75
	s_barrier
	ds_read_b128 v[174:177], v145 offset:16384
	ds_read_b128 v[178:181], v145 offset:17408
	ds_read_b128 v[182:185], v144 offset:16384
	ds_read_b128 v[186:189], v144 offset:17408
	ds_read_b128 v[190:193], v143 offset:16384
	ds_read_b128 v[194:197], v143 offset:17408
	ds_read_b128 v[198:201], v142 offset:16384
	ds_read_b128 v[230:233], v142 offset:17408
	global_load_lds_dwordx4 v[228:229], off
	s_mov_b32 m0, s76
	v_lshl_add_u64 v[228:229], v[250:251], 0, s[26:27]
	global_load_lds_dwordx4 v[228:229], off
	s_barrier
	s_waitcnt lgkmcnt(0)
	s_setprio 1
	s_waitcnt lgkmcnt(0)
	v_mfma_f32_16x16x32_f16 v[54:57], v[158:161], v[174:177], v[54:57]
	v_mfma_f32_16x16x32_f16 v[50:53], v[166:169], v[174:177], v[50:53]
	v_mfma_f32_16x16x32_f16 v[46:49], v[158:161], v[182:185], v[46:49]
	v_mfma_f32_16x16x32_f16 v[42:45], v[166:169], v[182:185], v[42:45]
	v_mfma_f32_16x16x32_f16 v[38:41], v[158:161], v[190:193], v[38:41]
	v_mfma_f32_16x16x32_f16 v[34:37], v[166:169], v[190:193], v[34:37]
	v_mfma_f32_16x16x32_f16 v[30:33], v[158:161], v[198:201], v[30:33]
	v_mfma_f32_16x16x32_f16 v[26:29], v[166:169], v[198:201], v[26:29]
	v_mfma_f32_16x16x32_f16 v[54:57], v[162:165], v[178:181], v[54:57]
	v_mfma_f32_16x16x32_f16 v[50:53], v[170:173], v[178:181], v[50:53]
	v_mfma_f32_16x16x32_f16 v[46:49], v[162:165], v[186:189], v[46:49]
	v_mfma_f32_16x16x32_f16 v[42:45], v[170:173], v[186:189], v[42:45]
	v_mfma_f32_16x16x32_f16 v[38:41], v[162:165], v[194:197], v[38:41]
	v_mfma_f32_16x16x32_f16 v[34:37], v[170:173], v[194:197], v[34:37]
	v_mfma_f32_16x16x32_f16 v[30:33], v[162:165], v[230:233], v[30:33]
	v_mfma_f32_16x16x32_f16 v[26:29], v[170:173], v[230:233], v[26:29]
	s_setprio 0
	s_barrier
	v_add_u32_e32 v157, 0x2000, v219
	v_lshl_add_u64 v[158:159], v[252:253], 0, s[28:29]
	s_mov_b32 m0, s77
	v_readfirstlane_b32 s23, v157
	global_load_lds_dwordx4 v[158:159], off
	s_mov_b32 m0, s23
	v_lshl_add_u64 v[158:159], v[254:255], 0, s[28:29]
	global_load_lds_dwordx4 v[158:159], off
	s_waitcnt vmcnt(6)
	s_barrier
	s_setprio 1
	v_mfma_f32_16x16x32_f16 v[22:25], v[234:237], v[174:177], v[22:25]
	v_mfma_f32_16x16x32_f16 v[18:21], v[242:245], v[174:177], v[18:21]
	v_mfma_f32_16x16x32_f16 v[14:17], v[234:237], v[182:185], v[14:17]
	v_mfma_f32_16x16x32_f16 v[10:13], v[242:245], v[182:185], v[10:13]
	v_mfma_f32_16x16x32_f16 v[6:9], v[234:237], v[190:193], v[6:9]
	v_mfma_f32_16x16x32_f16 v[2:5], v[242:245], v[190:193], v[2:5]
	v_mfma_f32_16x16x32_f16 v[70:73], v[234:237], v[198:201], v[70:73]
	v_mfma_f32_16x16x32_f16 v[78:81], v[242:245], v[198:201], v[78:81]
	v_mfma_f32_16x16x32_f16 v[22:25], v[238:241], v[178:181], v[22:25]
	v_mfma_f32_16x16x32_f16 v[18:21], v[246:249], v[178:181], v[18:21]
	v_mfma_f32_16x16x32_f16 v[14:17], v[238:241], v[186:189], v[14:17]
	v_mfma_f32_16x16x32_f16 v[10:13], v[246:249], v[186:189], v[10:13]
	v_mfma_f32_16x16x32_f16 v[6:9], v[238:241], v[194:197], v[6:9]
	v_mfma_f32_16x16x32_f16 v[2:5], v[246:249], v[194:197], v[2:5]
	v_mfma_f32_16x16x32_f16 v[70:73], v[238:241], v[230:233], v[70:73]
	v_mfma_f32_16x16x32_f16 v[78:81], v[246:249], v[230:233], v[78:81]
	s_setprio 0
	s_barrier
	ds_read_b128 v[158:161], v148
	ds_read_b128 v[162:165], v148 offset:1024
	ds_read_b128 v[166:169], v148 offset:2048
	ds_read_b128 v[170:173], v148 offset:3072
	v_lshl_add_u64 v[228:229], v[212:213], 0, s[28:29]
	s_mov_b32 m0, s78
	ds_read_b128 v[174:177], v145 offset:32768
	ds_read_b128 v[178:181], v145 offset:33792
	ds_read_b128 v[182:185], v144 offset:32768
	ds_read_b128 v[186:189], v144 offset:33792
	ds_read_b128 v[190:193], v143 offset:32768
	ds_read_b128 v[194:197], v143 offset:33792
	ds_read_b128 v[198:201], v142 offset:32768
	ds_read_b128 v[230:233], v142 offset:33792
	global_load_lds_dwordx4 v[228:229], off
	s_mov_b32 m0, s79
	v_lshl_add_u64 v[228:229], v[250:251], 0, s[28:29]
	global_load_lds_dwordx4 v[228:229], off
	s_waitcnt lgkmcnt(8)
	s_barrier
	s_waitcnt lgkmcnt(0)
	s_setprio 1
	s_waitcnt lgkmcnt(0)
	v_mfma_f32_16x16x32_f16 v[126:129], v[158:161], v[174:177], v[126:129]
	v_mfma_f32_16x16x32_f16 v[122:125], v[166:169], v[174:177], v[122:125]
	v_mfma_f32_16x16x32_f16 v[118:121], v[158:161], v[182:185], v[118:121]
	v_mfma_f32_16x16x32_f16 v[114:117], v[166:169], v[182:185], v[114:117]
	v_mfma_f32_16x16x32_f16 v[110:113], v[158:161], v[190:193], v[110:113]
	v_mfma_f32_16x16x32_f16 v[106:109], v[166:169], v[190:193], v[106:109]
	v_mfma_f32_16x16x32_f16 v[102:105], v[158:161], v[198:201], v[102:105]
	v_mfma_f32_16x16x32_f16 v[98:101], v[166:169], v[198:201], v[98:101]
	v_mfma_f32_16x16x32_f16 v[126:129], v[162:165], v[178:181], v[126:129]
	v_mfma_f32_16x16x32_f16 v[122:125], v[170:173], v[178:181], v[122:125]
	v_mfma_f32_16x16x32_f16 v[118:121], v[162:165], v[186:189], v[118:121]
	v_mfma_f32_16x16x32_f16 v[114:117], v[170:173], v[186:189], v[114:117]
	v_mfma_f32_16x16x32_f16 v[110:113], v[162:165], v[194:197], v[110:113]
	v_mfma_f32_16x16x32_f16 v[106:109], v[170:173], v[194:197], v[106:109]
	v_mfma_f32_16x16x32_f16 v[102:105], v[162:165], v[230:233], v[102:105]
	v_mfma_f32_16x16x32_f16 v[98:101], v[170:173], v[230:233], v[98:101]
	s_setprio 0
	s_barrier
	v_lshl_add_u64 v[228:229], v[252:253], 0, s[30:31]
	s_mov_b32 m0, s80
	ds_read_b128 v[234:237], v146
	ds_read_b128 v[238:241], v146 offset:1024
	ds_read_b128 v[242:245], v146 offset:2048
	ds_read_b128 v[246:249], v146 offset:3072
	global_load_lds_dwordx4 v[228:229], off
	s_mov_b32 m0, s81
	v_lshl_add_u64 v[228:229], v[254:255], 0, s[30:31]
	global_load_lds_dwordx4 v[228:229], off
	s_barrier
	s_waitcnt lgkmcnt(0)
	s_setprio 1
	s_waitcnt lgkmcnt(0)
	v_mfma_f32_16x16x32_f16 v[94:97], v[234:237], v[174:177], v[94:97]
	v_mfma_f32_16x16x32_f16 v[90:93], v[242:245], v[174:177], v[90:93]
	v_mfma_f32_16x16x32_f16 v[86:89], v[234:237], v[182:185], v[86:89]
	v_mfma_f32_16x16x32_f16 v[82:85], v[242:245], v[182:185], v[82:85]
	v_mfma_f32_16x16x32_f16 v[74:77], v[234:237], v[190:193], v[74:77]
	v_mfma_f32_16x16x32_f16 v[66:69], v[242:245], v[190:193], v[66:69]
	v_mfma_f32_16x16x32_f16 v[62:65], v[234:237], v[198:201], v[62:65]
	v_mfma_f32_16x16x32_f16 v[58:61], v[242:245], v[198:201], v[58:61]
	v_mfma_f32_16x16x32_f16 v[94:97], v[238:241], v[178:181], v[94:97]
	v_mfma_f32_16x16x32_f16 v[90:93], v[246:249], v[178:181], v[90:93]
	v_mfma_f32_16x16x32_f16 v[86:89], v[238:241], v[186:189], v[86:89]
	v_mfma_f32_16x16x32_f16 v[82:85], v[246:249], v[186:189], v[82:85]
	v_mfma_f32_16x16x32_f16 v[74:77], v[238:241], v[194:197], v[74:77]
	v_mfma_f32_16x16x32_f16 v[66:69], v[246:249], v[194:197], v[66:69]
	v_mfma_f32_16x16x32_f16 v[62:65], v[238:241], v[230:233], v[62:65]
	v_mfma_f32_16x16x32_f16 v[58:61], v[246:249], v[230:233], v[58:61]
	s_setprio 0
	v_lshl_add_u64 v[212:213], v[212:213], 0, s[30:31]
	s_mov_b32 m0, s82
	s_barrier
	ds_read_b128 v[174:177], v145 offset:49152
	ds_read_b128 v[178:181], v145 offset:50176
	ds_read_b128 v[182:185], v144 offset:49152
	ds_read_b128 v[186:189], v144 offset:50176
	ds_read_b128 v[190:193], v143 offset:49152
	ds_read_b128 v[194:197], v143 offset:50176
	ds_read_b128 v[198:201], v142 offset:49152
	ds_read_b128 v[230:233], v142 offset:50176
	global_load_lds_dwordx4 v[212:213], off
	s_mov_b32 m0, s83
	v_lshl_add_u64 v[212:213], v[250:251], 0, s[30:31]
	global_load_lds_dwordx4 v[212:213], off
	s_barrier
	s_waitcnt lgkmcnt(0)
	s_setprio 1
	s_waitcnt lgkmcnt(0)
	v_mfma_f32_16x16x32_f16 v[54:57], v[158:161], v[174:177], v[54:57]
	v_mfma_f32_16x16x32_f16 v[50:53], v[166:169], v[174:177], v[50:53]
	v_mfma_f32_16x16x32_f16 v[46:49], v[158:161], v[182:185], v[46:49]
	v_mfma_f32_16x16x32_f16 v[42:45], v[166:169], v[182:185], v[42:45]
	v_mfma_f32_16x16x32_f16 v[38:41], v[158:161], v[190:193], v[38:41]
	v_mfma_f32_16x16x32_f16 v[34:37], v[166:169], v[190:193], v[34:37]
	v_mfma_f32_16x16x32_f16 v[30:33], v[158:161], v[198:201], v[30:33]
	v_mfma_f32_16x16x32_f16 v[26:29], v[166:169], v[198:201], v[26:29]
	v_mfma_f32_16x16x32_f16 v[54:57], v[162:165], v[178:181], v[54:57]
	v_mfma_f32_16x16x32_f16 v[50:53], v[170:173], v[178:181], v[50:53]
	v_mfma_f32_16x16x32_f16 v[46:49], v[162:165], v[186:189], v[46:49]
	v_mfma_f32_16x16x32_f16 v[42:45], v[170:173], v[186:189], v[42:45]
	v_mfma_f32_16x16x32_f16 v[38:41], v[162:165], v[194:197], v[38:41]
	v_mfma_f32_16x16x32_f16 v[34:37], v[170:173], v[194:197], v[34:37]
	v_mfma_f32_16x16x32_f16 v[30:33], v[162:165], v[230:233], v[30:33]
	v_mfma_f32_16x16x32_f16 v[26:29], v[170:173], v[230:233], v[26:29]
	s_setprio 0
	s_barrier
	s_mov_b32 m0, s84
	v_lshl_add_u64 v[158:159], v[252:253], 0, s[34:35]
	global_load_lds_dwordx4 v[158:159], off
	s_mov_b32 m0, s85
	v_lshl_add_u64 v[158:159], v[254:255], 0, s[34:35]
	global_load_lds_dwordx4 v[158:159], off
	s_waitcnt vmcnt(6)
	s_barrier
	s_setprio 1
	v_mfma_f32_16x16x32_f16 v[22:25], v[234:237], v[174:177], v[22:25]
	v_mfma_f32_16x16x32_f16 v[18:21], v[242:245], v[174:177], v[18:21]
	v_mfma_f32_16x16x32_f16 v[14:17], v[234:237], v[182:185], v[14:17]
	v_mfma_f32_16x16x32_f16 v[10:13], v[242:245], v[182:185], v[10:13]
	v_mfma_f32_16x16x32_f16 v[6:9], v[234:237], v[190:193], v[6:9]
	v_mfma_f32_16x16x32_f16 v[2:5], v[242:245], v[190:193], v[2:5]
	v_mfma_f32_16x16x32_f16 v[70:73], v[234:237], v[198:201], v[70:73]
	v_mfma_f32_16x16x32_f16 v[78:81], v[242:245], v[198:201], v[78:81]
	v_mfma_f32_16x16x32_f16 v[22:25], v[238:241], v[178:181], v[22:25]
	v_mfma_f32_16x16x32_f16 v[18:21], v[246:249], v[178:181], v[18:21]
	v_mfma_f32_16x16x32_f16 v[14:17], v[238:241], v[186:189], v[14:17]
	v_mfma_f32_16x16x32_f16 v[10:13], v[246:249], v[186:189], v[10:13]
	v_mfma_f32_16x16x32_f16 v[6:9], v[238:241], v[194:197], v[6:9]
	v_mfma_f32_16x16x32_f16 v[2:5], v[246:249], v[194:197], v[2:5]
	v_mfma_f32_16x16x32_f16 v[70:73], v[238:241], v[230:233], v[70:73]
	v_mfma_f32_16x16x32_f16 v[78:81], v[246:249], v[230:233], v[78:81]
	s_setprio 0
	s_add_i32 s3, s3, 2
	v_lshl_add_u64 v[134:135], v[134:135], 0, s[26:27]
	v_lshl_add_u64 v[136:137], v[136:137], 0, s[26:27]
	v_lshl_add_u64 v[138:139], v[138:139], 0, s[26:27]
	s_cmp_lt_u32 s3, 28
	v_lshl_add_u64 v[140:141], v[140:141], 0, s[26:27]
	s_barrier
	s_cbranch_scc1 .LBB1_67
	v_add_u32_e32 v147, 0xc000, v218
	s_mov_b64 s[0:1], 0xf80
	v_readfirstlane_b32 s3, v147
	v_lshl_add_u64 v[130:131], v[130:131], 0, s[0:1]
	s_mov_b32 m0, s3
	ds_read_b128 v[134:137], v156
	ds_read_b128 v[138:141], v156 offset:1024
	ds_read_b128 v[150:153], v156 offset:2048
	ds_read_b128 v[156:159], v156 offset:3072
	global_load_lds_dwordx4 v[130:131], off
	v_lshl_add_u64 v[130:131], v[132:133], 0, s[0:1]
	v_add_u32_e32 v132, 0xe000, v218
	s_nop 0
	v_readfirstlane_b32 s0, v132
	s_mov_b32 m0, s0
	s_nop 0
	global_load_lds_dwordx4 v[130:131], off
	ds_read_b128 v[130:133], v145
	ds_read_b128 v[160:163], v145 offset:1024
	ds_read_b128 v[164:167], v144
	ds_read_b128 v[168:171], v144 offset:1024
	ds_read_b128 v[172:175], v143
	ds_read_b128 v[176:179], v143 offset:1024
	ds_read_b128 v[180:183], v142
	ds_read_b128 v[184:187], v142 offset:1024
	s_barrier
	s_waitcnt lgkmcnt(0)
	s_setprio 1
	s_waitcnt lgkmcnt(0)
	v_mfma_f32_16x16x32_f16 v[126:129], v[134:137], v[130:133], v[126:129]
	v_mfma_f32_16x16x32_f16 v[118:121], v[134:137], v[164:167], v[118:121]
	v_mfma_f32_16x16x32_f16 v[110:113], v[134:137], v[172:175], v[110:113]
	v_mfma_f32_16x16x32_f16 v[106:109], v[150:153], v[172:175], v[106:109]
	v_mfma_f32_16x16x32_f16 v[126:129], v[138:141], v[160:163], v[126:129]
	v_mfma_f32_16x16x32_f16 v[122:125], v[150:153], v[130:133], v[122:125]
	v_mfma_f32_16x16x32_f16 v[118:121], v[138:141], v[168:171], v[118:121]
	v_mfma_f32_16x16x32_f16 v[114:117], v[150:153], v[164:167], v[114:117]
	v_mfma_f32_16x16x32_f16 v[110:113], v[138:141], v[176:179], v[110:113]
	v_mfma_f32_16x16x32_f16 v[106:109], v[156:159], v[176:179], v[106:109]
	v_mfma_f32_16x16x32_f16 v[102:105], v[134:137], v[180:183], v[102:105]
	v_mfma_f32_16x16x32_f16 v[98:101], v[150:153], v[180:183], v[98:101]
	v_mfma_f32_16x16x32_f16 v[188:191], v[156:159], v[160:163], v[122:125]
	v_mfma_f32_16x16x32_f16 v[192:195], v[156:159], v[168:171], v[114:117]
	v_mfma_f32_16x16x32_f16 v[196:199], v[138:141], v[184:187], v[102:105]
	v_mfma_f32_16x16x32_f16 v[230:233], v[156:159], v[184:187], v[98:101]
	s_setprio 0
	s_barrier
	s_nop 1
	ds_read_b128 v[98:101], v155
	ds_read_b128 v[102:105], v155 offset:1024
	ds_read_b128 v[114:117], v155 offset:2048
	ds_read_b128 v[122:125], v155 offset:3072
	s_barrier
	s_waitcnt lgkmcnt(0)
	s_setprio 1
	s_waitcnt lgkmcnt(0)
	v_mfma_f32_16x16x32_f16 v[94:97], v[98:101], v[130:133], v[94:97]
	v_mfma_f32_16x16x32_f16 v[90:93], v[114:117], v[130:133], v[90:93]
	v_mfma_f32_16x16x32_f16 v[74:77], v[98:101], v[172:175], v[74:77]
	v_mfma_f32_16x16x32_f16 v[66:69], v[114:117], v[172:175], v[66:69]
	v_mfma_f32_16x16x32_f16 v[62:65], v[98:101], v[180:183], v[62:65]
	v_mfma_f32_16x16x32_f16 v[94:97], v[102:105], v[160:163], v[94:97]
	v_mfma_f32_16x16x32_f16 v[90:93], v[122:125], v[160:163], v[90:93]
	v_mfma_f32_16x16x32_f16 v[86:89], v[98:101], v[164:167], v[86:89]
	v_mfma_f32_16x16x32_f16 v[82:85], v[114:117], v[164:167], v[82:85]
	v_mfma_f32_16x16x32_f16 v[74:77], v[102:105], v[176:179], v[74:77]
	v_mfma_f32_16x16x32_f16 v[66:69], v[122:125], v[176:179], v[66:69]
	v_mfma_f32_16x16x32_f16 v[62:65], v[102:105], v[184:187], v[62:65]
	v_mfma_f32_16x16x32_f16 v[58:61], v[114:117], v[180:183], v[58:61]
	v_mfma_f32_16x16x32_f16 v[130:133], v[102:105], v[168:171], v[86:89]
	v_mfma_f32_16x16x32_f16 v[160:163], v[122:125], v[168:171], v[82:85]
	v_mfma_f32_16x16x32_f16 v[164:167], v[122:125], v[184:187], v[58:61]
	s_setprio 0
	s_barrier
	s_nop 2
	ds_read_b128 v[58:61], v145 offset:16384
	ds_read_b128 v[82:85], v145 offset:17408
	ds_read_b128 v[86:89], v144 offset:16384
	ds_read_b128 v[168:171], v144 offset:17408
	ds_read_b128 v[172:175], v143 offset:16384
	ds_read_b128 v[176:179], v143 offset:17408
	ds_read_b128 v[180:183], v142 offset:16384
	ds_read_b128 v[184:187], v142 offset:17408
	s_waitcnt vmcnt(4)
	s_barrier
	s_waitcnt lgkmcnt(0)
	s_setprio 1
	s_waitcnt lgkmcnt(0)
	v_mfma_f32_16x16x32_f16 v[54:57], v[134:137], v[58:61], v[54:57]
	v_mfma_f32_16x16x32_f16 v[50:53], v[150:153], v[58:61], v[50:53]
	v_mfma_f32_16x16x32_f16 v[46:49], v[134:137], v[86:89], v[46:49]
	v_mfma_f32_16x16x32_f16 v[42:45], v[150:153], v[86:89], v[42:45]
	v_mfma_f32_16x16x32_f16 v[38:41], v[134:137], v[172:175], v[38:41]
	v_mfma_f32_16x16x32_f16 v[26:29], v[150:153], v[180:183], v[26:29]
	v_mfma_f32_16x16x32_f16 v[54:57], v[138:141], v[82:85], v[54:57]
	v_mfma_f32_16x16x32_f16 v[50:53], v[156:159], v[82:85], v[50:53]
	v_mfma_f32_16x16x32_f16 v[46:49], v[138:141], v[168:171], v[46:49]
	v_mfma_f32_16x16x32_f16 v[42:45], v[156:159], v[168:171], v[42:45]
	v_mfma_f32_16x16x32_f16 v[38:41], v[138:141], v[176:179], v[38:41]
	v_mfma_f32_16x16x32_f16 v[34:37], v[150:153], v[172:175], v[34:37]
	v_mfma_f32_16x16x32_f16 v[30:33], v[134:137], v[180:183], v[30:33]
	v_mfma_f32_16x16x32_f16 v[26:29], v[156:159], v[184:187], v[26:29]
	v_mfma_f32_16x16x32_f16 v[234:237], v[156:159], v[176:179], v[34:37]
	v_mfma_f32_16x16x32_f16 v[134:137], v[138:141], v[184:187], v[30:33]
	s_setprio 0
	s_setprio 1
	v_mfma_f32_16x16x32_f16 v[2:5], v[114:117], v[172:175], v[2:5]
	v_mfma_f32_16x16x32_f16 v[22:25], v[98:101], v[58:61], v[22:25]
	v_mfma_f32_16x16x32_f16 v[14:17], v[98:101], v[86:89], v[14:17]
	v_mfma_f32_16x16x32_f16 v[10:13], v[114:117], v[86:89], v[10:13]
	v_mfma_f32_16x16x32_f16 v[6:9], v[98:101], v[172:175], v[6:9]
	v_mfma_f32_16x16x32_f16 v[154:157], v[122:125], v[176:179], v[2:5]
	v_mfma_f32_16x16x32_f16 v[2:5], v[98:101], v[180:183], v[70:73]
	v_mfma_f32_16x16x32_f16 v[22:25], v[102:105], v[82:85], v[22:25]
	v_mfma_f32_16x16x32_f16 v[18:21], v[114:117], v[58:61], v[18:21]
	v_mfma_f32_16x16x32_f16 v[150:153], v[102:105], v[168:171], v[14:17]
	v_mfma_f32_16x16x32_f16 v[10:13], v[122:125], v[168:171], v[10:13]
	v_mfma_f32_16x16x32_f16 v[6:9], v[102:105], v[176:179], v[6:9]
	v_mfma_f32_16x16x32_f16 v[168:171], v[102:105], v[184:187], v[2:5]
	v_mfma_f32_16x16x32_f16 v[2:5], v[114:117], v[180:183], v[78:81]
	v_mfma_f32_16x16x32_f16 v[138:141], v[122:125], v[82:85], v[18:21]
	v_mfma_f32_16x16x32_f16 v[172:175], v[122:125], v[184:187], v[2:5]
	s_setprio 0
	s_barrier
	s_nop 3
	ds_read_b128 v[2:5], v148
	ds_read_b128 v[14:17], v148 offset:1024
	ds_read_b128 v[176:179], v148 offset:2048
	ds_read_b128 v[180:183], v148 offset:3072
	ds_read_b128 v[18:21], v145 offset:32768
	ds_read_b128 v[30:33], v145 offset:33792
	ds_read_b128 v[34:37], v144 offset:32768
	ds_read_b128 v[78:81], v144 offset:33792
	ds_read_b128 v[184:187], v143 offset:32768
	ds_read_b128 v[238:241], v143 offset:33792
	ds_read_b128 v[242:245], v142 offset:32768
	ds_read_b128 v[246:249], v142 offset:33792
	s_waitcnt vmcnt(2)
	s_barrier
	s_waitcnt lgkmcnt(0)
	s_setprio 1
	s_waitcnt lgkmcnt(0)
	v_mfma_f32_16x16x32_f16 v[58:61], v[2:5], v[18:21], v[126:129]
	v_mfma_f32_16x16x32_f16 v[122:125], v[14:17], v[30:33], v[58:61]
	v_mfma_f32_16x16x32_f16 v[58:61], v[176:179], v[18:21], v[188:191]
	v_mfma_f32_16x16x32_f16 v[114:117], v[180:183], v[30:33], v[58:61]
	v_mfma_f32_16x16x32_f16 v[58:61], v[2:5], v[34:37], v[118:121]
	v_mfma_f32_16x16x32_f16 v[102:105], v[14:17], v[78:81], v[58:61]
	v_mfma_f32_16x16x32_f16 v[58:61], v[176:179], v[34:37], v[192:195]
	v_mfma_f32_16x16x32_f16 v[98:101], v[180:183], v[78:81], v[58:61]
	v_mfma_f32_16x16x32_f16 v[58:61], v[2:5], v[184:187], v[110:113]
	v_mfma_f32_16x16x32_f16 v[86:89], v[14:17], v[238:241], v[58:61]
	v_mfma_f32_16x16x32_f16 v[58:61], v[176:179], v[184:187], v[106:109]
	v_mfma_f32_16x16x32_f16 v[82:85], v[180:183], v[238:241], v[58:61]
	v_mfma_f32_16x16x32_f16 v[58:61], v[2:5], v[242:245], v[196:199]
	v_mfma_f32_16x16x32_f16 v[70:73], v[14:17], v[246:249], v[58:61]
	v_mfma_f32_16x16x32_f16 v[58:61], v[176:179], v[242:245], v[230:233]
	v_mfma_f32_16x16x32_f16 v[58:61], v[180:183], v[246:249], v[58:61]
	s_setprio 0
	s_barrier
	ds_read_b128 v[188:191], v146
	ds_read_b128 v[192:195], v146 offset:1024
	ds_read_b128 v[196:199], v146 offset:2048
	ds_read_b128 v[146:149], v146 offset:3072
	s_waitcnt vmcnt(0)
	s_barrier
	s_waitcnt lgkmcnt(0)
	s_setprio 1
	s_waitcnt lgkmcnt(0)
	v_mfma_f32_16x16x32_f16 v[94:97], v[188:191], v[18:21], v[94:97]
	v_mfma_f32_16x16x32_f16 v[18:21], v[196:199], v[18:21], v[90:93]
	v_mfma_f32_16x16x32_f16 v[118:121], v[146:149], v[30:33], v[18:21]
	v_mfma_f32_16x16x32_f16 v[18:21], v[188:191], v[34:37], v[130:133]
	v_mfma_f32_16x16x32_f16 v[110:113], v[192:195], v[78:81], v[18:21]
	v_mfma_f32_16x16x32_f16 v[18:21], v[196:199], v[34:37], v[160:163]
	v_mfma_f32_16x16x32_f16 v[106:109], v[146:149], v[78:81], v[18:21]
	v_mfma_f32_16x16x32_f16 v[18:21], v[188:191], v[184:187], v[74:77]
	v_mfma_f32_16x16x32_f16 v[126:129], v[192:195], v[30:33], v[94:97]
	v_mfma_f32_16x16x32_f16 v[94:97], v[192:195], v[238:241], v[18:21]
	v_mfma_f32_16x16x32_f16 v[18:21], v[196:199], v[184:187], v[66:69]
	v_mfma_f32_16x16x32_f16 v[90:93], v[146:149], v[238:241], v[18:21]
	v_mfma_f32_16x16x32_f16 v[18:21], v[188:191], v[242:245], v[62:65]
	v_mfma_f32_16x16x32_f16 v[78:81], v[192:195], v[246:249], v[18:21]
	v_mfma_f32_16x16x32_f16 v[18:21], v[196:199], v[242:245], v[164:167]
	v_mfma_f32_16x16x32_f16 v[74:77], v[146:149], v[246:249], v[18:21]
	s_setprio 0
	s_barrier
	ds_read_b128 v[130:133], v145 offset:49152
	ds_read_b128 v[158:161], v145 offset:50176
	ds_read_b128 v[162:165], v144 offset:49152
	ds_read_b128 v[184:187], v144 offset:50176
	ds_read_b128 v[230:233], v143 offset:49152
	ds_read_b128 v[238:241], v143 offset:50176
	ds_read_b128 v[242:245], v142 offset:49152
	ds_read_b128 v[142:145], v142 offset:50176
	s_barrier
	s_waitcnt lgkmcnt(0)
	s_setprio 1
	s_waitcnt lgkmcnt(0)
	v_mfma_f32_16x16x32_f16 v[18:21], v[2:5], v[130:133], v[54:57]
	v_mfma_f32_16x16x32_f16 v[66:69], v[14:17], v[158:161], v[18:21]
	v_mfma_f32_16x16x32_f16 v[18:21], v[176:179], v[130:133], v[50:53]
	v_mfma_f32_16x16x32_f16 v[50:53], v[180:183], v[158:161], v[18:21]
	v_mfma_f32_16x16x32_f16 v[18:21], v[2:5], v[162:165], v[46:49]
	v_mfma_f32_16x16x32_f16 v[46:49], v[14:17], v[184:187], v[18:21]
	v_mfma_f32_16x16x32_f16 v[18:21], v[176:179], v[162:165], v[42:45]
	v_mfma_f32_16x16x32_f16 v[34:37], v[180:183], v[184:187], v[18:21]
	v_mfma_f32_16x16x32_f16 v[18:21], v[2:5], v[230:233], v[38:41]
	v_mfma_f32_16x16x32_f16 v[2:5], v[2:5], v[242:245], v[134:137]
	v_mfma_f32_16x16x32_f16 v[30:33], v[14:17], v[238:241], v[18:21]
	v_mfma_f32_16x16x32_f16 v[18:21], v[176:179], v[230:233], v[234:237]
	v_mfma_f32_16x16x32_f16 v[14:17], v[14:17], v[142:145], v[2:5]
	v_mfma_f32_16x16x32_f16 v[2:5], v[176:179], v[242:245], v[26:29]
	v_mfma_f32_16x16x32_f16 v[18:21], v[180:183], v[238:241], v[18:21]
	v_mfma_f32_16x16x32_f16 v[2:5], v[180:183], v[142:145], v[2:5]
	s_setprio 0
	s_setprio 1
	v_mfma_f32_16x16x32_f16 v[22:25], v[188:191], v[130:133], v[22:25]
	v_mfma_f32_16x16x32_f16 v[62:65], v[192:195], v[158:161], v[22:25]
	v_mfma_f32_16x16x32_f16 v[22:25], v[196:199], v[130:133], v[138:141]
	v_mfma_f32_16x16x32_f16 v[6:9], v[188:191], v[230:233], v[6:9]
	v_mfma_f32_16x16x32_f16 v[54:57], v[146:149], v[158:161], v[22:25]
	v_mfma_f32_16x16x32_f16 v[22:25], v[188:191], v[162:165], v[150:153]
	v_mfma_f32_16x16x32_f16 v[26:29], v[192:195], v[238:241], v[6:9]
	v_mfma_f32_16x16x32_f16 v[6:9], v[196:199], v[230:233], v[154:157]
	v_mfma_f32_16x16x32_f16 v[42:45], v[192:195], v[184:187], v[22:25]
	v_mfma_f32_16x16x32_f16 v[10:13], v[196:199], v[162:165], v[10:13]
	v_mfma_f32_16x16x32_f16 v[22:25], v[146:149], v[238:241], v[6:9]
	v_mfma_f32_16x16x32_f16 v[6:9], v[188:191], v[242:245], v[168:171]
	v_mfma_f32_16x16x32_f16 v[38:41], v[146:149], v[184:187], v[10:13]
	v_mfma_f32_16x16x32_f16 v[10:13], v[192:195], v[142:145], v[6:9]
	v_mfma_f32_16x16x32_f16 v[6:9], v[196:199], v[242:245], v[172:175]
	v_mfma_f32_16x16x32_f16 v[6:9], v[146:149], v[142:145], v[6:9]
	s_setprio 0
	s_movk_i32 s0, 0x100
	v_cmp_gt_u32_e64 s[0:1], s0, v0
	s_barrier
	s_and_saveexec_b64 s[26:27], s[0:1]
	s_cbranch_execz .LBB1_70
	s_barrier

.LBB1_112:
	s_or_b64 exec, exec, s[8:9]
	s_add_i32 s8, 0, 0x20000
	v_lshlrev_b32_e32 v4, 6, v0
	s_add_u32 s6, s12, s6
	v_and_b32_e32 v4, 0x4000, v4
	v_lshlrev_b32_e32 v5, 13, v217
	s_addc_u32 s7, s13, s7
	v_bfe_u32 v74, v0, 6, 1
	s_waitcnt vmcnt(6)
	v_and_b32_e32 v5, 0x2000, v5
	v_add3_u32 v4, 0, v4, v225
	s_add_u32 s4, s14, s4
	v_lshlrev_b32_e32 v3, 13, v74
	v_add_u32_e32 v6, s8, v225
	v_add_u32_e32 v7, 0x18000, v4
	v_add_u32_e32 v78, v4, v5
	s_addc_u32 s5, s15, s5
	v_add_u32_e32 v91, s8, v222
	v_add_u32_e32 v86, 0x19000, v78
	v_add_u32_e32 v87, 0x19400, v78
	v_add_u32_e32 v88, 0x19800, v78
	v_add_u32_e32 v89, 0x19c00, v78
	v_lshl_add_u64 v[66:67], s[6:7], 0, v[210:211]
	v_lshl_add_u64 v[68:69], s[6:7], 0, v[208:209]
	v_lshl_add_u64 v[70:71], s[4:5], 0, v[210:211]
	v_lshl_add_u64 v[72:73], s[4:5], 0, v[208:209]
	s_mov_b32 s3, -3
	v_add_u32_e32 v90, v224, v3
	s_mov_b64 s[4:5], 0x1000100
	v_add_u32_e32 v92, 0x2000, v91
	s_mov_b64 s[6:7], 0x100
	v_add_u32_e32 v93, 0x2000, v220
	s_mov_b64 s[8:9], 0x80100
	v_add_u32_e32 v94, 0x2000, v221
	v_add_u32_e32 v83, v223, v3
	s_mov_b64 s[12:13], 0x1000180
	s_mov_b64 s[14:15], 0x180
	s_mov_b64 s[16:17], 0x80180
	v_add_u32_e32 v95, v6, v3
	v_add_u32_e32 v96, v7, v5
	s_mov_b64 s[18:19], 0x1000200
	s_mov_b64 s[20:21], 0x200
	s_mov_b64 s[22:23], 0x80200
	v_mov_b32_e32 v3, v2
	v_mov_b32_e32 v4, v2
	v_mov_b32_e32 v5, v2
	v_mov_b32_e32 v6, v2
	v_mov_b32_e32 v7, v2
	v_mov_b32_e32 v8, v2
	v_mov_b32_e32 v9, v2
	v_mov_b32_e32 v10, v2
	v_mov_b32_e32 v11, v2
	v_mov_b32_e32 v12, v2
	v_mov_b32_e32 v13, v2
	v_mov_b32_e32 v14, v2
	v_mov_b32_e32 v15, v2
	v_mov_b32_e32 v16, v2
	v_mov_b32_e32 v17, v2
	v_mov_b32_e32 v18, v2
	v_mov_b32_e32 v19, v2
	v_mov_b32_e32 v20, v2
	v_mov_b32_e32 v21, v2
	v_mov_b32_e32 v22, v2
	v_mov_b32_e32 v23, v2
	v_mov_b32_e32 v24, v2
	v_mov_b32_e32 v25, v2
	v_mov_b32_e32 v26, v2
	v_mov_b32_e32 v27, v2
	v_mov_b32_e32 v28, v2
	v_mov_b32_e32 v29, v2
	v_mov_b32_e32 v30, v2
	v_mov_b32_e32 v31, v2
	v_mov_b32_e32 v32, v2
	v_mov_b32_e32 v33, v2
	v_mov_b32_e32 v34, v2
	v_mov_b32_e32 v35, v2
	v_mov_b32_e32 v36, v2
	v_mov_b32_e32 v37, v2
	v_mov_b32_e32 v38, v2
	v_mov_b32_e32 v39, v2
	v_mov_b32_e32 v40, v2
	v_mov_b32_e32 v41, v2
	v_mov_b32_e32 v42, v2
	v_mov_b32_e32 v43, v2
	v_mov_b32_e32 v44, v2
	v_mov_b32_e32 v45, v2
	v_mov_b32_e32 v46, v2
	v_mov_b32_e32 v47, v2
	v_mov_b32_e32 v48, v2
	v_mov_b32_e32 v49, v2
	v_mov_b32_e32 v50, v2
	v_mov_b32_e32 v51, v2
	v_mov_b32_e32 v52, v2
	v_mov_b32_e32 v53, v2
	v_mov_b32_e32 v54, v2
	v_mov_b32_e32 v55, v2
	v_mov_b32_e32 v56, v2
	v_mov_b32_e32 v57, v2
	v_mov_b32_e32 v58, v2
	v_mov_b32_e32 v59, v2
	v_mov_b32_e32 v60, v2
	v_mov_b32_e32 v61, v2
	v_mov_b32_e32 v62, v2
	v_mov_b32_e32 v63, v2
	v_mov_b32_e32 v64, v2
	v_mov_b32_e32 v65, v2
	s_barrier
	s_barrier
	s_nop 1
	v_readfirstlane_b32 s74, v91
	v_readfirstlane_b32 s75, v92
	v_readfirstlane_b32 s76, v220
	v_readfirstlane_b32 s77, v93
	v_readfirstlane_b32 s78, v221
	v_readfirstlane_b32 s79, v94
	v_readfirstlane_b32 s80, v75
	v_readfirstlane_b32 s81, v76
	v_readfirstlane_b32 s82, v218
	v_readfirstlane_b32 s83, v77
	v_readfirstlane_b32 s84, v79
	v_readfirstlane_b32 s85, v80
	v_readfirstlane_b32 s86, v219
	v_readfirstlane_b32 s87, v81
	v_readfirstlane_b32 s88, v82
	v_readfirstlane_b32 s89, v84
	v_readfirstlane_b32 s90, v216
	v_readfirstlane_b32 s91, v85
	v_lshl_add_u64 v[162:163], v[72:73], 0, v[202:203]
	v_lshl_add_u64 v[98:99], v[162:163], 0, s[4:5]
	s_mov_b32 m0, s74
	v_lshl_add_u64 v[164:165], v[70:71], 0, v[202:203]
	global_load_lds_dwordx4 v[98:99], off
	v_lshl_add_u64 v[98:99], v[164:165], 0, s[4:5]
	s_mov_b32 m0, s75
	v_lshl_add_u64 v[166:167], v[68:69], 0, v[202:203]
	global_load_lds_dwordx4 v[98:99], off
	v_lshl_add_u64 v[98:99], v[166:167], 0, s[6:7]
	s_mov_b32 m0, s76
	v_lshl_add_u64 v[168:169], v[66:67], 0, v[202:203]
	global_load_lds_dwordx4 v[98:99], off
	s_mov_b32 m0, s77
	v_lshl_add_u64 v[98:99], v[168:169], 0, s[6:7]
	global_load_lds_dwordx4 v[98:99], off
	s_mov_b32 m0, s78
	v_lshl_add_u64 v[98:99], v[166:167], 0, s[8:9]
	global_load_lds_dwordx4 v[98:99], off
	s_mov_b32 m0, s79
	v_lshl_add_u64 v[98:99], v[168:169], 0, s[8:9]
	global_load_lds_dwordx4 v[98:99], off
	ds_read_b128 v[98:101], v90 offset:32768
	ds_read_b128 v[102:105], v90 offset:33792
	ds_read_b128 v[106:109], v90 offset:34816
	ds_read_b128 v[110:113], v90 offset:35840
	ds_read_b128 v[114:117], v90 offset:36864
	ds_read_b128 v[118:121], v90 offset:37888
	ds_read_b128 v[122:125], v90 offset:38912
	ds_read_b128 v[126:129], v90 offset:39936
	ds_read_b128 v[130:133], v78
	ds_read_b128 v[134:137], v78 offset:1024
	ds_read_b128 v[138:141], v78 offset:2048
	ds_read_b128 v[142:145], v78 offset:3072
	ds_read_b128 v[146:149], v78 offset:4096
	ds_read_b128 v[150:153], v78 offset:5120
	ds_read_b128 v[154:157], v78 offset:6144
	ds_read_b128 v[158:161], v78 offset:7168
	s_waitcnt vmcnt(6)
	s_waitcnt lgkmcnt(0)
	s_barrier
	s_setprio 1
	s_waitcnt lgkmcnt(0)
	v_mfma_f32_16x16x32_f16 v[62:65], v[98:101], v[130:133], v[62:65]
	s_lshl_b32 s60, s66, 16
	s_add_u32 s62, s58, s60
	s_addc_u32 s63, s59, 0
	s_lshl_b32 s61, s66, 15
	s_add_u32 s64, s52, s61
	s_addc_u32 s65, s53, 0
	v_lshlrev_b32_e32 v254, 5, v0
	v_lshlrev_b32_e32 v255, 4, v0
	global_load_dwordx4 v[230:233], v254, s[62:63] nt
	v_mfma_f32_16x16x32_f16 v[58:61], v[106:109], v[130:133], v[58:61]
	global_load_dwordx4 v[234:237], v254, s[62:63] offset:16 nt
	v_mfma_f32_16x16x32_f16 v[54:57], v[114:117], v[130:133], v[54:57]
	s_add_u32 s62, s62, 0x4000
	s_addc_u32 s63, s63, 0
	global_load_dwordx4 v[238:241], v254, s[62:63] nt
	v_mfma_f32_16x16x32_f16 v[50:53], v[122:125], v[130:133], v[50:53]
	global_load_dwordx4 v[242:245], v254, s[62:63] offset:16 nt
	v_mfma_f32_16x16x32_f16 v[46:49], v[98:101], v[138:141], v[46:49]
	s_add_u32 s62, s62, 0x4000
	s_addc_u32 s63, s63, 0
	global_load_dwordx4 v[246:249], v254, s[62:63] nt
	v_mfma_f32_16x16x32_f16 v[42:45], v[106:109], v[138:141], v[42:45]
	global_load_dwordx4 v[250:253], v254, s[62:63] offset:16 nt
	v_mfma_f32_16x16x32_f16 v[38:41], v[114:117], v[138:141], v[38:41]
	s_add_u32 s62, s62, 0x4000
	s_addc_u32 s63, s63, 0
	global_load_dwordx4 v[190:193], v254, s[62:63] nt
	v_mfma_f32_16x16x32_f16 v[34:37], v[122:125], v[138:141], v[34:37]
	global_load_dwordx4 v[194:197], v254, s[62:63] offset:16 nt
	v_mfma_f32_16x16x32_f16 v[30:33], v[98:101], v[146:149], v[30:33]
	v_mfma_f32_16x16x32_f16 v[26:29], v[106:109], v[146:149], v[26:29]
	v_mfma_f32_16x16x32_f16 v[22:25], v[114:117], v[146:149], v[22:25]
	v_mfma_f32_16x16x32_f16 v[18:21], v[122:125], v[146:149], v[18:21]
	v_mfma_f32_16x16x32_f16 v[14:17], v[98:101], v[154:157], v[14:17]
	v_mfma_f32_16x16x32_f16 v[10:13], v[106:109], v[154:157], v[10:13]
	v_mfma_f32_16x16x32_f16 v[6:9], v[114:117], v[154:157], v[6:9]
	v_mfma_f32_16x16x32_f16 v[2:5], v[122:125], v[154:157], v[2:5]
	v_mfma_f32_16x16x32_f16 v[62:65], v[102:105], v[134:137], v[62:65]
	v_mfma_f32_16x16x32_f16 v[58:61], v[110:113], v[134:137], v[58:61]
	v_mfma_f32_16x16x32_f16 v[54:57], v[118:121], v[134:137], v[54:57]
	v_mfma_f32_16x16x32_f16 v[50:53], v[126:129], v[134:137], v[50:53]
	v_mfma_f32_16x16x32_f16 v[46:49], v[102:105], v[142:145], v[46:49]
	v_mfma_f32_16x16x32_f16 v[42:45], v[110:113], v[142:145], v[42:45]
	v_mfma_f32_16x16x32_f16 v[38:41], v[118:121], v[142:145], v[38:41]
	v_mfma_f32_16x16x32_f16 v[34:37], v[126:129], v[142:145], v[34:37]
	v_mfma_f32_16x16x32_f16 v[30:33], v[102:105], v[150:153], v[30:33]
	v_mfma_f32_16x16x32_f16 v[26:29], v[110:113], v[150:153], v[26:29]
	v_mfma_f32_16x16x32_f16 v[22:25], v[118:121], v[150:153], v[22:25]
	v_mfma_f32_16x16x32_f16 v[18:21], v[126:129], v[150:153], v[18:21]
	v_mfma_f32_16x16x32_f16 v[14:17], v[102:105], v[158:161], v[14:17]
	v_mfma_f32_16x16x32_f16 v[10:13], v[110:113], v[158:161], v[10:13]
	v_mfma_f32_16x16x32_f16 v[6:9], v[118:121], v[158:161], v[6:9]
	v_mfma_f32_16x16x32_f16 v[2:5], v[126:129], v[158:161], v[2:5]
	s_setprio 0
	s_barrier
	v_lshl_add_u64 v[130:131], v[162:163], 0, s[12:13]
	s_mov_b32 m0, s80
	ds_read_b128 v[98:101], v78 offset:49152
	ds_read_b128 v[102:105], v78 offset:50176
	ds_read_b128 v[106:109], v78 offset:51200
	ds_read_b128 v[110:113], v78 offset:52224
	ds_read_b128 v[114:117], v78 offset:53248
	ds_read_b128 v[118:121], v78 offset:54272
	ds_read_b128 v[122:125], v78 offset:55296
	ds_read_b128 v[126:129], v78 offset:56320
	global_load_lds_dwordx4 v[130:131], off
	s_mov_b32 m0, s81
	v_lshl_add_u64 v[130:131], v[164:165], 0, s[12:13]
	global_load_lds_dwordx4 v[130:131], off
	s_mov_b32 m0, s82
	v_lshl_add_u64 v[130:131], v[166:167], 0, s[14:15]
	global_load_lds_dwordx4 v[130:131], off
	s_mov_b32 m0, s83
	v_lshl_add_u64 v[130:131], v[168:169], 0, s[14:15]
	global_load_lds_dwordx4 v[130:131], off
	s_mov_b32 m0, s84
	v_lshl_add_u64 v[130:131], v[166:167], 0, s[16:17]
	global_load_lds_dwordx4 v[130:131], off
	s_mov_b32 m0, s85
	v_lshl_add_u64 v[130:131], v[168:169], 0, s[16:17]
	global_load_lds_dwordx4 v[130:131], off
	ds_read_b128 v[130:133], v83
	ds_read_b128 v[134:137], v83 offset:1024
	ds_read_b128 v[138:141], v83 offset:2048
	ds_read_b128 v[142:145], v83 offset:3072
	ds_read_b128 v[146:149], v83 offset:4096
	ds_read_b128 v[150:153], v83 offset:5120
	ds_read_b128 v[154:157], v83 offset:6144
	ds_read_b128 v[158:161], v83 offset:7168
	s_waitcnt vmcnt(14)
	s_waitcnt lgkmcnt(0)
	s_barrier
	s_setprio 1
	s_waitcnt lgkmcnt(0)
	v_mfma_f32_16x16x32_f16 v[62:65], v[130:133], v[98:101], v[62:65]
	v_mfma_f32_16x16x32_f16 v[58:61], v[138:141], v[98:101], v[58:61]
	v_mfma_f32_16x16x32_f16 v[54:57], v[146:149], v[98:101], v[54:57]
	v_mfma_f32_16x16x32_f16 v[50:53], v[154:157], v[98:101], v[50:53]
	v_mfma_f32_16x16x32_f16 v[46:49], v[130:133], v[106:109], v[46:49]
	v_mfma_f32_16x16x32_f16 v[42:45], v[138:141], v[106:109], v[42:45]
	v_mfma_f32_16x16x32_f16 v[38:41], v[146:149], v[106:109], v[38:41]
	v_mfma_f32_16x16x32_f16 v[34:37], v[154:157], v[106:109], v[34:37]
	v_mfma_f32_16x16x32_f16 v[30:33], v[130:133], v[114:117], v[30:33]
	v_mfma_f32_16x16x32_f16 v[26:29], v[138:141], v[114:117], v[26:29]
	v_mfma_f32_16x16x32_f16 v[22:25], v[146:149], v[114:117], v[22:25]
	v_mfma_f32_16x16x32_f16 v[18:21], v[154:157], v[114:117], v[18:21]
	v_mfma_f32_16x16x32_f16 v[14:17], v[130:133], v[122:125], v[14:17]
	v_mfma_f32_16x16x32_f16 v[10:13], v[138:141], v[122:125], v[10:13]
	v_mfma_f32_16x16x32_f16 v[6:9], v[146:149], v[122:125], v[6:9]
	v_mfma_f32_16x16x32_f16 v[2:5], v[154:157], v[122:125], v[2:5]
	v_mfma_f32_16x16x32_f16 v[62:65], v[134:137], v[102:105], v[62:65]
	v_mfma_f32_16x16x32_f16 v[58:61], v[142:145], v[102:105], v[58:61]
	v_mfma_f32_16x16x32_f16 v[54:57], v[150:153], v[102:105], v[54:57]
	v_mfma_f32_16x16x32_f16 v[50:53], v[158:161], v[102:105], v[50:53]
	v_mfma_f32_16x16x32_f16 v[46:49], v[134:137], v[110:113], v[46:49]
	v_mfma_f32_16x16x32_f16 v[42:45], v[142:145], v[110:113], v[42:45]
	v_mfma_f32_16x16x32_f16 v[38:41], v[150:153], v[110:113], v[38:41]
	v_mfma_f32_16x16x32_f16 v[34:37], v[158:161], v[110:113], v[34:37]
	v_mfma_f32_16x16x32_f16 v[30:33], v[134:137], v[118:121], v[30:33]
	v_mfma_f32_16x16x32_f16 v[26:29], v[142:145], v[118:121], v[26:29]
	v_mfma_f32_16x16x32_f16 v[22:25], v[150:153], v[118:121], v[22:25]
	v_mfma_f32_16x16x32_f16 v[18:21], v[158:161], v[118:121], v[18:21]
	v_mfma_f32_16x16x32_f16 v[14:17], v[134:137], v[126:129], v[14:17]
	v_mfma_f32_16x16x32_f16 v[10:13], v[142:145], v[126:129], v[10:13]
	v_mfma_f32_16x16x32_f16 v[6:9], v[150:153], v[126:129], v[6:9]
	v_mfma_f32_16x16x32_f16 v[2:5], v[158:161], v[126:129], v[2:5]
	s_setprio 0
	s_barrier
	v_lshl_add_u64 v[130:131], v[162:163], 0, s[18:19]
	s_mov_b32 m0, s86
	ds_read_b128 v[98:101], v96
	ds_read_b128 v[102:105], v96 offset:1024
	ds_read_b128 v[106:109], v96 offset:2048
	ds_read_b128 v[110:113], v96 offset:3072
	ds_read_b128 v[114:117], v86
	ds_read_b128 v[118:121], v87
	ds_read_b128 v[122:125], v88
	ds_read_b128 v[126:129], v89
	global_load_lds_dwordx4 v[130:131], off
	s_mov_b32 m0, s87
	v_lshl_add_u64 v[130:131], v[164:165], 0, s[18:19]
	global_load_lds_dwordx4 v[130:131], off
	s_mov_b32 m0, s88
	v_lshl_add_u64 v[130:131], v[166:167], 0, s[20:21]
	global_load_lds_dwordx4 v[130:131], off
	s_mov_b32 m0, s89
	v_lshl_add_u64 v[130:131], v[168:169], 0, s[20:21]
	global_load_lds_dwordx4 v[130:131], off
	s_mov_b32 m0, s90
	v_lshl_add_u64 v[130:131], v[166:167], 0, s[22:23]
	global_load_lds_dwordx4 v[130:131], off
	s_mov_b32 m0, s91
	v_lshl_add_u64 v[130:131], v[168:169], 0, s[22:23]
	global_load_lds_dwordx4 v[130:131], off
	ds_read_b128 v[130:133], v95
	ds_read_b128 v[134:137], v95 offset:1024
	ds_read_b128 v[138:141], v95 offset:2048
	ds_read_b128 v[142:145], v95 offset:3072
	ds_read_b128 v[146:149], v95 offset:4096
	ds_read_b128 v[150:153], v95 offset:5120
	ds_read_b128 v[154:157], v95 offset:6144
	ds_read_b128 v[158:161], v95 offset:7168
	s_waitcnt vmcnt(6)
	s_waitcnt lgkmcnt(0)
	s_barrier
	s_setprio 1
	s_waitcnt lgkmcnt(0)
	v_mfma_f32_16x16x32_f16 v[62:65], v[130:133], v[98:101], v[62:65]
	v_cvt_pk_f16_f32 v230, v230, v231
	v_mfma_f32_16x16x32_f16 v[58:61], v[138:141], v[98:101], v[58:61]
	v_cvt_pk_f16_f32 v231, v232, v233
	v_mfma_f32_16x16x32_f16 v[54:57], v[146:149], v[98:101], v[54:57]
	v_cvt_pk_f16_f32 v232, v234, v235
	v_mfma_f32_16x16x32_f16 v[50:53], v[154:157], v[98:101], v[50:53]
	v_cvt_pk_f16_f32 v233, v236, v237
	v_mfma_f32_16x16x32_f16 v[46:49], v[130:133], v[106:109], v[46:49]
	global_store_dwordx4 v255, v[230:233], s[64:65]
	v_mfma_f32_16x16x32_f16 v[42:45], v[138:141], v[106:109], v[42:45]
	s_add_u32 s64, s64, 0x2000
	s_addc_u32 s65, s65, 0
	v_mfma_f32_16x16x32_f16 v[38:41], v[146:149], v[106:109], v[38:41]
	v_cvt_pk_f16_f32 v238, v238, v239
	v_mfma_f32_16x16x32_f16 v[34:37], v[154:157], v[106:109], v[34:37]
	v_cvt_pk_f16_f32 v239, v240, v241
	v_mfma_f32_16x16x32_f16 v[30:33], v[130:133], v[114:117], v[30:33]
	v_cvt_pk_f16_f32 v240, v242, v243
	v_mfma_f32_16x16x32_f16 v[26:29], v[138:141], v[114:117], v[26:29]
	v_cvt_pk_f16_f32 v241, v244, v245
	v_mfma_f32_16x16x32_f16 v[22:25], v[146:149], v[114:117], v[22:25]
	global_store_dwordx4 v255, v[238:241], s[64:65]
	v_mfma_f32_16x16x32_f16 v[18:21], v[154:157], v[114:117], v[18:21]
	s_add_u32 s64, s64, 0x2000
	s_addc_u32 s65, s65, 0
	v_mfma_f32_16x16x32_f16 v[14:17], v[130:133], v[122:125], v[14:17]
	v_cvt_pk_f16_f32 v246, v246, v247
	v_mfma_f32_16x16x32_f16 v[10:13], v[138:141], v[122:125], v[10:13]
	v_cvt_pk_f16_f32 v247, v248, v249
	v_mfma_f32_16x16x32_f16 v[6:9], v[146:149], v[122:125], v[6:9]
	v_cvt_pk_f16_f32 v248, v250, v251
	v_mfma_f32_16x16x32_f16 v[2:5], v[154:157], v[122:125], v[2:5]
	v_cvt_pk_f16_f32 v249, v252, v253
	v_mfma_f32_16x16x32_f16 v[62:65], v[134:137], v[102:105], v[62:65]
	global_store_dwordx4 v255, v[246:249], s[64:65]
	v_mfma_f32_16x16x32_f16 v[58:61], v[142:145], v[102:105], v[58:61]
	s_add_u32 s64, s64, 0x2000
	s_addc_u32 s65, s65, 0
	v_mfma_f32_16x16x32_f16 v[54:57], v[150:153], v[102:105], v[54:57]
	v_cvt_pk_f16_f32 v190, v190, v191
	v_mfma_f32_16x16x32_f16 v[50:53], v[158:161], v[102:105], v[50:53]
	v_cvt_pk_f16_f32 v191, v192, v193
	v_mfma_f32_16x16x32_f16 v[46:49], v[134:137], v[110:113], v[46:49]
	v_cvt_pk_f16_f32 v192, v194, v195
	v_mfma_f32_16x16x32_f16 v[42:45], v[142:145], v[110:113], v[42:45]
	v_cvt_pk_f16_f32 v193, v196, v197
	v_mfma_f32_16x16x32_f16 v[38:41], v[150:153], v[110:113], v[38:41]
	global_store_dwordx4 v255, v[190:193], s[64:65]
	v_mfma_f32_16x16x32_f16 v[34:37], v[158:161], v[110:113], v[34:37]
	v_mfma_f32_16x16x32_f16 v[30:33], v[134:137], v[118:121], v[30:33]
	v_mfma_f32_16x16x32_f16 v[26:29], v[142:145], v[118:121], v[26:29]
	v_mfma_f32_16x16x32_f16 v[22:25], v[150:153], v[118:121], v[22:25]
	v_mfma_f32_16x16x32_f16 v[18:21], v[158:161], v[118:121], v[18:21]
	v_mfma_f32_16x16x32_f16 v[14:17], v[134:137], v[126:129], v[14:17]
	v_mfma_f32_16x16x32_f16 v[10:13], v[142:145], v[126:129], v[10:13]
	v_mfma_f32_16x16x32_f16 v[6:9], v[150:153], v[126:129], v[6:9]
	v_mfma_f32_16x16x32_f16 v[2:5], v[158:161], v[126:129], v[2:5]
	s_setprio 0
	s_barrier
	s_add_i32 s3, s3, 3
	v_lshl_add_u64 v[66:67], v[66:67], 0, s[14:15]
	v_lshl_add_u64 v[68:69], v[68:69], 0, s[14:15]
	v_lshl_add_u64 v[70:71], v[70:71], 0, s[14:15]
	v_lshl_add_u64 v[72:73], v[72:73], 0, s[14:15]
.LBB1_113:
	v_lshl_add_u64 v[162:163], v[72:73], 0, v[202:203]
	v_lshl_add_u64 v[98:99], v[162:163], 0, s[4:5]
	s_mov_b32 m0, s74
	v_lshl_add_u64 v[164:165], v[70:71], 0, v[202:203]
	global_load_lds_dwordx4 v[98:99], off
	v_lshl_add_u64 v[98:99], v[164:165], 0, s[4:5]
	s_mov_b32 m0, s75
	v_lshl_add_u64 v[166:167], v[68:69], 0, v[202:203]
	global_load_lds_dwordx4 v[98:99], off
	v_lshl_add_u64 v[98:99], v[166:167], 0, s[6:7]
	s_mov_b32 m0, s76
	v_lshl_add_u64 v[168:169], v[66:67], 0, v[202:203]
	global_load_lds_dwordx4 v[98:99], off
	s_mov_b32 m0, s77
	v_lshl_add_u64 v[98:99], v[168:169], 0, s[6:7]
	global_load_lds_dwordx4 v[98:99], off
	s_mov_b32 m0, s78
	v_lshl_add_u64 v[98:99], v[166:167], 0, s[8:9]
	global_load_lds_dwordx4 v[98:99], off
	s_mov_b32 m0, s79
	v_lshl_add_u64 v[98:99], v[168:169], 0, s[8:9]
	global_load_lds_dwordx4 v[98:99], off
	ds_read_b128 v[98:101], v90 offset:32768
	ds_read_b128 v[102:105], v90 offset:33792
	ds_read_b128 v[106:109], v90 offset:34816
	ds_read_b128 v[110:113], v90 offset:35840
	ds_read_b128 v[114:117], v90 offset:36864
	ds_read_b128 v[118:121], v90 offset:37888
	ds_read_b128 v[122:125], v90 offset:38912
	ds_read_b128 v[126:129], v90 offset:39936
	ds_read_b128 v[130:133], v78
	ds_read_b128 v[134:137], v78 offset:1024
	ds_read_b128 v[138:141], v78 offset:2048
	ds_read_b128 v[142:145], v78 offset:3072
	ds_read_b128 v[146:149], v78 offset:4096
	ds_read_b128 v[150:153], v78 offset:5120
	ds_read_b128 v[154:157], v78 offset:6144
	ds_read_b128 v[158:161], v78 offset:7168
	s_waitcnt vmcnt(6)
	s_waitcnt lgkmcnt(0)
	s_barrier
	s_setprio 1
	s_waitcnt lgkmcnt(0)
	v_mfma_f32_16x16x32_f16 v[62:65], v[98:101], v[130:133], v[62:65]
	v_mfma_f32_16x16x32_f16 v[58:61], v[106:109], v[130:133], v[58:61]
	v_mfma_f32_16x16x32_f16 v[54:57], v[114:117], v[130:133], v[54:57]
	v_mfma_f32_16x16x32_f16 v[50:53], v[122:125], v[130:133], v[50:53]
	v_mfma_f32_16x16x32_f16 v[46:49], v[98:101], v[138:141], v[46:49]
	v_mfma_f32_16x16x32_f16 v[42:45], v[106:109], v[138:141], v[42:45]
	v_mfma_f32_16x16x32_f16 v[38:41], v[114:117], v[138:141], v[38:41]
	v_mfma_f32_16x16x32_f16 v[34:37], v[122:125], v[138:141], v[34:37]
	v_mfma_f32_16x16x32_f16 v[30:33], v[98:101], v[146:149], v[30:33]
	v_mfma_f32_16x16x32_f16 v[26:29], v[106:109], v[146:149], v[26:29]
	v_mfma_f32_16x16x32_f16 v[22:25], v[114:117], v[146:149], v[22:25]
	v_mfma_f32_16x16x32_f16 v[18:21], v[122:125], v[146:149], v[18:21]
	v_mfma_f32_16x16x32_f16 v[14:17], v[98:101], v[154:157], v[14:17]
	v_mfma_f32_16x16x32_f16 v[10:13], v[106:109], v[154:157], v[10:13]
	v_mfma_f32_16x16x32_f16 v[6:9], v[114:117], v[154:157], v[6:9]
	v_mfma_f32_16x16x32_f16 v[2:5], v[122:125], v[154:157], v[2:5]
	v_mfma_f32_16x16x32_f16 v[62:65], v[102:105], v[134:137], v[62:65]
	v_mfma_f32_16x16x32_f16 v[58:61], v[110:113], v[134:137], v[58:61]
	v_mfma_f32_16x16x32_f16 v[54:57], v[118:121], v[134:137], v[54:57]
	v_mfma_f32_16x16x32_f16 v[50:53], v[126:129], v[134:137], v[50:53]
	v_mfma_f32_16x16x32_f16 v[46:49], v[102:105], v[142:145], v[46:49]
	v_mfma_f32_16x16x32_f16 v[42:45], v[110:113], v[142:145], v[42:45]
	v_mfma_f32_16x16x32_f16 v[38:41], v[118:121], v[142:145], v[38:41]
	v_mfma_f32_16x16x32_f16 v[34:37], v[126:129], v[142:145], v[34:37]
	v_mfma_f32_16x16x32_f16 v[30:33], v[102:105], v[150:153], v[30:33]
	v_mfma_f32_16x16x32_f16 v[26:29], v[110:113], v[150:153], v[26:29]
	v_mfma_f32_16x16x32_f16 v[22:25], v[118:121], v[150:153], v[22:25]
	v_mfma_f32_16x16x32_f16 v[18:21], v[126:129], v[150:153], v[18:21]
	v_mfma_f32_16x16x32_f16 v[14:17], v[102:105], v[158:161], v[14:17]
	v_mfma_f32_16x16x32_f16 v[10:13], v[110:113], v[158:161], v[10:13]
	v_mfma_f32_16x16x32_f16 v[6:9], v[118:121], v[158:161], v[6:9]
	v_mfma_f32_16x16x32_f16 v[2:5], v[126:129], v[158:161], v[2:5]
	s_setprio 0
	s_barrier
	v_lshl_add_u64 v[130:131], v[162:163], 0, s[12:13]
	s_mov_b32 m0, s80
	ds_read_b128 v[98:101], v78 offset:49152
	ds_read_b128 v[102:105], v78 offset:50176
	ds_read_b128 v[106:109], v78 offset:51200
	ds_read_b128 v[110:113], v78 offset:52224
	ds_read_b128 v[114:117], v78 offset:53248
	ds_read_b128 v[118:121], v78 offset:54272
	ds_read_b128 v[122:125], v78 offset:55296
	ds_read_b128 v[126:129], v78 offset:56320
	global_load_lds_dwordx4 v[130:131], off
	s_mov_b32 m0, s81
	v_lshl_add_u64 v[130:131], v[164:165], 0, s[12:13]
	global_load_lds_dwordx4 v[130:131], off
	s_mov_b32 m0, s82
	v_lshl_add_u64 v[130:131], v[166:167], 0, s[14:15]
	global_load_lds_dwordx4 v[130:131], off
	s_mov_b32 m0, s83
	v_lshl_add_u64 v[130:131], v[168:169], 0, s[14:15]
	global_load_lds_dwordx4 v[130:131], off
	s_mov_b32 m0, s84
	v_lshl_add_u64 v[130:131], v[166:167], 0, s[16:17]
	global_load_lds_dwordx4 v[130:131], off
	s_mov_b32 m0, s85
	v_lshl_add_u64 v[130:131], v[168:169], 0, s[16:17]
	global_load_lds_dwordx4 v[130:131], off
	ds_read_b128 v[130:133], v83
	ds_read_b128 v[134:137], v83 offset:1024
	ds_read_b128 v[138:141], v83 offset:2048
	ds_read_b128 v[142:145], v83 offset:3072
	ds_read_b128 v[146:149], v83 offset:4096
	ds_read_b128 v[150:153], v83 offset:5120
	ds_read_b128 v[154:157], v83 offset:6144
	ds_read_b128 v[158:161], v83 offset:7168
	s_waitcnt vmcnt(6)
	s_waitcnt lgkmcnt(0)
	s_barrier
	s_setprio 1
	s_waitcnt lgkmcnt(0)
	v_mfma_f32_16x16x32_f16 v[62:65], v[130:133], v[98:101], v[62:65]
	v_mfma_f32_16x16x32_f16 v[58:61], v[138:141], v[98:101], v[58:61]
	v_mfma_f32_16x16x32_f16 v[54:57], v[146:149], v[98:101], v[54:57]
	v_mfma_f32_16x16x32_f16 v[50:53], v[154:157], v[98:101], v[50:53]
	v_mfma_f32_16x16x32_f16 v[46:49], v[130:133], v[106:109], v[46:49]
	v_mfma_f32_16x16x32_f16 v[42:45], v[138:141], v[106:109], v[42:45]
	v_mfma_f32_16x16x32_f16 v[38:41], v[146:149], v[106:109], v[38:41]
	v_mfma_f32_16x16x32_f16 v[34:37], v[154:157], v[106:109], v[34:37]
	v_mfma_f32_16x16x32_f16 v[30:33], v[130:133], v[114:117], v[30:33]
	v_mfma_f32_16x16x32_f16 v[26:29], v[138:141], v[114:117], v[26:29]
	v_mfma_f32_16x16x32_f16 v[22:25], v[146:149], v[114:117], v[22:25]
	v_mfma_f32_16x16x32_f16 v[18:21], v[154:157], v[114:117], v[18:21]
	v_mfma_f32_16x16x32_f16 v[14:17], v[130:133], v[122:125], v[14:17]
	v_mfma_f32_16x16x32_f16 v[10:13], v[138:141], v[122:125], v[10:13]
	v_mfma_f32_16x16x32_f16 v[6:9], v[146:149], v[122:125], v[6:9]
	v_mfma_f32_16x16x32_f16 v[2:5], v[154:157], v[122:125], v[2:5]
	v_mfma_f32_16x16x32_f16 v[62:65], v[134:137], v[102:105], v[62:65]
	v_mfma_f32_16x16x32_f16 v[58:61], v[142:145], v[102:105], v[58:61]
	v_mfma_f32_16x16x32_f16 v[54:57], v[150:153], v[102:105], v[54:57]
	v_mfma_f32_16x16x32_f16 v[50:53], v[158:161], v[102:105], v[50:53]
	v_mfma_f32_16x16x32_f16 v[46:49], v[134:137], v[110:113], v[46:49]
	v_mfma_f32_16x16x32_f16 v[42:45], v[142:145], v[110:113], v[42:45]
	v_mfma_f32_16x16x32_f16 v[38:41], v[150:153], v[110:113], v[38:41]
	v_mfma_f32_16x16x32_f16 v[34:37], v[158:161], v[110:113], v[34:37]
	v_mfma_f32_16x16x32_f16 v[30:33], v[134:137], v[118:121], v[30:33]
	v_mfma_f32_16x16x32_f16 v[26:29], v[142:145], v[118:121], v[26:29]
	v_mfma_f32_16x16x32_f16 v[22:25], v[150:153], v[118:121], v[22:25]
	v_mfma_f32_16x16x32_f16 v[18:21], v[158:161], v[118:121], v[18:21]
	v_mfma_f32_16x16x32_f16 v[14:17], v[134:137], v[126:129], v[14:17]
	v_mfma_f32_16x16x32_f16 v[10:13], v[142:145], v[126:129], v[10:13]
	v_mfma_f32_16x16x32_f16 v[6:9], v[150:153], v[126:129], v[6:9]
	v_mfma_f32_16x16x32_f16 v[2:5], v[158:161], v[126:129], v[2:5]
	s_setprio 0
	s_barrier
	v_lshl_add_u64 v[130:131], v[162:163], 0, s[18:19]
	s_mov_b32 m0, s86
	ds_read_b128 v[98:101], v96
	ds_read_b128 v[102:105], v96 offset:1024
	ds_read_b128 v[106:109], v96 offset:2048
	ds_read_b128 v[110:113], v96 offset:3072
	ds_read_b128 v[114:117], v86
	ds_read_b128 v[118:121], v87
	ds_read_b128 v[122:125], v88
	ds_read_b128 v[126:129], v89
	global_load_lds_dwordx4 v[130:131], off
	s_mov_b32 m0, s87
	v_lshl_add_u64 v[130:131], v[164:165], 0, s[18:19]
	global_load_lds_dwordx4 v[130:131], off
	s_mov_b32 m0, s88
	v_lshl_add_u64 v[130:131], v[166:167], 0, s[20:21]
	global_load_lds_dwordx4 v[130:131], off
	s_mov_b32 m0, s89
	v_lshl_add_u64 v[130:131], v[168:169], 0, s[20:21]
	global_load_lds_dwordx4 v[130:131], off
	s_mov_b32 m0, s90
	v_lshl_add_u64 v[130:131], v[166:167], 0, s[22:23]
	global_load_lds_dwordx4 v[130:131], off
	s_mov_b32 m0, s91
	v_lshl_add_u64 v[130:131], v[168:169], 0, s[22:23]
	global_load_lds_dwordx4 v[130:131], off
	ds_read_b128 v[130:133], v95
	ds_read_b128 v[134:137], v95 offset:1024
	ds_read_b128 v[138:141], v95 offset:2048
	ds_read_b128 v[142:145], v95 offset:3072
	ds_read_b128 v[146:149], v95 offset:4096
	ds_read_b128 v[150:153], v95 offset:5120
	ds_read_b128 v[154:157], v95 offset:6144
	ds_read_b128 v[158:161], v95 offset:7168
	s_waitcnt vmcnt(6)
	s_waitcnt lgkmcnt(0)
	s_barrier
	s_setprio 1
	s_waitcnt lgkmcnt(0)
	v_mfma_f32_16x16x32_f16 v[62:65], v[130:133], v[98:101], v[62:65]
	v_mfma_f32_16x16x32_f16 v[58:61], v[138:141], v[98:101], v[58:61]
	v_mfma_f32_16x16x32_f16 v[54:57], v[146:149], v[98:101], v[54:57]
	v_mfma_f32_16x16x32_f16 v[50:53], v[154:157], v[98:101], v[50:53]
	v_mfma_f32_16x16x32_f16 v[46:49], v[130:133], v[106:109], v[46:49]
	v_mfma_f32_16x16x32_f16 v[42:45], v[138:141], v[106:109], v[42:45]
	v_mfma_f32_16x16x32_f16 v[38:41], v[146:149], v[106:109], v[38:41]
	v_mfma_f32_16x16x32_f16 v[34:37], v[154:157], v[106:109], v[34:37]
	v_mfma_f32_16x16x32_f16 v[30:33], v[130:133], v[114:117], v[30:33]
	v_mfma_f32_16x16x32_f16 v[26:29], v[138:141], v[114:117], v[26:29]
	v_mfma_f32_16x16x32_f16 v[22:25], v[146:149], v[114:117], v[22:25]
	v_mfma_f32_16x16x32_f16 v[18:21], v[154:157], v[114:117], v[18:21]
	v_mfma_f32_16x16x32_f16 v[14:17], v[130:133], v[122:125], v[14:17]
	v_mfma_f32_16x16x32_f16 v[10:13], v[138:141], v[122:125], v[10:13]
	v_mfma_f32_16x16x32_f16 v[6:9], v[146:149], v[122:125], v[6:9]
	v_mfma_f32_16x16x32_f16 v[2:5], v[154:157], v[122:125], v[2:5]
	v_mfma_f32_16x16x32_f16 v[62:65], v[134:137], v[102:105], v[62:65]
	v_mfma_f32_16x16x32_f16 v[58:61], v[142:145], v[102:105], v[58:61]
	v_mfma_f32_16x16x32_f16 v[54:57], v[150:153], v[102:105], v[54:57]
	v_mfma_f32_16x16x32_f16 v[50:53], v[158:161], v[102:105], v[50:53]
	v_mfma_f32_16x16x32_f16 v[46:49], v[134:137], v[110:113], v[46:49]
	v_mfma_f32_16x16x32_f16 v[42:45], v[142:145], v[110:113], v[42:45]
	v_mfma_f32_16x16x32_f16 v[38:41], v[150:153], v[110:113], v[38:41]
	v_mfma_f32_16x16x32_f16 v[34:37], v[158:161], v[110:113], v[34:37]
	v_mfma_f32_16x16x32_f16 v[30:33], v[134:137], v[118:121], v[30:33]
	v_mfma_f32_16x16x32_f16 v[26:29], v[142:145], v[118:121], v[26:29]
	v_mfma_f32_16x16x32_f16 v[22:25], v[150:153], v[118:121], v[22:25]
	v_mfma_f32_16x16x32_f16 v[18:21], v[158:161], v[118:121], v[18:21]
	v_mfma_f32_16x16x32_f16 v[14:17], v[134:137], v[126:129], v[14:17]
	v_mfma_f32_16x16x32_f16 v[10:13], v[142:145], v[126:129], v[10:13]
	v_mfma_f32_16x16x32_f16 v[6:9], v[150:153], v[126:129], v[6:9]
	v_mfma_f32_16x16x32_f16 v[2:5], v[158:161], v[126:129], v[2:5]
	s_setprio 0
	s_barrier
	s_add_i32 s3, s3, 3
	v_lshl_add_u64 v[66:67], v[66:67], 0, s[14:15]
	v_lshl_add_u64 v[68:69], v[68:69], 0, s[14:15]
	v_lshl_add_u64 v[70:71], v[70:71], 0, s[14:15]
	s_cmp_lt_u32 s3, 27
	v_lshl_add_u64 v[72:73], v[72:73], 0, s[14:15]
	s_cbranch_scc1 .LBB1_113
	ds_read_b128 v[66:69], v90 offset:32768
	ds_read_b128 v[70:73], v90 offset:33792
	ds_read_b128 v[84:87], v90 offset:34816
	ds_read_b128 v[92:95], v90 offset:35840
	ds_read_b128 v[96:99], v90 offset:36864
	ds_read_b128 v[100:103], v90 offset:37888
	ds_read_b128 v[104:107], v90 offset:38912
	ds_read_b128 v[88:91], v90 offset:39936
	ds_read_b128 v[108:111], v78
	ds_read_b128 v[112:115], v78 offset:1024
	ds_read_b128 v[116:119], v78 offset:2048
	ds_read_b128 v[120:123], v78 offset:3072
	ds_read_b128 v[124:127], v78 offset:4096
	ds_read_b128 v[128:131], v78 offset:5120
	ds_read_b128 v[132:135], v78 offset:6144
	ds_read_b128 v[136:139], v78 offset:7168
	s_waitcnt vmcnt(0)
	s_waitcnt lgkmcnt(0)
	s_barrier
	s_setprio 1
	s_waitcnt lgkmcnt(0)
	v_mfma_f32_16x16x32_f16 v[62:65], v[66:69], v[108:111], v[62:65]
	v_mfma_f32_16x16x32_f16 v[58:61], v[84:87], v[108:111], v[58:61]
	v_mfma_f32_16x16x32_f16 v[54:57], v[96:99], v[108:111], v[54:57]
	v_mfma_f32_16x16x32_f16 v[50:53], v[104:107], v[108:111], v[50:53]
	v_mfma_f32_16x16x32_f16 v[46:49], v[66:69], v[116:119], v[46:49]
	v_mfma_f32_16x16x32_f16 v[42:45], v[84:87], v[116:119], v[42:45]
	v_mfma_f32_16x16x32_f16 v[38:41], v[96:99], v[116:119], v[38:41]
	v_mfma_f32_16x16x32_f16 v[34:37], v[104:107], v[116:119], v[34:37]
	v_mfma_f32_16x16x32_f16 v[30:33], v[66:69], v[124:127], v[30:33]
	v_mfma_f32_16x16x32_f16 v[26:29], v[84:87], v[124:127], v[26:29]
	v_mfma_f32_16x16x32_f16 v[22:25], v[96:99], v[124:127], v[22:25]
	v_mfma_f32_16x16x32_f16 v[18:21], v[104:107], v[124:127], v[18:21]
	v_mfma_f32_16x16x32_f16 v[14:17], v[66:69], v[132:135], v[14:17]
	v_mfma_f32_16x16x32_f16 v[10:13], v[84:87], v[132:135], v[10:13]
	v_mfma_f32_16x16x32_f16 v[6:9], v[96:99], v[132:135], v[6:9]
	v_mfma_f32_16x16x32_f16 v[2:5], v[104:107], v[132:135], v[2:5]
	v_mfma_f32_16x16x32_f16 v[62:65], v[70:73], v[112:115], v[62:65]
	v_mfma_f32_16x16x32_f16 v[58:61], v[92:95], v[112:115], v[58:61]
	v_mfma_f32_16x16x32_f16 v[54:57], v[100:103], v[112:115], v[54:57]
	v_mfma_f32_16x16x32_f16 v[50:53], v[88:91], v[112:115], v[50:53]
	v_mfma_f32_16x16x32_f16 v[46:49], v[70:73], v[120:123], v[46:49]
	v_mfma_f32_16x16x32_f16 v[42:45], v[92:95], v[120:123], v[42:45]
	v_mfma_f32_16x16x32_f16 v[38:41], v[100:103], v[120:123], v[38:41]
	v_mfma_f32_16x16x32_f16 v[34:37], v[88:91], v[120:123], v[34:37]
	v_mfma_f32_16x16x32_f16 v[30:33], v[70:73], v[128:131], v[30:33]
	v_mfma_f32_16x16x32_f16 v[26:29], v[92:95], v[128:131], v[26:29]
	v_mfma_f32_16x16x32_f16 v[22:25], v[100:103], v[128:131], v[22:25]
	v_mfma_f32_16x16x32_f16 v[18:21], v[88:91], v[128:131], v[18:21]
	v_mfma_f32_16x16x32_f16 v[14:17], v[70:73], v[136:139], v[14:17]
	v_mfma_f32_16x16x32_f16 v[10:13], v[92:95], v[136:139], v[10:13]
	v_mfma_f32_16x16x32_f16 v[6:9], v[100:103], v[136:139], v[6:9]
	v_mfma_f32_16x16x32_f16 v[2:5], v[88:91], v[136:139], v[2:5]
	s_setprio 0
	s_barrier
	ds_read_b128 v[66:69], v83
	ds_read_b128 v[70:73], v83 offset:1024
	ds_read_b128 v[84:87], v83 offset:2048
	ds_read_b128 v[88:91], v83 offset:3072
	ds_read_b128 v[92:95], v83 offset:4096
	ds_read_b128 v[96:99], v83 offset:5120
	ds_read_b128 v[100:103], v83 offset:6144
	ds_read_b128 v[80:83], v83 offset:7168
	ds_read_b128 v[104:107], v78 offset:49152
	ds_read_b128 v[108:111], v78 offset:50176
	ds_read_b128 v[112:115], v78 offset:51200
	ds_read_b128 v[116:119], v78 offset:52224
	ds_read_b128 v[120:123], v78 offset:53248
	ds_read_b128 v[124:127], v78 offset:54272
	ds_read_b128 v[128:131], v78 offset:55296
	ds_read_b128 v[76:79], v78 offset:56320
	s_waitcnt lgkmcnt(0)
	s_barrier
	s_setprio 1
	s_waitcnt lgkmcnt(0)
	v_mfma_f32_16x16x32_f16 v[62:65], v[66:69], v[104:107], v[62:65]
	v_mfma_f32_16x16x32_f16 v[58:61], v[84:87], v[104:107], v[58:61]
	v_mfma_f32_16x16x32_f16 v[54:57], v[92:95], v[104:107], v[54:57]
	v_mfma_f32_16x16x32_f16 v[50:53], v[100:103], v[104:107], v[50:53]
	v_mfma_f32_16x16x32_f16 v[46:49], v[66:69], v[112:115], v[46:49]
	v_mfma_f32_16x16x32_f16 v[42:45], v[84:87], v[112:115], v[42:45]
	v_mfma_f32_16x16x32_f16 v[38:41], v[92:95], v[112:115], v[38:41]
	v_mfma_f32_16x16x32_f16 v[34:37], v[100:103], v[112:115], v[34:37]
	v_mfma_f32_16x16x32_f16 v[30:33], v[66:69], v[120:123], v[30:33]
	v_mfma_f32_16x16x32_f16 v[26:29], v[84:87], v[120:123], v[26:29]
	v_mfma_f32_16x16x32_f16 v[22:25], v[92:95], v[120:123], v[22:25]
	v_mfma_f32_16x16x32_f16 v[18:21], v[100:103], v[120:123], v[18:21]
	v_mfma_f32_16x16x32_f16 v[14:17], v[66:69], v[128:131], v[14:17]
	v_mfma_f32_16x16x32_f16 v[10:13], v[84:87], v[128:131], v[10:13]
	v_mfma_f32_16x16x32_f16 v[6:9], v[92:95], v[128:131], v[6:9]
	v_mfma_f32_16x16x32_f16 v[2:5], v[100:103], v[128:131], v[2:5]
	v_mfma_f32_16x16x32_f16 v[62:65], v[70:73], v[108:111], v[62:65]
	v_mfma_f32_16x16x32_f16 v[58:61], v[88:91], v[108:111], v[58:61]
	v_mfma_f32_16x16x32_f16 v[54:57], v[96:99], v[108:111], v[54:57]
	v_mfma_f32_16x16x32_f16 v[50:53], v[80:83], v[108:111], v[50:53]
	v_mfma_f32_16x16x32_f16 v[46:49], v[70:73], v[116:119], v[46:49]
	v_mfma_f32_16x16x32_f16 v[42:45], v[88:91], v[116:119], v[42:45]
	v_mfma_f32_16x16x32_f16 v[38:41], v[96:99], v[116:119], v[38:41]
	v_mfma_f32_16x16x32_f16 v[34:37], v[80:83], v[116:119], v[34:37]
	v_mfma_f32_16x16x32_f16 v[30:33], v[70:73], v[124:127], v[30:33]
	v_mfma_f32_16x16x32_f16 v[26:29], v[88:91], v[124:127], v[26:29]
	v_mfma_f32_16x16x32_f16 v[22:25], v[96:99], v[124:127], v[22:25]
	v_mfma_f32_16x16x32_f16 v[18:21], v[80:83], v[124:127], v[18:21]
	v_mfma_f32_16x16x32_f16 v[14:17], v[70:73], v[76:79], v[14:17]
	v_mfma_f32_16x16x32_f16 v[10:13], v[88:91], v[76:79], v[10:13]
	v_mfma_f32_16x16x32_f16 v[6:9], v[96:99], v[76:79], v[6:9]
	v_mfma_f32_16x16x32_f16 v[2:5], v[80:83], v[76:79], v[2:5]
	s_setprio 0
	s_barrier
	s_and_saveexec_b64 s[4:5], s[0:1]
	s_cbranch_execz .LBB1_116
	s_barrier

.LBB2_7:
	v_lshl_add_u64 v[170:171], v[74:75], 0, v[66:67]
	v_lshl_add_u64 v[106:107], v[170:171], 0, s[4:5]
	s_mov_b32 m0, s50
	v_lshl_add_u64 v[172:173], v[72:73], 0, v[66:67]
	global_load_lds_dwordx4 v[106:107], off
	v_lshl_add_u64 v[106:107], v[172:173], 0, s[4:5]
	s_mov_b32 m0, s51
	v_lshl_add_u64 v[174:175], v[70:71], 0, v[66:67]
	global_load_lds_dwordx4 v[106:107], off
	v_lshl_add_u64 v[106:107], v[174:175], 0, s[4:5]
	s_mov_b32 m0, s52
	v_lshl_add_u64 v[176:177], v[68:69], 0, v[66:67]
	global_load_lds_dwordx4 v[106:107], off
	s_mov_b32 m0, s53
	v_lshl_add_u64 v[106:107], v[176:177], 0, s[4:5]
	global_load_lds_dwordx4 v[106:107], off
	s_mov_b32 m0, s54
	v_lshl_add_u64 v[106:107], v[174:175], 0, s[6:7]
	global_load_lds_dwordx4 v[106:107], off
	s_mov_b32 m0, s55
	v_lshl_add_u64 v[106:107], v[176:177], 0, s[6:7]
	global_load_lds_dwordx4 v[106:107], off
	ds_read_b128 v[106:109], v90 offset:32768
	ds_read_b128 v[110:113], v90 offset:33792
	ds_read_b128 v[114:117], v90 offset:34816
	ds_read_b128 v[118:121], v90 offset:35840
	ds_read_b128 v[122:125], v90 offset:36864
	ds_read_b128 v[126:129], v90 offset:37888
	ds_read_b128 v[130:133], v90 offset:38912
	ds_read_b128 v[134:137], v90 offset:39936
	ds_read_b128 v[138:141], v83
	ds_read_b128 v[142:145], v83 offset:1024
	ds_read_b128 v[146:149], v83 offset:2048
	ds_read_b128 v[150:153], v83 offset:3072
	ds_read_b128 v[154:157], v83 offset:4096
	ds_read_b128 v[158:161], v83 offset:5120
	ds_read_b128 v[162:165], v83 offset:6144
	ds_read_b128 v[166:169], v83 offset:7168
	s_waitcnt vmcnt(6)
	s_waitcnt lgkmcnt(0)
	s_barrier
	s_setprio 1
	s_waitcnt lgkmcnt(0)
	v_mfma_f32_16x16x32_f16 v[62:65], v[106:109], v[138:141], v[62:65]
	v_mfma_f32_16x16x32_f16 v[58:61], v[114:117], v[138:141], v[58:61]
	v_mfma_f32_16x16x32_f16 v[54:57], v[122:125], v[138:141], v[54:57]
	v_mfma_f32_16x16x32_f16 v[50:53], v[130:133], v[138:141], v[50:53]
	v_mfma_f32_16x16x32_f16 v[46:49], v[106:109], v[146:149], v[46:49]
	v_mfma_f32_16x16x32_f16 v[42:45], v[114:117], v[146:149], v[42:45]
	v_mfma_f32_16x16x32_f16 v[38:41], v[122:125], v[146:149], v[38:41]
	v_mfma_f32_16x16x32_f16 v[34:37], v[130:133], v[146:149], v[34:37]
	v_mfma_f32_16x16x32_f16 v[30:33], v[106:109], v[154:157], v[30:33]
	v_mfma_f32_16x16x32_f16 v[26:29], v[114:117], v[154:157], v[26:29]
	v_mfma_f32_16x16x32_f16 v[22:25], v[122:125], v[154:157], v[22:25]
	v_mfma_f32_16x16x32_f16 v[18:21], v[130:133], v[154:157], v[18:21]
	v_mfma_f32_16x16x32_f16 v[14:17], v[106:109], v[162:165], v[14:17]
	v_mfma_f32_16x16x32_f16 v[10:13], v[114:117], v[162:165], v[10:13]
	v_mfma_f32_16x16x32_f16 v[6:9], v[122:125], v[162:165], v[6:9]
	v_mfma_f32_16x16x32_f16 v[2:5], v[130:133], v[162:165], v[2:5]
	v_mfma_f32_16x16x32_f16 v[62:65], v[110:113], v[142:145], v[62:65]
	v_mfma_f32_16x16x32_f16 v[58:61], v[118:121], v[142:145], v[58:61]
	v_mfma_f32_16x16x32_f16 v[54:57], v[126:129], v[142:145], v[54:57]
	v_mfma_f32_16x16x32_f16 v[50:53], v[134:137], v[142:145], v[50:53]
	v_mfma_f32_16x16x32_f16 v[46:49], v[110:113], v[150:153], v[46:49]
	v_mfma_f32_16x16x32_f16 v[42:45], v[118:121], v[150:153], v[42:45]
	v_mfma_f32_16x16x32_f16 v[38:41], v[126:129], v[150:153], v[38:41]
	v_mfma_f32_16x16x32_f16 v[34:37], v[134:137], v[150:153], v[34:37]
	v_mfma_f32_16x16x32_f16 v[30:33], v[110:113], v[158:161], v[30:33]
	v_mfma_f32_16x16x32_f16 v[26:29], v[118:121], v[158:161], v[26:29]
	v_mfma_f32_16x16x32_f16 v[22:25], v[126:129], v[158:161], v[22:25]
	v_mfma_f32_16x16x32_f16 v[18:21], v[134:137], v[158:161], v[18:21]
	v_mfma_f32_16x16x32_f16 v[14:17], v[110:113], v[166:169], v[14:17]
	v_mfma_f32_16x16x32_f16 v[10:13], v[118:121], v[166:169], v[10:13]
	v_mfma_f32_16x16x32_f16 v[6:9], v[126:129], v[166:169], v[6:9]
	v_mfma_f32_16x16x32_f16 v[2:5], v[134:137], v[166:169], v[2:5]
	s_setprio 0
	s_barrier
	v_lshl_add_u64 v[138:139], v[170:171], 0, s[12:13]
	s_mov_b32 m0, s56
	ds_read_b128 v[106:109], v83 offset:49152
	ds_read_b128 v[110:113], v83 offset:50176
	ds_read_b128 v[114:117], v83 offset:51200
	ds_read_b128 v[118:121], v83 offset:52224
	ds_read_b128 v[122:125], v83 offset:53248
	ds_read_b128 v[126:129], v83 offset:54272
	ds_read_b128 v[130:133], v83 offset:55296
	ds_read_b128 v[134:137], v83 offset:56320
	global_load_lds_dwordx4 v[138:139], off
	s_mov_b32 m0, s57
	v_lshl_add_u64 v[138:139], v[172:173], 0, s[12:13]
	global_load_lds_dwordx4 v[138:139], off
	s_mov_b32 m0, s58
	v_lshl_add_u64 v[138:139], v[174:175], 0, s[12:13]
	global_load_lds_dwordx4 v[138:139], off
	s_mov_b32 m0, s59
	v_lshl_add_u64 v[138:139], v[176:177], 0, s[12:13]
	global_load_lds_dwordx4 v[138:139], off
	s_mov_b32 m0, s60
	v_lshl_add_u64 v[138:139], v[174:175], 0, s[14:15]
	global_load_lds_dwordx4 v[138:139], off
	s_mov_b32 m0, s61
	v_lshl_add_u64 v[138:139], v[176:177], 0, s[14:15]
	global_load_lds_dwordx4 v[138:139], off
	ds_read_b128 v[138:141], v89
	ds_read_b128 v[142:145], v89 offset:1024
	ds_read_b128 v[146:149], v89 offset:2048
	ds_read_b128 v[150:153], v89 offset:3072
	ds_read_b128 v[154:157], v89 offset:4096
	ds_read_b128 v[158:161], v89 offset:5120
	ds_read_b128 v[162:165], v89 offset:6144
	ds_read_b128 v[166:169], v89 offset:7168
	s_waitcnt vmcnt(6)
	s_waitcnt lgkmcnt(0)
	s_barrier
	s_setprio 1
	s_waitcnt lgkmcnt(0)
	v_mfma_f32_16x16x32_f16 v[62:65], v[138:141], v[106:109], v[62:65]
	v_mfma_f32_16x16x32_f16 v[58:61], v[146:149], v[106:109], v[58:61]
	v_mfma_f32_16x16x32_f16 v[54:57], v[154:157], v[106:109], v[54:57]
	v_mfma_f32_16x16x32_f16 v[50:53], v[162:165], v[106:109], v[50:53]
	v_mfma_f32_16x16x32_f16 v[46:49], v[138:141], v[114:117], v[46:49]
	v_mfma_f32_16x16x32_f16 v[42:45], v[146:149], v[114:117], v[42:45]
	v_mfma_f32_16x16x32_f16 v[38:41], v[154:157], v[114:117], v[38:41]
	v_mfma_f32_16x16x32_f16 v[34:37], v[162:165], v[114:117], v[34:37]
	v_mfma_f32_16x16x32_f16 v[30:33], v[138:141], v[122:125], v[30:33]
	v_mfma_f32_16x16x32_f16 v[26:29], v[146:149], v[122:125], v[26:29]
	v_mfma_f32_16x16x32_f16 v[22:25], v[154:157], v[122:125], v[22:25]
	v_mfma_f32_16x16x32_f16 v[18:21], v[162:165], v[122:125], v[18:21]
	v_mfma_f32_16x16x32_f16 v[14:17], v[138:141], v[130:133], v[14:17]
	v_mfma_f32_16x16x32_f16 v[10:13], v[146:149], v[130:133], v[10:13]
	v_mfma_f32_16x16x32_f16 v[6:9], v[154:157], v[130:133], v[6:9]
	v_mfma_f32_16x16x32_f16 v[2:5], v[162:165], v[130:133], v[2:5]
	v_mfma_f32_16x16x32_f16 v[62:65], v[142:145], v[110:113], v[62:65]
	v_mfma_f32_16x16x32_f16 v[58:61], v[150:153], v[110:113], v[58:61]
	v_mfma_f32_16x16x32_f16 v[54:57], v[158:161], v[110:113], v[54:57]
	v_mfma_f32_16x16x32_f16 v[50:53], v[166:169], v[110:113], v[50:53]
	v_mfma_f32_16x16x32_f16 v[46:49], v[142:145], v[118:121], v[46:49]
	v_mfma_f32_16x16x32_f16 v[42:45], v[150:153], v[118:121], v[42:45]
	v_mfma_f32_16x16x32_f16 v[38:41], v[158:161], v[118:121], v[38:41]
	v_mfma_f32_16x16x32_f16 v[34:37], v[166:169], v[118:121], v[34:37]
	v_mfma_f32_16x16x32_f16 v[30:33], v[142:145], v[126:129], v[30:33]
	v_mfma_f32_16x16x32_f16 v[26:29], v[150:153], v[126:129], v[26:29]
	v_mfma_f32_16x16x32_f16 v[22:25], v[158:161], v[126:129], v[22:25]
	v_mfma_f32_16x16x32_f16 v[18:21], v[166:169], v[126:129], v[18:21]
	v_mfma_f32_16x16x32_f16 v[14:17], v[142:145], v[134:137], v[14:17]
	v_mfma_f32_16x16x32_f16 v[10:13], v[150:153], v[134:137], v[10:13]
	v_mfma_f32_16x16x32_f16 v[6:9], v[158:161], v[134:137], v[6:9]
	v_mfma_f32_16x16x32_f16 v[2:5], v[166:169], v[134:137], v[2:5]
	s_setprio 0
	s_barrier
	v_lshl_add_u64 v[138:139], v[170:171], 0, s[16:17]
	s_mov_b32 m0, s62
	ds_read_b128 v[106:109], v95
	ds_read_b128 v[110:113], v95 offset:1024
	ds_read_b128 v[114:117], v95 offset:2048
	ds_read_b128 v[118:121], v95 offset:3072
	ds_read_b128 v[122:125], v96
	ds_read_b128 v[126:129], v97
	ds_read_b128 v[130:133], v98
	ds_read_b128 v[134:137], v99
	global_load_lds_dwordx4 v[138:139], off
	s_mov_b32 m0, s63
	v_lshl_add_u64 v[138:139], v[172:173], 0, s[16:17]
	global_load_lds_dwordx4 v[138:139], off
	s_mov_b32 m0, s64
	v_lshl_add_u64 v[138:139], v[174:175], 0, s[16:17]
	global_load_lds_dwordx4 v[138:139], off
	s_mov_b32 m0, s65
	v_lshl_add_u64 v[138:139], v[176:177], 0, s[16:17]
	global_load_lds_dwordx4 v[138:139], off
	s_mov_b32 m0, s66
	v_lshl_add_u64 v[138:139], v[174:175], 0, s[18:19]
	global_load_lds_dwordx4 v[138:139], off
	s_mov_b32 m0, s67
	v_lshl_add_u64 v[138:139], v[176:177], 0, s[18:19]
	global_load_lds_dwordx4 v[138:139], off
	ds_read_b128 v[138:141], v94
	ds_read_b128 v[142:145], v94 offset:1024
	ds_read_b128 v[146:149], v94 offset:2048
	ds_read_b128 v[150:153], v94 offset:3072
	ds_read_b128 v[154:157], v94 offset:4096
	ds_read_b128 v[158:161], v94 offset:5120
	ds_read_b128 v[162:165], v94 offset:6144
	ds_read_b128 v[166:169], v94 offset:7168
	s_waitcnt vmcnt(6)
	s_waitcnt lgkmcnt(0)
	s_barrier
	s_setprio 1
	s_waitcnt lgkmcnt(0)
	v_mfma_f32_16x16x32_f16 v[62:65], v[138:141], v[106:109], v[62:65]
	v_mfma_f32_16x16x32_f16 v[58:61], v[146:149], v[106:109], v[58:61]
	v_mfma_f32_16x16x32_f16 v[54:57], v[154:157], v[106:109], v[54:57]
	v_mfma_f32_16x16x32_f16 v[50:53], v[162:165], v[106:109], v[50:53]
	v_mfma_f32_16x16x32_f16 v[46:49], v[138:141], v[114:117], v[46:49]
	v_mfma_f32_16x16x32_f16 v[42:45], v[146:149], v[114:117], v[42:45]
	v_mfma_f32_16x16x32_f16 v[38:41], v[154:157], v[114:117], v[38:41]
	v_mfma_f32_16x16x32_f16 v[34:37], v[162:165], v[114:117], v[34:37]
	v_mfma_f32_16x16x32_f16 v[30:33], v[138:141], v[122:125], v[30:33]
	v_mfma_f32_16x16x32_f16 v[26:29], v[146:149], v[122:125], v[26:29]
	v_mfma_f32_16x16x32_f16 v[22:25], v[154:157], v[122:125], v[22:25]
	v_mfma_f32_16x16x32_f16 v[18:21], v[162:165], v[122:125], v[18:21]
	v_mfma_f32_16x16x32_f16 v[14:17], v[138:141], v[130:133], v[14:17]
	v_mfma_f32_16x16x32_f16 v[10:13], v[146:149], v[130:133], v[10:13]
	v_mfma_f32_16x16x32_f16 v[6:9], v[154:157], v[130:133], v[6:9]
	v_mfma_f32_16x16x32_f16 v[2:5], v[162:165], v[130:133], v[2:5]
	v_mfma_f32_16x16x32_f16 v[62:65], v[142:145], v[110:113], v[62:65]
	v_mfma_f32_16x16x32_f16 v[58:61], v[150:153], v[110:113], v[58:61]
	v_mfma_f32_16x16x32_f16 v[54:57], v[158:161], v[110:113], v[54:57]
	v_mfma_f32_16x16x32_f16 v[50:53], v[166:169], v[110:113], v[50:53]
	v_mfma_f32_16x16x32_f16 v[46:49], v[142:145], v[118:121], v[46:49]
	v_mfma_f32_16x16x32_f16 v[42:45], v[150:153], v[118:121], v[42:45]
	v_mfma_f32_16x16x32_f16 v[38:41], v[158:161], v[118:121], v[38:41]
	v_mfma_f32_16x16x32_f16 v[34:37], v[166:169], v[118:121], v[34:37]
	v_mfma_f32_16x16x32_f16 v[30:33], v[142:145], v[126:129], v[30:33]
	v_mfma_f32_16x16x32_f16 v[26:29], v[150:153], v[126:129], v[26:29]
	v_mfma_f32_16x16x32_f16 v[22:25], v[158:161], v[126:129], v[22:25]
	v_mfma_f32_16x16x32_f16 v[18:21], v[166:169], v[126:129], v[18:21]
	v_mfma_f32_16x16x32_f16 v[14:17], v[142:145], v[134:137], v[14:17]
	v_mfma_f32_16x16x32_f16 v[10:13], v[150:153], v[134:137], v[10:13]
	v_mfma_f32_16x16x32_f16 v[6:9], v[158:161], v[134:137], v[6:9]
	v_mfma_f32_16x16x32_f16 v[2:5], v[166:169], v[134:137], v[2:5]
	s_setprio 0
	s_barrier
	s_add_i32 s9, s9, 3
	v_lshl_add_u64 v[68:69], v[68:69], 0, s[12:13]
	v_lshl_add_u64 v[70:71], v[70:71], 0, s[12:13]
	v_lshl_add_u64 v[72:73], v[72:73], 0, s[12:13]
	s_cmp_lt_u32 s9, 27
	v_lshl_add_u64 v[74:75], v[74:75], 0, s[12:13]
	s_cbranch_scc1 .LBB2_7
	ds_read_b128 v[66:69], v90 offset:32768
	ds_read_b128 v[70:73], v90 offset:33792
	ds_read_b128 v[78:81], v90 offset:34816
	ds_read_b128 v[84:87], v90 offset:35840
	ds_read_b128 v[92:95], v90 offset:36864
	ds_read_b128 v[96:99], v90 offset:37888
	ds_read_b128 v[100:103], v90 offset:38912
	ds_read_b128 v[104:107], v90 offset:39936
	ds_read_b128 v[108:111], v83
	ds_read_b128 v[112:115], v83 offset:1024
	ds_read_b128 v[116:119], v83 offset:2048
	ds_read_b128 v[120:123], v83 offset:3072
	ds_read_b128 v[124:127], v83 offset:4096
	ds_read_b128 v[128:131], v83 offset:5120
	ds_read_b128 v[132:135], v83 offset:6144
	ds_read_b128 v[136:139], v83 offset:7168
	s_waitcnt vmcnt(0)
	s_waitcnt lgkmcnt(0)
	s_barrier
	s_setprio 1
	s_waitcnt lgkmcnt(0)
	v_mfma_f32_16x16x32_f16 v[62:65], v[66:69], v[108:111], v[62:65]
	v_mfma_f32_16x16x32_f16 v[58:61], v[78:81], v[108:111], v[58:61]
	v_mfma_f32_16x16x32_f16 v[54:57], v[92:95], v[108:111], v[54:57]
	v_mfma_f32_16x16x32_f16 v[50:53], v[100:103], v[108:111], v[50:53]
	v_mfma_f32_16x16x32_f16 v[46:49], v[66:69], v[116:119], v[46:49]
	v_mfma_f32_16x16x32_f16 v[42:45], v[78:81], v[116:119], v[42:45]
	v_mfma_f32_16x16x32_f16 v[38:41], v[92:95], v[116:119], v[38:41]
	v_mfma_f32_16x16x32_f16 v[34:37], v[100:103], v[116:119], v[34:37]
	v_mfma_f32_16x16x32_f16 v[62:65], v[70:73], v[112:115], v[62:65]
	v_mfma_f32_16x16x32_f16 v[58:61], v[84:87], v[112:115], v[58:61]
	v_mfma_f32_16x16x32_f16 v[54:57], v[96:99], v[112:115], v[54:57]
	v_mfma_f32_16x16x32_f16 v[50:53], v[104:107], v[112:115], v[50:53]
	v_mfma_f32_16x16x32_f16 v[46:49], v[70:73], v[120:123], v[46:49]
	v_mfma_f32_16x16x32_f16 v[42:45], v[84:87], v[120:123], v[42:45]
	v_mfma_f32_16x16x32_f16 v[38:41], v[96:99], v[120:123], v[38:41]
	v_mfma_f32_16x16x32_f16 v[34:37], v[104:107], v[120:123], v[34:37]
	v_mfma_f32_16x16x32_f16 v[30:33], v[66:69], v[124:127], v[30:33]
	v_mfma_f32_16x16x32_f16 v[26:29], v[78:81], v[124:127], v[26:29]
	v_mfma_f32_16x16x32_f16 v[22:25], v[92:95], v[124:127], v[22:25]
	v_mfma_f32_16x16x32_f16 v[18:21], v[100:103], v[124:127], v[18:21]
	v_mfma_f32_16x16x32_f16 v[14:17], v[66:69], v[132:135], v[14:17]
	v_mfma_f32_16x16x32_f16 v[10:13], v[78:81], v[132:135], v[10:13]
	v_mfma_f32_16x16x32_f16 v[6:9], v[92:95], v[132:135], v[6:9]
	v_mfma_f32_16x16x32_f16 v[2:5], v[100:103], v[132:135], v[2:5]
	v_mfma_f32_16x16x32_f16 v[108:111], v[70:73], v[128:131], v[30:33]
	v_mfma_f32_16x16x32_f16 v[112:115], v[84:87], v[128:131], v[26:29]
	v_mfma_f32_16x16x32_f16 v[116:119], v[96:99], v[128:131], v[22:25]
	v_mfma_f32_16x16x32_f16 v[120:123], v[104:107], v[128:131], v[18:21]
	v_mfma_f32_16x16x32_f16 v[66:69], v[70:73], v[136:139], v[14:17]
	v_mfma_f32_16x16x32_f16 v[70:73], v[84:87], v[136:139], v[10:13]
	v_mfma_f32_16x16x32_f16 v[78:81], v[96:99], v[136:139], v[6:9]
	v_mfma_f32_16x16x32_f16 v[84:87], v[104:107], v[136:139], v[2:5]
	s_setprio 0
	s_barrier
	ds_read_b128 v[90:93], v89
	ds_read_b128 v[94:97], v89 offset:1024
	ds_read_b128 v[98:101], v89 offset:2048
	ds_read_b128 v[102:105], v89 offset:3072
	ds_read_b128 v[124:127], v89 offset:4096
	ds_read_b128 v[128:131], v89 offset:5120
	ds_read_b128 v[132:135], v89 offset:6144
	ds_read_b128 v[136:139], v89 offset:7168
	ds_read_b128 v[14:17], v83 offset:49152
	ds_read_b128 v[18:21], v83 offset:50176
	ds_read_b128 v[30:33], v83 offset:51200
	ds_read_b128 v[140:143], v83 offset:52224
	ds_read_b128 v[144:147], v83 offset:53248
	ds_read_b128 v[148:151], v83 offset:54272
	ds_read_b128 v[152:155], v83 offset:55296
	ds_read_b128 v[156:159], v83 offset:56320
	s_waitcnt lgkmcnt(0)
	s_barrier
	s_setprio 1
	s_waitcnt lgkmcnt(0)
	v_mfma_f32_16x16x32_f16 v[2:5], v[90:93], v[14:17], v[62:65]
	v_mfma_f32_16x16x32_f16 v[6:9], v[98:101], v[14:17], v[58:61]
	v_mfma_f32_16x16x32_f16 v[10:13], v[124:127], v[14:17], v[54:57]
	v_mfma_f32_16x16x32_f16 v[14:17], v[132:135], v[14:17], v[50:53]
	v_mfma_f32_16x16x32_f16 v[2:5], v[94:97], v[18:21], v[2:5]
	v_mfma_f32_16x16x32_f16 v[6:9], v[102:105], v[18:21], v[6:9]
	v_mfma_f32_16x16x32_f16 v[10:13], v[128:131], v[18:21], v[10:13]
	v_mfma_f32_16x16x32_f16 v[14:17], v[136:139], v[18:21], v[14:17]
	v_mfma_f32_16x16x32_f16 v[18:21], v[90:93], v[30:33], v[46:49]
	v_mfma_f32_16x16x32_f16 v[22:25], v[98:101], v[30:33], v[42:45]
	v_mfma_f32_16x16x32_f16 v[26:29], v[124:127], v[30:33], v[38:41]
	v_mfma_f32_16x16x32_f16 v[30:33], v[132:135], v[30:33], v[34:37]
	v_mfma_f32_16x16x32_f16 v[34:37], v[90:93], v[144:147], v[108:111]
	v_mfma_f32_16x16x32_f16 v[38:41], v[98:101], v[144:147], v[112:115]
	v_mfma_f32_16x16x32_f16 v[42:45], v[124:127], v[144:147], v[116:119]
	v_mfma_f32_16x16x32_f16 v[46:49], v[132:135], v[144:147], v[120:123]
	v_mfma_f32_16x16x32_f16 v[50:53], v[90:93], v[152:155], v[66:69]
	v_mfma_f32_16x16x32_f16 v[54:57], v[98:101], v[152:155], v[70:73]
	v_mfma_f32_16x16x32_f16 v[58:61], v[124:127], v[152:155], v[78:81]
	v_mfma_f32_16x16x32_f16 v[62:65], v[132:135], v[152:155], v[84:87]
	v_mfma_f32_16x16x32_f16 v[18:21], v[94:97], v[140:143], v[18:21]
	v_mfma_f32_16x16x32_f16 v[22:25], v[102:105], v[140:143], v[22:25]
	v_mfma_f32_16x16x32_f16 v[26:29], v[128:131], v[140:143], v[26:29]
	v_mfma_f32_16x16x32_f16 v[30:33], v[136:139], v[140:143], v[30:33]
	v_mfma_f32_16x16x32_f16 v[34:37], v[94:97], v[148:151], v[34:37]
	v_mfma_f32_16x16x32_f16 v[38:41], v[102:105], v[148:151], v[38:41]
	v_mfma_f32_16x16x32_f16 v[42:45], v[128:131], v[148:151], v[42:45]
	v_mfma_f32_16x16x32_f16 v[46:49], v[136:139], v[148:151], v[46:49]
	v_mfma_f32_16x16x32_f16 v[50:53], v[94:97], v[156:159], v[50:53]
	v_mfma_f32_16x16x32_f16 v[54:57], v[102:105], v[156:159], v[54:57]
	v_mfma_f32_16x16x32_f16 v[58:61], v[128:131], v[156:159], v[58:61]
	v_mfma_f32_16x16x32_f16 v[62:65], v[136:139], v[156:159], v[62:65]
	s_setprio 0
	s_movk_i32 s4, 0x100
	v_cmp_gt_u32_e32 vcc, s4, v0
	s_barrier
	s_and_saveexec_b64 s[4:5], vcc
	s_cbranch_execz .LBB2_10
	s_barrier
